# packed f32 VALU split into scalar pairs in all GEMM-phase epilogues (928 sites)
# baseline (speedup 1.0000x reference)
.LBB0_294:
	s_cmp_lt_u32 s62, 8
	s_cbranch_scc1 .LBB0_296
	s_lshl_b32 s10, s62, 7
	v_mov_b64_e32 v[128:129], s[12:13]
	s_addk_i32 s10, 0xfc00
	v_mad_i64_i32 v[130:131], s[22:23], v164, s58, v[128:129]
	s_lshl_b64 s[22:23], s[10:11], 1
	s_nop 0
	v_lshl_add_u64 v[130:131], v[130:131], 0, s[22:23]
	s_mov_b32 s17, s11
	v_lshl_add_u64 v[130:131], v[130:131], 0, s[16:17]
	v_lshlrev_b32_e32 v144, 4, v136
	v_lshl_add_u64 v[134:135], v[130:131], 0, v[144:145]
	v_mul_f32_e64 v130, v124, v116
	v_mul_f32_e64 v131, v125, v117
	v_add_co_u32_e32 v134, vcc, s59, v134
	v_mul_f32_e64 v132, v126, v118
	v_mul_f32_e64 v133, v127, v119
	v_cvt_pk_bf16_f32 v130, v130, v131
	s_nop 0
	v_addc_co_u32_e32 v135, vcc, 0, v135, vcc
	v_mul_f32_e64 v138, v122, v114
	v_mul_f32_e64 v139, v123, v115
	v_mul_f32_e64 v140, v120, v112
	v_mul_f32_e64 v141, v121, v113
	v_cvt_pk_bf16_f32 v131, v132, v133
	s_nop 0
	v_cvt_pk_bf16_f32 v132, v140, v141
	v_cvt_pk_bf16_f32 v133, v138, v139
	global_store_dwordx4 v[134:135], v[130:133], off
	v_mul_f32_e64 v138, v106, v98
	v_mul_f32_e64 v139, v107, v99
	v_mul_f32_e64 v140, v104, v96
	v_mul_f32_e64 v141, v105, v97
	v_or_b32_e32 v130, 16, v164
	v_mad_i64_i32 v[130:131], s[24:25], v130, s58, v[128:129]
	v_lshl_add_u64 v[130:131], v[130:131], 0, s[22:23]
	v_lshl_add_u64 v[130:131], v[130:131], 0, s[16:17]
	v_lshl_add_u64 v[134:135], v[130:131], 0, v[144:145]
	v_mul_f32_e64 v130, v108, v100
	v_mul_f32_e64 v131, v109, v101
	v_add_co_u32_e32 v134, vcc, s59, v134
	v_mul_f32_e64 v132, v110, v102
	v_mul_f32_e64 v133, v111, v103
	v_cvt_pk_bf16_f32 v130, v130, v131
	s_nop 0
	v_addc_co_u32_e32 v135, vcc, 0, v135, vcc
	v_cvt_pk_bf16_f32 v131, v132, v133
	v_cvt_pk_bf16_f32 v132, v140, v141
	v_cvt_pk_bf16_f32 v133, v138, v139
	global_store_dwordx4 v[134:135], v[130:133], off
	v_mul_f32_e64 v138, v90, v82
	v_mul_f32_e64 v139, v91, v83
	v_mul_f32_e64 v140, v88, v80
	v_mul_f32_e64 v141, v89, v81
	v_or_b32_e32 v130, 32, v164
	v_mad_i64_i32 v[130:131], s[24:25], v130, s58, v[128:129]
	v_lshl_add_u64 v[130:131], v[130:131], 0, s[22:23]
	v_lshl_add_u64 v[130:131], v[130:131], 0, s[16:17]
	v_lshl_add_u64 v[134:135], v[130:131], 0, v[144:145]
	v_mul_f32_e64 v130, v92, v84
	v_mul_f32_e64 v131, v93, v85
	v_add_co_u32_e32 v134, vcc, s59, v134
	v_mul_f32_e64 v132, v94, v86
	v_mul_f32_e64 v133, v95, v87
	v_cvt_pk_bf16_f32 v130, v130, v131
	s_nop 0
	v_addc_co_u32_e32 v135, vcc, 0, v135, vcc
	v_cvt_pk_bf16_f32 v131, v132, v133
	v_cvt_pk_bf16_f32 v132, v140, v141
	v_cvt_pk_bf16_f32 v133, v138, v139
	global_store_dwordx4 v[134:135], v[130:133], off
	v_mul_f32_e64 v138, v74, v54
	v_mul_f32_e64 v139, v75, v55
	v_mul_f32_e64 v140, v72, v52
	v_mul_f32_e64 v141, v73, v53
	v_or_b32_e32 v130, 48, v164
	v_mad_i64_i32 v[130:131], s[24:25], v130, s58, v[128:129]
	v_lshl_add_u64 v[130:131], v[130:131], 0, s[22:23]
	v_lshl_add_u64 v[130:131], v[130:131], 0, s[16:17]
	v_lshl_add_u64 v[134:135], v[130:131], 0, v[144:145]
	v_mul_f32_e64 v130, v76, v68
	v_mul_f32_e64 v131, v77, v69
	v_add_co_u32_e32 v134, vcc, s59, v134
	v_mul_f32_e64 v132, v78, v70
	v_mul_f32_e64 v133, v79, v71
	v_cvt_pk_bf16_f32 v130, v130, v131
	s_nop 0
	v_addc_co_u32_e32 v135, vcc, 0, v135, vcc
	v_cvt_pk_bf16_f32 v131, v132, v133
	v_cvt_pk_bf16_f32 v132, v140, v141
	v_cvt_pk_bf16_f32 v133, v138, v139
	global_store_dwordx4 v[134:135], v[130:133], off
	v_mul_f32_e64 v138, v62, v50
	v_mul_f32_e64 v139, v63, v51
	v_mul_f32_e64 v140, v60, v48
	v_mul_f32_e64 v141, v61, v49
	v_add_u32_e32 v130, 0x80, v164
	v_mad_i64_i32 v[130:131], s[24:25], v130, s58, v[128:129]
	v_lshl_add_u64 v[130:131], v[130:131], 0, s[22:23]
	v_lshl_add_u64 v[130:131], v[130:131], 0, s[16:17]
	v_lshl_add_u64 v[134:135], v[130:131], 0, v[144:145]
	v_mul_f32_e64 v130, v64, v56
	v_mul_f32_e64 v131, v65, v57
	v_add_co_u32_e32 v134, vcc, s59, v134
	v_mul_f32_e64 v132, v66, v58
	v_mul_f32_e64 v133, v67, v59
	v_cvt_pk_bf16_f32 v130, v130, v131
	s_nop 0
	v_addc_co_u32_e32 v135, vcc, 0, v135, vcc
	v_cvt_pk_bf16_f32 v131, v132, v133
	v_cvt_pk_bf16_f32 v132, v140, v141
	v_cvt_pk_bf16_f32 v133, v138, v139
	global_store_dwordx4 v[134:135], v[130:133], off
	v_mul_f32_e64 v138, v42, v34
	v_mul_f32_e64 v139, v43, v35
	v_mul_f32_e64 v140, v40, v32
	v_mul_f32_e64 v141, v41, v33
	v_add_u32_e32 v130, 0x90, v164
	v_mad_i64_i32 v[130:131], s[24:25], v130, s58, v[128:129]
	v_lshl_add_u64 v[130:131], v[130:131], 0, s[22:23]
	v_lshl_add_u64 v[130:131], v[130:131], 0, s[16:17]
	v_lshl_add_u64 v[134:135], v[130:131], 0, v[144:145]
	v_mul_f32_e64 v130, v44, v36
	v_mul_f32_e64 v131, v45, v37
	v_add_co_u32_e32 v134, vcc, s59, v134
	v_mul_f32_e64 v132, v46, v38
	v_mul_f32_e64 v133, v47, v39
	v_cvt_pk_bf16_f32 v130, v130, v131
	s_nop 0
	v_addc_co_u32_e32 v135, vcc, 0, v135, vcc
	v_cvt_pk_bf16_f32 v131, v132, v133
	v_cvt_pk_bf16_f32 v132, v140, v141
	v_cvt_pk_bf16_f32 v133, v138, v139
	global_store_dwordx4 v[134:135], v[130:133], off
	v_mul_f32_e64 v138, v26, v18
	v_mul_f32_e64 v139, v27, v19
	v_mul_f32_e64 v140, v24, v16
	v_mul_f32_e64 v141, v25, v17
	v_add_u32_e32 v130, 0xa0, v164
	v_mad_i64_i32 v[130:131], s[24:25], v130, s58, v[128:129]
	v_lshl_add_u64 v[130:131], v[130:131], 0, s[22:23]
	v_lshl_add_u64 v[130:131], v[130:131], 0, s[16:17]
	v_lshl_add_u64 v[134:135], v[130:131], 0, v[144:145]
	v_mul_f32_e64 v130, v28, v20
	v_mul_f32_e64 v131, v29, v21
	v_add_co_u32_e32 v134, vcc, s59, v134
	v_mul_f32_e64 v132, v30, v22
	v_mul_f32_e64 v133, v31, v23
	v_cvt_pk_bf16_f32 v130, v130, v131
	s_nop 0
	v_addc_co_u32_e32 v135, vcc, 0, v135, vcc
	v_cvt_pk_bf16_f32 v131, v132, v133
	v_cvt_pk_bf16_f32 v132, v140, v141
	v_cvt_pk_bf16_f32 v133, v138, v139
	global_store_dwordx4 v[134:135], v[130:133], off
	v_mul_f32_e64 v134, v10, v2
	v_mul_f32_e64 v135, v11, v3
	v_mul_f32_e64 v138, v8, v0
	v_mul_f32_e64 v139, v9, v1
	v_add_u32_e32 v130, 0xb0, v164
	v_mad_i64_i32 v[128:129], s[24:25], v130, s58, v[128:129]
	v_lshl_add_u64 v[128:129], v[128:129], 0, s[22:23]
	v_lshl_add_u64 v[128:129], v[128:129], 0, s[16:17]
	v_lshl_add_u64 v[132:133], v[128:129], 0, v[144:145]
	v_add_co_u32_e32 v132, vcc, 0x1000, v132
	v_mul_f32_e64 v130, v14, v6
	v_mul_f32_e64 v131, v15, v7
	v_mul_f32_e64 v128, v12, v4
	v_mul_f32_e64 v129, v13, v5
	v_addc_co_u32_e32 v133, vcc, 0, v133, vcc
	s_mov_b64 s[22:23], 0
	v_cvt_pk_bf16_f32 v128, v128, v129
	v_cvt_pk_bf16_f32 v129, v130, v131
	v_cvt_pk_bf16_f32 v130, v138, v139
	v_cvt_pk_bf16_f32 v131, v134, v135
	global_store_dwordx4 v[132:133], v[128:131], off

.LBB0_299:
	s_cmp_lt_i32 s62, 2
	s_cselect_b64 vcc, -1, 0
	s_and_b64 s[22:23], vcc, exec
	s_cselect_b32 s23, s5, s7
	s_cselect_b32 s22, s4, s6
	v_lshlrev_b32_e32 v176, 5, v136
	global_load_dwordx4 v[132:135], v176, s[22:23]
	global_load_dwordx4 v[128:131], v176, s[22:23] offset:16
	v_and_b32_e32 v137, 64, v163
	v_xor_b32_e32 v172, 16, v163
	v_mul_f32_e64 v138, v126, v126
	v_mul_f32_e64 v139, v127, v127
	v_mul_f32_e64 v140, v124, v124
	v_mul_f32_e64 v141, v125, v125
	v_mul_f32_e64 v142, v122, v122
	v_mul_f32_e64 v143, v123, v123
	v_mul_f32_e64 v166, v120, v120
	v_mul_f32_e64 v167, v121, v121
	v_add_u32_e32 v182, 64, v137
	v_cndmask_b32_e32 v165, 1.0, v162, vcc
	v_lshlrev_b32_e32 v144, 4, v136
	v_pk_mov_b32 v[136:137], v[140:141], v[138:139] op_sel:[1,0]
	v_mov_b32_e32 v141, v139
	v_pk_mov_b32 v[138:139], v[166:167], v[142:143] op_sel:[1,0]
	v_mov_b32_e32 v167, v143
	v_cmp_lt_i32_e32 vcc, v172, v182
	v_add_f32_e64 v174, v138, v166
	v_add_f32_e64 v175, v139, v167
	v_mul_f32_e32 v168, v117, v117
	v_cndmask_b32_e32 v183, v163, v172, vcc
	v_add_f32_e64 v172, v136, v140
	v_add_f32_e64 v173, v137, v141
	global_load_dwordx4 v[136:139], v176, s[22:23] offset:144
	global_load_dwordx4 v[140:143], v176, s[22:23] offset:128
	v_mul_f32_e32 v170, v119, v119
	v_mul_f32_e32 v178, v112, v112
	v_mul_f32_e32 v179, v113, v113
	v_mul_f32_e32 v180, v114, v114
	v_mul_f32_e32 v181, v115, v115
	v_fma_f32 v169, v117, v117, v168
	v_fma_f32 v168, v116, v116, v168
	v_fma_f32 v171, v119, v119, v170
	v_fma_f32 v170, v118, v118, v170
	v_pk_add_f32 v[172:173], v[172:173], v[172:173] op_sel:[0,1] op_sel_hi:[1,0]
	v_pk_add_f32 v[174:175], v[174:175], v[174:175] op_sel:[0,1] op_sel_hi:[1,0]
	v_mov_b32_e32 v169, v180
	v_mov_b32_e32 v171, v181
	v_mov_b32_e32 v173, v178
	v_mov_b32_e32 v175, v179
	v_add_f32_e64 v168, v168, v170
	v_add_f32_e64 v169, v169, v171
	v_add_f32_e64 v170, v172, v174
	v_add_f32_e64 v171, v173, v175
	v_lshlrev_b32_e32 v166, 2, v183
	v_add_f32_e64 v168, v170, v168
	v_add_f32_e64 v169, v171, v169
	v_xor_b32_e32 v177, 32, v163
	v_add_f32_e32 v170, v168, v169
	ds_bpermute_b32 v171, v166, v170
	v_cmp_lt_i32_e32 vcc, v177, v182
	v_mov_b64_e32 v[150:151], s[12:13]
	v_mad_i64_i32 v[168:169], s[22:23], v164, s58, v[150:151]
	v_cndmask_b32_e32 v167, v163, v177, vcc
	v_lshlrev_b32_e32 v167, 2, v167
	s_waitcnt lgkmcnt(0)
	v_add_f32_e32 v170, v170, v171
	ds_bpermute_b32 v171, v167, v170
	s_lshl_b32 s22, s62, 8
	s_ashr_i32 s23, s22, 31
	s_lshl_b64 s[22:23], s[22:23], 1
	s_lshl_b32 s10, s54, 1
	s_waitcnt lgkmcnt(0)
	v_add_f32_e32 v170, v170, v171
	v_fmamk_f32 v170, v170, 0x3c800000, v161
	v_mul_f32_e32 v171, 0x4b800000, v170
	v_cmp_gt_f32_e32 vcc, s60, v170
	v_lshl_add_u64 v[168:169], v[168:169], 0, s[22:23]
	v_lshl_add_u64 v[168:169], v[168:169], 0, s[10:11]
	v_cndmask_b32_e32 v170, v170, v171, vcc
	v_rsq_f32_e32 v170, v170
	v_lshl_add_u64 v[168:169], v[168:169], 0, v[144:145]
	v_mul_f32_e32 v171, 0x45800000, v170
	v_cndmask_b32_e32 v170, v170, v171, vcc
	v_mul_f32_e32 v170, v165, v170
	v_mul_f32_e64 v124, v124, v170
	v_mul_f32_e64 v125, v125, v170
	v_mul_f32_e64 v126, v126, v170
	v_mul_f32_e64 v127, v127, v170
	v_mul_f32_e64 v120, v120, v170
	v_mul_f32_e64 v121, v121, v170
	v_mul_f32_e64 v122, v122, v170
	v_mul_f32_e64 v123, v123, v170
	v_mul_f32_e64 v172, v116, v170
	v_mul_f32_e64 v173, v117, v170
	v_mul_f32_e64 v174, v118, v170
	v_mul_f32_e64 v175, v119, v170
	v_mul_f32_e64 v112, v112, v170
	v_mul_f32_e64 v113, v113, v170
	v_mul_f32_e64 v114, v114, v170
	v_mul_f32_e64 v115, v115, v170
	s_waitcnt vmcnt(0)
	v_mul_f32_e64 v118, v134, v126
	v_mul_f32_e64 v119, v135, v127
	v_mul_f32_e64 v116, v132, v124
	v_mul_f32_e64 v117, v133, v125
	v_mul_f32_e64 v122, v130, v122
	v_mul_f32_e64 v123, v131, v123
	v_mul_f32_e64 v120, v128, v120
	v_mul_f32_e64 v121, v129, v121
	v_cvt_pk_bf16_f32 v116, v116, v117
	v_cvt_pk_bf16_f32 v117, v118, v119
	s_nop 0
	v_cvt_pk_bf16_f32 v118, v120, v121
	v_cvt_pk_bf16_f32 v119, v122, v123
	global_store_dwordx4 v[168:169], v[116:119], off
	s_nop 1
	v_mul_f32_e64 v116, v110, v110
	v_mul_f32_e64 v117, v111, v111
	v_mul_f32_e64 v118, v108, v108
	v_mul_f32_e64 v119, v109, v109
	s_nop 0
	v_pk_mov_b32 v[120:121], v[118:119], v[116:117] op_sel:[1,0]
	v_mov_b32_e32 v119, v117
	v_add_f32_e64 v116, v120, v118
	v_add_f32_e64 v117, v121, v119
	v_mul_f32_e64 v118, v106, v106
	v_mul_f32_e64 v119, v107, v107
	v_mul_f32_e64 v120, v104, v104
	v_mul_f32_e64 v121, v105, v105
	v_pk_add_f32 v[116:117], v[116:117], v[116:117] op_sel:[0,1] op_sel_hi:[1,0]
	v_pk_mov_b32 v[122:123], v[120:121], v[118:119] op_sel:[1,0]
	v_mov_b32_e32 v121, v119
	v_add_f32_e64 v118, v122, v120
	v_add_f32_e64 v119, v123, v121
	v_mul_f32_e32 v120, v96, v96
	v_mul_f32_e32 v121, v97, v97
	v_pk_add_f32 v[118:119], v[118:119], v[118:119] op_sel:[0,1] op_sel_hi:[1,0]
	v_mov_b32_e32 v117, v120
	v_mov_b32_e32 v119, v121
	v_add_f32_e64 v116, v116, v118
	v_add_f32_e64 v117, v117, v119
	v_mul_f32_e32 v118, v101, v101
	v_mul_f32_e32 v120, v103, v103
	v_mul_f32_e32 v122, v98, v98
	v_mul_f32_e32 v123, v99, v99
	v_fma_f32 v119, v101, v101, v118
	v_fma_f32 v118, v100, v100, v118
	v_fma_f32 v121, v103, v103, v120
	v_fma_f32 v120, v102, v102, v120
	v_mov_b32_e32 v119, v122
	v_mov_b32_e32 v121, v123
	v_add_f32_e64 v118, v118, v120
	v_add_f32_e64 v119, v119, v121
	s_nop 0
	v_add_f32_e64 v116, v116, v118
	v_add_f32_e64 v117, v117, v119
	v_mul_f32_e64 v118, v140, v172
	v_mul_f32_e64 v119, v141, v173
	v_add_f32_e32 v120, v116, v117
	ds_bpermute_b32 v121, v166, v120
	v_mul_f32_e64 v116, v142, v174
	v_mul_f32_e64 v117, v143, v175
	s_waitcnt lgkmcnt(0)
	v_add_f32_e32 v122, v120, v121
	ds_bpermute_b32 v123, v167, v122
	v_mul_f32_e64 v120, v138, v114
	v_mul_f32_e64 v121, v139, v115
	v_mul_f32_e64 v114, v136, v112
	v_mul_f32_e64 v115, v137, v113
	v_cvt_pk_bf16_f32 v112, v118, v119
	v_cvt_pk_bf16_f32 v113, v116, v117
	s_waitcnt lgkmcnt(0)
	v_add_f32_e32 v116, v122, v123
	v_fmamk_f32 v116, v116, 0x3c800000, v161
	v_mul_f32_e32 v117, 0x4b800000, v116
	v_cmp_gt_f32_e32 vcc, s60, v116
	v_cvt_pk_bf16_f32 v114, v114, v115
	v_cvt_pk_bf16_f32 v115, v120, v121
	global_store_dwordx4 v[168:169], v[112:115], off offset:64
	s_nop 0
	v_cndmask_b32_e32 v116, v116, v117, vcc
	v_rsq_f32_e32 v116, v116
	v_or_b32_e32 v113, 16, v164
	v_mad_i64_i32 v[114:115], s[24:25], v113, s58, v[150:151]
	v_mul_f32_e32 v112, 0x45800000, v116
	v_cndmask_b32_e32 v112, v116, v112, vcc
	v_mul_f32_e32 v112, v165, v112
	v_lshl_add_u64 v[114:115], v[114:115], 0, s[22:23]
	v_mul_f32_e64 v104, v104, v112
	v_mul_f32_e64 v105, v105, v112
	v_mul_f32_e64 v106, v106, v112
	v_mul_f32_e64 v107, v107, v112
	v_lshl_add_u64 v[114:115], v[114:115], 0, s[10:11]
	v_mul_f32_e64 v108, v108, v112
	v_mul_f32_e64 v109, v109, v112
	v_mul_f32_e64 v110, v110, v112
	v_mul_f32_e64 v111, v111, v112
	v_mul_f32_e64 v116, v130, v106
	v_mul_f32_e64 v117, v131, v107
	v_mul_f32_e64 v106, v128, v104
	v_mul_f32_e64 v107, v129, v105
	v_lshl_add_u64 v[114:115], v[114:115], 0, v[144:145]
	v_mul_f32_e64 v110, v134, v110
	v_mul_f32_e64 v111, v135, v111
	v_mul_f32_e64 v108, v132, v108
	v_mul_f32_e64 v109, v133, v109
	v_mul_f32_e64 v100, v100, v112
	v_mul_f32_e64 v101, v101, v112
	v_cvt_pk_bf16_f32 v104, v108, v109
	v_cvt_pk_bf16_f32 v105, v110, v111
	v_cvt_pk_bf16_f32 v106, v106, v107
	v_cvt_pk_bf16_f32 v107, v116, v117
	global_store_dwordx4 v[114:115], v[104:107], off
	v_mul_f32_e64 v100, v140, v100
	v_mul_f32_e64 v101, v141, v101
	v_mul_f32_e64 v96, v96, v112
	v_mul_f32_e64 v97, v97, v112
	v_mul_f32_e64 v104, v94, v94
	v_mul_f32_e64 v105, v95, v95
	v_mul_f32_e64 v106, v92, v92
	v_mul_f32_e64 v107, v93, v93
	v_mul_f32_e64 v98, v98, v112
	v_mul_f32_e64 v99, v99, v112
	v_pk_mov_b32 v[108:109], v[106:107], v[104:105] op_sel:[1,0]
	v_mov_b32_e32 v107, v105
	v_add_f32_e64 v104, v108, v106
	v_add_f32_e64 v105, v109, v107
	v_mul_f32_e64 v106, v90, v90
	v_mul_f32_e64 v107, v91, v91
	v_mul_f32_e64 v108, v88, v88
	v_mul_f32_e64 v109, v89, v89
	v_pk_add_f32 v[104:105], v[104:105], v[104:105] op_sel:[0,1] op_sel_hi:[1,0]
	v_pk_mov_b32 v[110:111], v[108:109], v[106:107] op_sel:[1,0]
	v_mov_b32_e32 v109, v107
	v_add_f32_e64 v106, v110, v108
	v_add_f32_e64 v107, v111, v109
	v_mul_f32_e32 v108, v80, v80
	v_mul_f32_e32 v109, v81, v81
	v_pk_add_f32 v[106:107], v[106:107], v[106:107] op_sel:[0,1] op_sel_hi:[1,0]
	v_mov_b32_e32 v105, v108
	v_mov_b32_e32 v107, v109
	v_add_f32_e64 v104, v104, v106
	v_add_f32_e64 v105, v105, v107
	v_mul_f32_e32 v106, v85, v85
	v_mul_f32_e32 v108, v87, v87
	v_mul_f32_e32 v110, v82, v82
	v_mul_f32_e32 v111, v83, v83
	v_fma_f32 v107, v85, v85, v106
	v_fma_f32 v106, v84, v84, v106
	v_fma_f32 v109, v87, v87, v108
	v_fma_f32 v108, v86, v86, v108
	v_mov_b32_e32 v107, v110
	v_mov_b32_e32 v109, v111
	v_add_f32_e64 v106, v106, v108
	v_add_f32_e64 v107, v107, v109
	v_mul_f32_e64 v102, v102, v112
	v_mul_f32_e64 v103, v103, v112
	v_add_f32_e64 v104, v104, v106
	v_add_f32_e64 v105, v105, v107
	v_mul_f32_e64 v102, v142, v102
	v_mul_f32_e64 v103, v143, v103
	v_add_f32_e32 v104, v104, v105
	ds_bpermute_b32 v105, v166, v104
	s_waitcnt lgkmcnt(0)
	v_add_f32_e32 v106, v104, v105
	ds_bpermute_b32 v107, v167, v106
	v_mul_f32_e64 v104, v138, v98
	v_mul_f32_e64 v105, v139, v99
	v_mul_f32_e64 v98, v136, v96
	v_mul_f32_e64 v99, v137, v97
	v_cvt_pk_bf16_f32 v96, v100, v101
	v_cvt_pk_bf16_f32 v97, v102, v103
	s_waitcnt lgkmcnt(0)
	v_add_f32_e32 v100, v106, v107
	v_fmamk_f32 v100, v100, 0x3c800000, v161
	v_mul_f32_e32 v101, 0x4b800000, v100
	v_cmp_gt_f32_e32 vcc, s60, v100
	v_cvt_pk_bf16_f32 v98, v98, v99
	v_cvt_pk_bf16_f32 v99, v104, v105
	global_store_dwordx4 v[114:115], v[96:99], off offset:64
	s_nop 0
	v_cndmask_b32_e32 v100, v100, v101, vcc
	v_rsq_f32_e32 v100, v100
	v_or_b32_e32 v97, 32, v164
	v_mad_i64_i32 v[98:99], s[24:25], v97, s58, v[150:151]
	v_mul_f32_e32 v96, 0x45800000, v100
	v_cndmask_b32_e32 v96, v100, v96, vcc
	v_mul_f32_e32 v96, v165, v96
	v_lshl_add_u64 v[98:99], v[98:99], 0, s[22:23]
	v_mul_f32_e64 v88, v88, v96
	v_mul_f32_e64 v89, v89, v96
	v_mul_f32_e64 v90, v90, v96
	v_mul_f32_e64 v91, v91, v96
	v_lshl_add_u64 v[98:99], v[98:99], 0, s[10:11]
	v_mul_f32_e64 v92, v92, v96
	v_mul_f32_e64 v93, v93, v96
	v_mul_f32_e64 v94, v94, v96
	v_mul_f32_e64 v95, v95, v96
	v_mul_f32_e64 v100, v130, v90
	v_mul_f32_e64 v101, v131, v91
	v_mul_f32_e64 v90, v128, v88
	v_mul_f32_e64 v91, v129, v89
	v_lshl_add_u64 v[98:99], v[98:99], 0, v[144:145]
	v_mul_f32_e64 v94, v134, v94
	v_mul_f32_e64 v95, v135, v95
	v_mul_f32_e64 v92, v132, v92
	v_mul_f32_e64 v93, v133, v93
	v_mul_f32_e64 v84, v84, v96
	v_mul_f32_e64 v85, v85, v96
	v_cvt_pk_bf16_f32 v88, v92, v93
	v_cvt_pk_bf16_f32 v89, v94, v95
	v_cvt_pk_bf16_f32 v90, v90, v91
	v_cvt_pk_bf16_f32 v91, v100, v101
	global_store_dwordx4 v[98:99], v[88:91], off
	v_mul_f32_e64 v84, v140, v84
	v_mul_f32_e64 v85, v141, v85
	v_mul_f32_e64 v80, v80, v96
	v_mul_f32_e64 v81, v81, v96
	v_mul_f32_e64 v88, v78, v78
	v_mul_f32_e64 v89, v79, v79
	v_mul_f32_e64 v90, v76, v76
	v_mul_f32_e64 v91, v77, v77
	v_mul_f32_e64 v82, v82, v96
	v_mul_f32_e64 v83, v83, v96
	v_pk_mov_b32 v[92:93], v[90:91], v[88:89] op_sel:[1,0]
	v_mov_b32_e32 v91, v89
	v_add_f32_e64 v88, v92, v90
	v_add_f32_e64 v89, v93, v91
	v_mul_f32_e64 v90, v74, v74
	v_mul_f32_e64 v91, v75, v75
	v_mul_f32_e64 v92, v72, v72
	v_mul_f32_e64 v93, v73, v73
	v_pk_add_f32 v[88:89], v[88:89], v[88:89] op_sel:[0,1] op_sel_hi:[1,0]
	v_pk_mov_b32 v[94:95], v[92:93], v[90:91] op_sel:[1,0]
	v_mov_b32_e32 v93, v91
	v_add_f32_e64 v90, v94, v92
	v_add_f32_e64 v91, v95, v93
	v_mul_f32_e32 v92, v52, v52
	v_mul_f32_e32 v93, v53, v53
	v_pk_add_f32 v[90:91], v[90:91], v[90:91] op_sel:[0,1] op_sel_hi:[1,0]
	v_mov_b32_e32 v89, v92
	v_mov_b32_e32 v91, v93
	v_add_f32_e64 v88, v88, v90
	v_add_f32_e64 v89, v89, v91
	v_mul_f32_e32 v90, v69, v69
	v_mul_f32_e32 v92, v71, v71
	v_mul_f32_e32 v94, v54, v54
	v_mul_f32_e32 v95, v55, v55
	v_fma_f32 v91, v69, v69, v90
	v_fma_f32 v90, v68, v68, v90
	v_fma_f32 v93, v71, v71, v92
	v_fma_f32 v92, v70, v70, v92
	v_mov_b32_e32 v91, v94
	v_mov_b32_e32 v93, v95
	v_add_f32_e64 v90, v90, v92
	v_add_f32_e64 v91, v91, v93
	v_mul_f32_e64 v86, v86, v96
	v_mul_f32_e64 v87, v87, v96
	v_add_f32_e64 v88, v88, v90
	v_add_f32_e64 v89, v89, v91
	v_mul_f32_e64 v86, v142, v86
	v_mul_f32_e64 v87, v143, v87
	v_add_f32_e32 v88, v88, v89
	ds_bpermute_b32 v89, v166, v88
	s_waitcnt lgkmcnt(0)
	v_add_f32_e32 v90, v88, v89
	ds_bpermute_b32 v91, v167, v90
	v_mul_f32_e64 v88, v138, v82
	v_mul_f32_e64 v89, v139, v83
	v_mul_f32_e64 v82, v136, v80
	v_mul_f32_e64 v83, v137, v81
	v_cvt_pk_bf16_f32 v80, v84, v85
	v_cvt_pk_bf16_f32 v81, v86, v87
	s_waitcnt lgkmcnt(0)
	v_add_f32_e32 v84, v90, v91
	v_fmamk_f32 v84, v84, 0x3c800000, v161
	v_mul_f32_e32 v85, 0x4b800000, v84
	v_cmp_gt_f32_e32 vcc, s60, v84
	v_cvt_pk_bf16_f32 v82, v82, v83
	v_cvt_pk_bf16_f32 v83, v88, v89
	global_store_dwordx4 v[98:99], v[80:83], off offset:64
	s_nop 0
	v_cndmask_b32_e32 v84, v84, v85, vcc
	v_rsq_f32_e32 v84, v84
	v_or_b32_e32 v81, 48, v164
	v_mad_i64_i32 v[82:83], s[24:25], v81, s58, v[150:151]
	v_mul_f32_e32 v80, 0x45800000, v84
	v_cndmask_b32_e32 v80, v84, v80, vcc
	v_mul_f32_e32 v80, v165, v80
	v_lshl_add_u64 v[82:83], v[82:83], 0, s[22:23]
	v_mul_f32_e64 v72, v72, v80
	v_mul_f32_e64 v73, v73, v80
	v_mul_f32_e64 v74, v74, v80
	v_mul_f32_e64 v75, v75, v80
	v_lshl_add_u64 v[82:83], v[82:83], 0, s[10:11]
	v_mul_f32_e64 v76, v76, v80
	v_mul_f32_e64 v77, v77, v80
	v_mul_f32_e64 v78, v78, v80
	v_mul_f32_e64 v79, v79, v80
	v_mul_f32_e64 v84, v130, v74
	v_mul_f32_e64 v85, v131, v75
	v_mul_f32_e64 v74, v128, v72
	v_mul_f32_e64 v75, v129, v73
	v_lshl_add_u64 v[82:83], v[82:83], 0, v[144:145]
	v_mul_f32_e64 v78, v134, v78
	v_mul_f32_e64 v79, v135, v79
	v_mul_f32_e64 v76, v132, v76
	v_mul_f32_e64 v77, v133, v77
	v_mul_f32_e64 v52, v52, v80
	v_mul_f32_e64 v53, v53, v80
	v_cvt_pk_bf16_f32 v72, v76, v77
	v_cvt_pk_bf16_f32 v73, v78, v79
	v_cvt_pk_bf16_f32 v74, v74, v75
	v_cvt_pk_bf16_f32 v75, v84, v85
	global_store_dwordx4 v[82:83], v[72:75], off
	v_mul_f32_e64 v54, v54, v80
	v_mul_f32_e64 v55, v55, v80
	v_mul_f32_e64 v68, v68, v80
	v_mul_f32_e64 v69, v69, v80
	v_mul_f32_e64 v72, v66, v66
	v_mul_f32_e64 v73, v67, v67
	v_mul_f32_e64 v74, v64, v64
	v_mul_f32_e64 v75, v65, v65
	v_mul_f32_e64 v70, v70, v80
	v_mul_f32_e64 v71, v71, v80
	v_pk_mov_b32 v[76:77], v[74:75], v[72:73] op_sel:[1,0]
	v_mov_b32_e32 v75, v73
	v_add_f32_e64 v72, v76, v74
	v_add_f32_e64 v73, v77, v75
	v_mul_f32_e64 v74, v62, v62
	v_mul_f32_e64 v75, v63, v63
	v_mul_f32_e64 v76, v60, v60
	v_mul_f32_e64 v77, v61, v61
	v_pk_add_f32 v[72:73], v[72:73], v[72:73] op_sel:[0,1] op_sel_hi:[1,0]
	v_pk_mov_b32 v[78:79], v[76:77], v[74:75] op_sel:[1,0]
	v_mov_b32_e32 v77, v75
	v_add_f32_e64 v74, v78, v76
	v_add_f32_e64 v75, v79, v77
	v_mul_f32_e32 v76, v48, v48
	v_mul_f32_e32 v77, v49, v49
	v_pk_add_f32 v[74:75], v[74:75], v[74:75] op_sel:[0,1] op_sel_hi:[1,0]
	v_mov_b32_e32 v73, v76
	v_mov_b32_e32 v75, v77
	v_add_f32_e64 v72, v72, v74
	v_add_f32_e64 v73, v73, v75
	v_mul_f32_e32 v74, v57, v57
	v_mul_f32_e32 v76, v59, v59
	v_mul_f32_e32 v78, v50, v50
	v_mul_f32_e32 v79, v51, v51
	v_fma_f32 v75, v57, v57, v74
	v_fma_f32 v74, v56, v56, v74
	v_fma_f32 v77, v59, v59, v76
	v_fma_f32 v76, v58, v58, v76
	v_mov_b32_e32 v75, v78
	v_mov_b32_e32 v77, v79
	v_add_f32_e64 v74, v74, v76
	v_add_f32_e64 v75, v75, v77
	v_mul_f32_e64 v70, v142, v70
	v_mul_f32_e64 v71, v143, v71
	v_add_f32_e64 v72, v72, v74
	v_add_f32_e64 v73, v73, v75
	v_mul_f32_e64 v68, v140, v68
	v_mul_f32_e64 v69, v141, v69
	v_add_f32_e32 v74, v72, v73
	ds_bpermute_b32 v75, v166, v74
	v_mul_f32_e64 v72, v138, v54
	v_mul_f32_e64 v73, v139, v55
	v_mul_f32_e64 v54, v136, v52
	v_mul_f32_e64 v55, v137, v53
	v_cvt_pk_bf16_f32 v52, v68, v69
	v_cvt_pk_bf16_f32 v53, v70, v71
	s_waitcnt lgkmcnt(0)
	v_add_f32_e32 v74, v74, v75
	ds_bpermute_b32 v75, v167, v74
	v_cvt_pk_bf16_f32 v54, v54, v55
	s_waitcnt lgkmcnt(0)
	v_add_f32_e32 v55, v74, v75
	v_fmamk_f32 v55, v55, 0x3c800000, v161
	v_mul_f32_e32 v68, 0x4b800000, v55
	v_cmp_gt_f32_e32 vcc, s60, v55
	s_nop 1
	v_cndmask_b32_e32 v55, v55, v68, vcc
	v_rsq_f32_e32 v68, v55
	v_cvt_pk_bf16_f32 v55, v72, v73
	global_store_dwordx4 v[82:83], v[52:55], off offset:64
	s_nop 1
	v_mul_f32_e32 v53, 0x45800000, v68
	v_add_u32_e32 v52, 0x80, v164
	v_cndmask_b32_e32 v53, v68, v53, vcc
	v_mul_f32_e32 v68, v165, v53
	v_mad_i64_i32 v[52:53], s[24:25], v52, s58, v[150:151]
	v_lshl_add_u64 v[52:53], v[52:53], 0, s[22:23]
	v_lshl_add_u64 v[52:53], v[52:53], 0, s[10:11]
	v_lshl_add_u64 v[70:71], v[52:53], 0, v[144:145]
	v_mul_f32_e64 v52, v64, v68
	v_mul_f32_e64 v53, v65, v68
	v_mul_f32_e64 v54, v66, v68
	v_mul_f32_e64 v55, v67, v68
	v_mul_f32_e64 v52, v132, v52
	v_mul_f32_e64 v53, v133, v53
	v_mul_f32_e64 v54, v134, v54
	v_mul_f32_e64 v55, v135, v55
	v_mul_f32_e64 v60, v60, v68
	v_mul_f32_e64 v61, v61, v68
	v_mul_f32_e64 v62, v62, v68
	v_mul_f32_e64 v63, v63, v68
	v_mul_f32_e64 v60, v128, v60
	v_mul_f32_e64 v61, v129, v61
	v_mul_f32_e64 v62, v130, v62
	v_mul_f32_e64 v63, v131, v63
	v_cvt_pk_bf16_f32 v52, v52, v53
	v_cvt_pk_bf16_f32 v53, v54, v55
	v_cvt_pk_bf16_f32 v54, v60, v61
	v_mul_f32_e64 v48, v48, v68
	v_mul_f32_e64 v49, v49, v68
	v_cvt_pk_bf16_f32 v55, v62, v63
	global_store_dwordx4 v[70:71], v[52:55], off
	v_mul_f32_e64 v50, v50, v68
	v_mul_f32_e64 v51, v51, v68
	s_nop 0
	v_mul_f32_e64 v52, v56, v68
	v_mul_f32_e64 v53, v57, v68
	v_mul_f32_e64 v54, v58, v68
	v_mul_f32_e64 v55, v59, v68
	v_mul_f32_e64 v56, v46, v46
	v_mul_f32_e64 v57, v47, v47
	v_mul_f32_e64 v58, v44, v44
	v_mul_f32_e64 v59, v45, v45
	v_mul_f32_e64 v52, v140, v52
	v_mul_f32_e64 v53, v141, v53
	v_pk_mov_b32 v[60:61], v[58:59], v[56:57] op_sel:[1,0]
	v_mov_b32_e32 v59, v57
	v_add_f32_e64 v56, v60, v58
	v_add_f32_e64 v57, v61, v59
	v_mul_f32_e64 v58, v42, v42
	v_mul_f32_e64 v59, v43, v43
	v_mul_f32_e64 v60, v40, v40
	v_mul_f32_e64 v61, v41, v41
	v_pk_add_f32 v[56:57], v[56:57], v[56:57] op_sel:[0,1] op_sel_hi:[1,0]
	v_pk_mov_b32 v[62:63], v[60:61], v[58:59] op_sel:[1,0]
	v_mov_b32_e32 v61, v59
	v_add_f32_e64 v58, v62, v60
	v_add_f32_e64 v59, v63, v61
	v_mul_f32_e32 v60, v32, v32
	v_mul_f32_e32 v61, v33, v33
	v_pk_add_f32 v[58:59], v[58:59], v[58:59] op_sel:[0,1] op_sel_hi:[1,0]
	v_mov_b32_e32 v57, v60
	v_mov_b32_e32 v59, v61
	v_add_f32_e64 v56, v56, v58
	v_add_f32_e64 v57, v57, v59
	v_mul_f32_e32 v58, v37, v37
	v_mul_f32_e32 v60, v39, v39
	v_mul_f32_e32 v62, v34, v34
	v_mul_f32_e32 v63, v35, v35
	v_fma_f32 v59, v37, v37, v58
	v_fma_f32 v58, v36, v36, v58
	v_fma_f32 v61, v39, v39, v60
	v_fma_f32 v60, v38, v38, v60
	v_mov_b32_e32 v59, v62
	v_mov_b32_e32 v61, v63
	v_add_f32_e64 v58, v58, v60
	v_add_f32_e64 v59, v59, v61
	v_mul_f32_e64 v54, v142, v54
	v_mul_f32_e64 v55, v143, v55
	v_add_f32_e64 v56, v56, v58
	v_add_f32_e64 v57, v57, v59
	s_nop 0
	v_add_f32_e32 v56, v56, v57
	ds_bpermute_b32 v57, v166, v56
	s_waitcnt lgkmcnt(0)
	v_add_f32_e32 v58, v56, v57
	ds_bpermute_b32 v59, v167, v58
	v_mul_f32_e64 v56, v138, v50
	v_mul_f32_e64 v57, v139, v51
	v_mul_f32_e64 v50, v136, v48
	v_mul_f32_e64 v51, v137, v49
	v_cvt_pk_bf16_f32 v48, v52, v53
	v_cvt_pk_bf16_f32 v49, v54, v55
	s_waitcnt lgkmcnt(0)
	v_add_f32_e32 v52, v58, v59
	v_fmamk_f32 v52, v52, 0x3c800000, v161
	v_mul_f32_e32 v53, 0x4b800000, v52
	v_cmp_gt_f32_e32 vcc, s60, v52
	v_cvt_pk_bf16_f32 v50, v50, v51
	v_cvt_pk_bf16_f32 v51, v56, v57
	global_store_dwordx4 v[70:71], v[48:51], off offset:64
	s_nop 0
	v_cndmask_b32_e32 v52, v52, v53, vcc
	v_rsq_f32_e32 v52, v52
	v_add_u32_e32 v49, 0x90, v164
	v_mad_i64_i32 v[50:51], s[24:25], v49, s58, v[150:151]
	v_mul_f32_e32 v48, 0x45800000, v52
	v_cndmask_b32_e32 v48, v52, v48, vcc
	v_mul_f32_e32 v48, v165, v48
	v_lshl_add_u64 v[50:51], v[50:51], 0, s[22:23]
	v_mul_f32_e64 v40, v40, v48
	v_mul_f32_e64 v41, v41, v48
	v_mul_f32_e64 v42, v42, v48
	v_mul_f32_e64 v43, v43, v48
	v_lshl_add_u64 v[50:51], v[50:51], 0, s[10:11]
	v_mul_f32_e64 v44, v44, v48
	v_mul_f32_e64 v45, v45, v48
	v_mul_f32_e64 v46, v46, v48
	v_mul_f32_e64 v47, v47, v48
	v_mul_f32_e64 v52, v130, v42
	v_mul_f32_e64 v53, v131, v43
	v_mul_f32_e64 v42, v128, v40
	v_mul_f32_e64 v43, v129, v41
	v_lshl_add_u64 v[50:51], v[50:51], 0, v[144:145]
	v_mul_f32_e64 v46, v134, v46
	v_mul_f32_e64 v47, v135, v47
	v_mul_f32_e64 v44, v132, v44
	v_mul_f32_e64 v45, v133, v45
	v_mul_f32_e64 v36, v36, v48
	v_mul_f32_e64 v37, v37, v48
	v_cvt_pk_bf16_f32 v40, v44, v45
	v_cvt_pk_bf16_f32 v41, v46, v47
	v_cvt_pk_bf16_f32 v42, v42, v43
	v_cvt_pk_bf16_f32 v43, v52, v53
	global_store_dwordx4 v[50:51], v[40:43], off
	v_mul_f32_e64 v36, v140, v36
	v_mul_f32_e64 v37, v141, v37
	v_mul_f32_e64 v32, v32, v48
	v_mul_f32_e64 v33, v33, v48
	v_mul_f32_e64 v40, v30, v30
	v_mul_f32_e64 v41, v31, v31
	v_mul_f32_e64 v42, v28, v28
	v_mul_f32_e64 v43, v29, v29
	v_mul_f32_e64 v34, v34, v48
	v_mul_f32_e64 v35, v35, v48
	v_pk_mov_b32 v[44:45], v[42:43], v[40:41] op_sel:[1,0]
	v_mov_b32_e32 v43, v41
	v_add_f32_e64 v40, v44, v42
	v_add_f32_e64 v41, v45, v43
	v_mul_f32_e64 v42, v26, v26
	v_mul_f32_e64 v43, v27, v27
	v_mul_f32_e64 v44, v24, v24
	v_mul_f32_e64 v45, v25, v25
	v_pk_add_f32 v[40:41], v[40:41], v[40:41] op_sel:[0,1] op_sel_hi:[1,0]
	v_pk_mov_b32 v[46:47], v[44:45], v[42:43] op_sel:[1,0]
	v_mov_b32_e32 v45, v43
	v_add_f32_e64 v42, v46, v44
	v_add_f32_e64 v43, v47, v45
	v_mul_f32_e32 v44, v16, v16
	v_mul_f32_e32 v45, v17, v17
	v_pk_add_f32 v[42:43], v[42:43], v[42:43] op_sel:[0,1] op_sel_hi:[1,0]
	v_mov_b32_e32 v41, v44
	v_mov_b32_e32 v43, v45
	v_add_f32_e64 v40, v40, v42
	v_add_f32_e64 v41, v41, v43
	v_mul_f32_e32 v42, v21, v21
	v_mul_f32_e32 v44, v23, v23
	v_mul_f32_e32 v46, v18, v18
	v_mul_f32_e32 v47, v19, v19
	v_fma_f32 v43, v21, v21, v42
	v_fma_f32 v42, v20, v20, v42
	v_fma_f32 v45, v23, v23, v44
	v_fma_f32 v44, v22, v22, v44
	v_mov_b32_e32 v43, v46
	v_mov_b32_e32 v45, v47
	v_add_f32_e64 v42, v42, v44
	v_add_f32_e64 v43, v43, v45
	v_mul_f32_e64 v38, v38, v48
	v_mul_f32_e64 v39, v39, v48
	v_add_f32_e64 v40, v40, v42
	v_add_f32_e64 v41, v41, v43
	v_mul_f32_e64 v38, v142, v38
	v_mul_f32_e64 v39, v143, v39
	v_add_f32_e32 v40, v40, v41
	ds_bpermute_b32 v41, v166, v40
	s_waitcnt lgkmcnt(0)
	v_add_f32_e32 v42, v40, v41
	ds_bpermute_b32 v43, v167, v42
	v_mul_f32_e64 v40, v138, v34
	v_mul_f32_e64 v41, v139, v35
	v_mul_f32_e64 v34, v136, v32
	v_mul_f32_e64 v35, v137, v33
	v_cvt_pk_bf16_f32 v32, v36, v37
	v_cvt_pk_bf16_f32 v33, v38, v39
	s_waitcnt lgkmcnt(0)
	v_add_f32_e32 v36, v42, v43
	v_fmamk_f32 v36, v36, 0x3c800000, v161
	v_mul_f32_e32 v37, 0x4b800000, v36
	v_cmp_gt_f32_e32 vcc, s60, v36
	v_cvt_pk_bf16_f32 v34, v34, v35
	v_cvt_pk_bf16_f32 v35, v40, v41
	global_store_dwordx4 v[50:51], v[32:35], off offset:64
	s_nop 0
	v_cndmask_b32_e32 v36, v36, v37, vcc
	v_rsq_f32_e32 v36, v36
	v_add_u32_e32 v33, 0xa0, v164
	v_mad_i64_i32 v[34:35], s[24:25], v33, s58, v[150:151]
	v_mul_f32_e32 v32, 0x45800000, v36
	v_cndmask_b32_e32 v32, v36, v32, vcc
	v_mul_f32_e32 v32, v165, v32
	v_lshl_add_u64 v[34:35], v[34:35], 0, s[22:23]
	v_mul_f32_e64 v24, v24, v32
	v_mul_f32_e64 v25, v25, v32
	v_mul_f32_e64 v26, v26, v32
	v_mul_f32_e64 v27, v27, v32
	v_lshl_add_u64 v[34:35], v[34:35], 0, s[10:11]
	v_mul_f32_e64 v28, v28, v32
	v_mul_f32_e64 v29, v29, v32
	v_mul_f32_e64 v30, v30, v32
	v_mul_f32_e64 v31, v31, v32
	v_mul_f32_e64 v36, v130, v26
	v_mul_f32_e64 v37, v131, v27
	v_mul_f32_e64 v26, v128, v24
	v_mul_f32_e64 v27, v129, v25
	v_lshl_add_u64 v[34:35], v[34:35], 0, v[144:145]
	v_mul_f32_e64 v30, v134, v30
	v_mul_f32_e64 v31, v135, v31
	v_mul_f32_e64 v28, v132, v28
	v_mul_f32_e64 v29, v133, v29
	v_mul_f32_e64 v20, v20, v32
	v_mul_f32_e64 v21, v21, v32
	v_cvt_pk_bf16_f32 v24, v28, v29
	v_cvt_pk_bf16_f32 v25, v30, v31
	v_cvt_pk_bf16_f32 v26, v26, v27
	v_cvt_pk_bf16_f32 v27, v36, v37
	global_store_dwordx4 v[34:35], v[24:27], off
	v_mul_f32_e64 v20, v140, v20
	v_mul_f32_e64 v21, v141, v21
	v_mul_f32_e64 v16, v16, v32
	v_mul_f32_e64 v17, v17, v32
	v_mul_f32_e64 v24, v14, v14
	v_mul_f32_e64 v25, v15, v15
	v_mul_f32_e64 v26, v12, v12
	v_mul_f32_e64 v27, v13, v13
	v_mul_f32_e64 v18, v18, v32
	v_mul_f32_e64 v19, v19, v32
	v_pk_mov_b32 v[28:29], v[26:27], v[24:25] op_sel:[1,0]
	v_mov_b32_e32 v27, v25
	v_add_f32_e64 v24, v28, v26
	v_add_f32_e64 v25, v29, v27
	v_mul_f32_e64 v26, v10, v10
	v_mul_f32_e64 v27, v11, v11
	v_mul_f32_e64 v28, v8, v8
	v_mul_f32_e64 v29, v9, v9
	v_pk_add_f32 v[24:25], v[24:25], v[24:25] op_sel:[0,1] op_sel_hi:[1,0]
	v_pk_mov_b32 v[30:31], v[28:29], v[26:27] op_sel:[1,0]
	v_mov_b32_e32 v29, v27
	v_add_f32_e64 v26, v30, v28
	v_add_f32_e64 v27, v31, v29
	v_mul_f32_e32 v28, v0, v0
	v_mul_f32_e32 v29, v1, v1
	v_pk_add_f32 v[26:27], v[26:27], v[26:27] op_sel:[0,1] op_sel_hi:[1,0]
	v_mov_b32_e32 v25, v28
	v_mov_b32_e32 v27, v29
	v_add_f32_e64 v24, v24, v26
	v_add_f32_e64 v25, v25, v27
	v_mul_f32_e32 v26, v5, v5
	v_mul_f32_e32 v28, v7, v7
	v_mul_f32_e32 v30, v2, v2
	v_mul_f32_e32 v31, v3, v3
	v_fma_f32 v27, v5, v5, v26
	v_fma_f32 v26, v4, v4, v26
	v_fma_f32 v29, v7, v7, v28
	v_fma_f32 v28, v6, v6, v28
	v_mov_b32_e32 v27, v30
	v_mov_b32_e32 v29, v31
	v_add_f32_e64 v26, v26, v28
	v_add_f32_e64 v27, v27, v29
	v_mul_f32_e64 v22, v22, v32
	v_mul_f32_e64 v23, v23, v32
	v_add_f32_e64 v24, v24, v26
	v_add_f32_e64 v25, v25, v27
	v_mul_f32_e64 v22, v142, v22
	v_mul_f32_e64 v23, v143, v23
	v_add_f32_e32 v24, v24, v25
	ds_bpermute_b32 v25, v166, v24
	s_waitcnt lgkmcnt(0)
	v_add_f32_e32 v26, v24, v25
	ds_bpermute_b32 v27, v167, v26
	v_mul_f32_e64 v24, v138, v18
	v_mul_f32_e64 v25, v139, v19
	v_mul_f32_e64 v18, v136, v16
	v_mul_f32_e64 v19, v137, v17
	v_cvt_pk_bf16_f32 v16, v20, v21
	v_cvt_pk_bf16_f32 v17, v22, v23
	s_waitcnt lgkmcnt(0)
	v_add_f32_e32 v20, v26, v27
	v_fmamk_f32 v20, v20, 0x3c800000, v161
	v_mul_f32_e32 v21, 0x4b800000, v20
	v_cmp_gt_f32_e32 vcc, s60, v20
	v_cvt_pk_bf16_f32 v18, v18, v19
	v_cvt_pk_bf16_f32 v19, v24, v25
	global_store_dwordx4 v[34:35], v[16:19], off offset:64
	s_nop 0
	v_cndmask_b32_e32 v20, v20, v21, vcc
	v_rsq_f32_e32 v20, v20
	v_add_u32_e32 v17, 0xb0, v164
	v_mad_i64_i32 v[18:19], s[24:25], v17, s58, v[150:151]
	v_mul_f32_e32 v16, 0x45800000, v20
	v_cndmask_b32_e32 v16, v20, v16, vcc
	v_mul_f32_e32 v16, v165, v16
	v_lshl_add_u64 v[18:19], v[18:19], 0, s[22:23]
	v_lshl_add_u64 v[18:19], v[18:19], 0, s[10:11]
	v_mul_f32_e64 v12, v12, v16
	v_mul_f32_e64 v13, v13, v16
	v_mul_f32_e64 v14, v14, v16
	v_mul_f32_e64 v15, v15, v16
	v_mul_f32_e64 v8, v8, v16
	v_mul_f32_e64 v9, v9, v16
	v_mul_f32_e64 v10, v10, v16
	v_mul_f32_e64 v11, v11, v16
	v_lshl_add_u64 v[18:19], v[18:19], 0, v[144:145]
	v_mul_f32_e64 v14, v134, v14
	v_mul_f32_e64 v15, v135, v15
	v_mul_f32_e64 v12, v132, v12
	v_mul_f32_e64 v13, v133, v13
	v_mul_f32_e64 v20, v130, v10
	v_mul_f32_e64 v21, v131, v11
	v_mul_f32_e64 v10, v128, v8
	v_mul_f32_e64 v11, v129, v9
	v_cvt_pk_bf16_f32 v8, v12, v13
	v_cvt_pk_bf16_f32 v9, v14, v15
	v_mul_f32_e64 v0, v0, v16
	v_mul_f32_e64 v1, v1, v16
	v_mul_f32_e64 v2, v2, v16
	v_mul_f32_e64 v3, v3, v16
	v_cvt_pk_bf16_f32 v10, v10, v11
	v_cvt_pk_bf16_f32 v11, v20, v21
	global_store_dwordx4 v[18:19], v[8:11], off
	v_mul_f32_e64 v4, v4, v16
	v_mul_f32_e64 v5, v5, v16
	v_mul_f32_e64 v6, v6, v16
	v_mul_f32_e64 v7, v7, v16
	v_mul_f32_e64 v8, v138, v2
	v_mul_f32_e64 v9, v139, v3
	v_mul_f32_e64 v2, v136, v0
	v_mul_f32_e64 v3, v137, v1
	v_mul_f32_e64 v6, v142, v6
	v_mul_f32_e64 v7, v143, v7
	v_mul_f32_e64 v4, v140, v4
	v_mul_f32_e64 v5, v141, v5
	s_nop 0
	v_cvt_pk_bf16_f32 v0, v4, v5
	v_cvt_pk_bf16_f32 v1, v6, v7
	v_cvt_pk_bf16_f32 v2, v2, v3
	v_cvt_pk_bf16_f32 v3, v8, v9
	global_store_dwordx4 v[18:19], v[0:3], off offset:64
	s_andn2_b64 vcc, exec, s[0:1]
	s_mov_b64 s[0:1], -1
	s_cbranch_vccnz .LBB0_282

.LBB0_502:
	s_lshl_b32 s44, s77, 8
	v_lshrrev_b32_e32 v40, 1, v44
	s_add_i32 s44, s44, s67
	v_and_b32_e32 v40, 24, v40
	v_lshl_or_b32 v40, s76, 8, v40
	v_and_or_b32 v152, v44, 15, s44
	v_or_b32_e32 v56, s68, v40
	s_lshl_b64 s[42:43], s[42:43], 2
	v_ashrrev_i32_e32 v153, 31, v152
	s_add_u32 s42, s6, s42
	v_ashrrev_i32_e32 v57, 31, v56
	v_lshlrev_b64 v[44:45], 12, v[152:153]
	s_addc_u32 s43, s7, s43
	v_lshlrev_b64 v[148:149], 2, v[56:57]
	v_lshl_add_u64 v[154:155], s[10:11], 0, v[44:45]
	v_lshl_add_u64 v[46:47], s[42:43], 0, v[148:149]
	v_lshl_add_u64 v[58:59], s[8:9], 0, v[44:45]
	v_lshl_add_u64 v[44:45], v[154:155], 0, s[20:21]
	v_add_co_u32_e32 v40, vcc, s74, v46
	v_cndmask_b32_e64 v45, v45, v59, s[2:3]
	v_cndmask_b32_e64 v44, v44, v58, s[2:3]
	v_addc_co_u32_e32 v41, vcc, 0, v47, vcc
	v_lshl_add_u64 v[174:175], v[44:45], 0, v[148:149]
	global_load_dwordx4 v[40:43], v[40:41], off
	s_nop 0
	global_load_dwordx4 v[166:169], v[174:175], off offset:16
	global_load_dwordx4 v[170:173], v[174:175], off
	v_lshl_add_u64 v[58:59], v[46:47], 0, s[18:19]
	global_load_dwordx4 v[44:47], v[58:59], off offset:16
	v_lshlrev_b64 v[60:61], 11, v[152:153]
	v_lshl_add_u64 v[60:61], s[14:15], 0, v[60:61]
	v_lshlrev_b64 v[150:151], 1, v[56:57]
	v_lshl_add_u64 v[176:177], v[60:61], 0, v[150:151]
	global_load_dwordx4 v[60:63], v[58:59], off offset:512
	s_nop 0
	global_load_dwordx4 v[56:59], v[58:59], off offset:528
	s_andn2_b64 vcc, exec, s[0:1]
	s_mov_b64 s[0:1], -1
	s_waitcnt vmcnt(0)
	v_fma_f32 v138, v138, v42, v172
	v_fma_f32 v139, v139, v43, v173
	v_fma_f32 v136, v136, v40, v170
	v_fma_f32 v137, v137, v41, v171
	v_fma_f32 v142, v142, v46, v168
	v_fma_f32 v143, v143, v47, v169
	v_fma_f32 v140, v140, v44, v166
	v_fma_f32 v141, v141, v45, v167
	v_cvt_pk_bf16_f32 v136, v136, v137
	v_cvt_pk_bf16_f32 v137, v138, v139
	v_or_b32_e32 v166, 16, v152
	v_cvt_pk_bf16_f32 v138, v140, v141
	v_cvt_pk_bf16_f32 v139, v142, v143
	global_store_dwordx4 v[176:177], v[136:139], off
	global_load_dwordx4 v[136:139], v[174:175], off offset:512
	s_nop 0
	global_load_dwordx4 v[140:143], v[174:175], off offset:528
	v_ashrrev_i32_e32 v167, 31, v166
	v_lshlrev_b64 v[168:169], 12, v[166:167]
	v_lshl_add_u64 v[168:169], s[8:9], 0, v[168:169]
	v_lshl_add_u64 v[170:171], v[154:155], 0, s[22:23]
	v_cndmask_b32_e64 v169, v171, v169, s[2:3]
	v_cndmask_b32_e64 v168, v170, v168, s[2:3]
	v_lshl_add_u64 v[168:169], v[168:169], 0, v[148:149]
	s_waitcnt vmcnt(1)
	v_fma_f32 v130, v130, v62, v138
	v_fma_f32 v131, v131, v63, v139
	v_fma_f32 v128, v128, v60, v136
	v_fma_f32 v129, v129, v61, v137
	s_waitcnt vmcnt(0)
	v_fma_f32 v134, v134, v58, v142
	v_fma_f32 v135, v135, v59, v143
	v_fma_f32 v132, v132, v56, v140
	v_fma_f32 v133, v133, v57, v141
	v_cvt_pk_bf16_f32 v128, v128, v129
	v_cvt_pk_bf16_f32 v129, v130, v131
	v_lshlrev_b64 v[136:137], 11, v[166:167]
	v_cvt_pk_bf16_f32 v130, v132, v133
	v_cvt_pk_bf16_f32 v131, v134, v135
	global_store_dwordx4 v[176:177], v[128:131], off offset:256
	global_load_dwordx4 v[128:131], v[168:169], off
	global_load_dwordx4 v[132:135], v[168:169], off offset:16
	v_lshl_add_u64 v[136:137], s[14:15], 0, v[136:137]
	v_lshl_add_u64 v[136:137], v[136:137], 0, v[150:151]
	s_waitcnt vmcnt(1)
	v_fma_f32 v122, v122, v42, v130
	v_fma_f32 v123, v123, v43, v131
	v_fma_f32 v120, v120, v40, v128
	v_fma_f32 v121, v121, v41, v129
	s_waitcnt vmcnt(0)
	v_fma_f32 v126, v126, v46, v134
	v_fma_f32 v127, v127, v47, v135
	v_fma_f32 v124, v124, v44, v132
	v_fma_f32 v125, v125, v45, v133
	v_cvt_pk_bf16_f32 v120, v120, v121
	v_cvt_pk_bf16_f32 v121, v122, v123
	v_or_b32_e32 v128, 32, v152
	v_cvt_pk_bf16_f32 v122, v124, v125
	v_cvt_pk_bf16_f32 v123, v126, v127
	global_store_dwordx4 v[136:137], v[120:123], off
	global_load_dwordx4 v[120:123], v[168:169], off offset:512
	s_nop 0
	global_load_dwordx4 v[124:127], v[168:169], off offset:528
	v_ashrrev_i32_e32 v129, 31, v128
	v_lshlrev_b64 v[130:131], 12, v[128:129]
	v_lshl_add_u64 v[130:131], s[8:9], 0, v[130:131]
	v_lshl_add_u64 v[132:133], v[154:155], 0, s[24:25]
	v_cndmask_b32_e64 v131, v133, v131, s[2:3]
	v_cndmask_b32_e64 v130, v132, v130, s[2:3]
	v_lshl_add_u64 v[130:131], v[130:131], 0, v[148:149]
	s_waitcnt vmcnt(1)
	v_fma_f32 v114, v114, v62, v122
	v_fma_f32 v115, v115, v63, v123
	v_fma_f32 v112, v112, v60, v120
	v_fma_f32 v113, v113, v61, v121
	s_waitcnt vmcnt(0)
	v_fma_f32 v118, v118, v58, v126
	v_fma_f32 v119, v119, v59, v127
	v_fma_f32 v116, v116, v56, v124
	v_fma_f32 v117, v117, v57, v125
	v_cvt_pk_bf16_f32 v112, v112, v113
	v_cvt_pk_bf16_f32 v113, v114, v115
	v_lshlrev_b64 v[120:121], 11, v[128:129]
	v_cvt_pk_bf16_f32 v114, v116, v117
	v_cvt_pk_bf16_f32 v115, v118, v119
	global_store_dwordx4 v[136:137], v[112:115], off offset:256
	global_load_dwordx4 v[112:115], v[130:131], off
	global_load_dwordx4 v[116:119], v[130:131], off offset:16
	v_lshl_add_u64 v[120:121], s[14:15], 0, v[120:121]
	v_lshl_add_u64 v[120:121], v[120:121], 0, v[150:151]
	s_waitcnt vmcnt(1)
	v_fma_f32 v106, v106, v42, v114
	v_fma_f32 v107, v107, v43, v115
	v_fma_f32 v104, v104, v40, v112
	v_fma_f32 v105, v105, v41, v113
	s_waitcnt vmcnt(0)
	v_fma_f32 v110, v110, v46, v118
	v_fma_f32 v111, v111, v47, v119
	v_fma_f32 v108, v108, v44, v116
	v_fma_f32 v109, v109, v45, v117
	v_cvt_pk_bf16_f32 v104, v104, v105
	v_cvt_pk_bf16_f32 v105, v106, v107
	v_or_b32_e32 v112, 48, v152
	v_cvt_pk_bf16_f32 v106, v108, v109
	v_cvt_pk_bf16_f32 v107, v110, v111
	global_store_dwordx4 v[120:121], v[104:107], off
	global_load_dwordx4 v[104:107], v[130:131], off offset:512
	s_nop 0
	global_load_dwordx4 v[108:111], v[130:131], off offset:528
	v_ashrrev_i32_e32 v113, 31, v112
	v_lshlrev_b64 v[114:115], 12, v[112:113]
	v_lshl_add_u64 v[114:115], s[8:9], 0, v[114:115]
	v_lshl_add_u64 v[116:117], v[154:155], 0, s[26:27]
	v_cndmask_b32_e64 v115, v117, v115, s[2:3]
	v_cndmask_b32_e64 v114, v116, v114, s[2:3]
	v_lshl_add_u64 v[114:115], v[114:115], 0, v[148:149]
	s_waitcnt vmcnt(1)
	v_fma_f32 v98, v98, v62, v106
	v_fma_f32 v99, v99, v63, v107
	v_fma_f32 v96, v96, v60, v104
	v_fma_f32 v97, v97, v61, v105
	s_waitcnt vmcnt(0)
	v_fma_f32 v102, v102, v58, v110
	v_fma_f32 v103, v103, v59, v111
	v_fma_f32 v100, v100, v56, v108
	v_fma_f32 v101, v101, v57, v109
	v_cvt_pk_bf16_f32 v96, v96, v97
	v_cvt_pk_bf16_f32 v97, v98, v99
	v_lshlrev_b64 v[104:105], 11, v[112:113]
	v_cvt_pk_bf16_f32 v98, v100, v101
	v_cvt_pk_bf16_f32 v99, v102, v103
	global_store_dwordx4 v[120:121], v[96:99], off offset:256
	global_load_dwordx4 v[96:99], v[114:115], off
	global_load_dwordx4 v[100:103], v[114:115], off offset:16
	v_lshl_add_u64 v[104:105], s[14:15], 0, v[104:105]
	v_lshl_add_u64 v[104:105], v[104:105], 0, v[150:151]
	s_waitcnt vmcnt(1)
	v_fma_f32 v90, v90, v42, v98
	v_fma_f32 v91, v91, v43, v99
	v_fma_f32 v88, v88, v40, v96
	v_fma_f32 v89, v89, v41, v97
	s_waitcnt vmcnt(0)
	v_fma_f32 v94, v94, v46, v102
	v_fma_f32 v95, v95, v47, v103
	v_fma_f32 v92, v92, v44, v100
	v_fma_f32 v93, v93, v45, v101
	v_cvt_pk_bf16_f32 v88, v88, v89
	v_cvt_pk_bf16_f32 v89, v90, v91
	v_add_u32_e32 v96, 0x80, v152
	v_cvt_pk_bf16_f32 v90, v92, v93
	v_cvt_pk_bf16_f32 v91, v94, v95
	global_store_dwordx4 v[104:105], v[88:91], off
	global_load_dwordx4 v[88:91], v[114:115], off offset:512
	s_nop 0
	global_load_dwordx4 v[92:95], v[114:115], off offset:528
	v_ashrrev_i32_e32 v97, 31, v96
	v_lshlrev_b64 v[98:99], 12, v[96:97]
	v_lshl_add_u64 v[98:99], s[8:9], 0, v[98:99]
	v_lshl_add_u64 v[100:101], v[154:155], 0, s[28:29]
	v_cndmask_b32_e64 v99, v101, v99, s[2:3]
	v_cndmask_b32_e64 v98, v100, v98, s[2:3]
	v_lshl_add_u64 v[98:99], v[98:99], 0, v[148:149]
	s_waitcnt vmcnt(1)
	v_fma_f32 v74, v74, v62, v90
	v_fma_f32 v75, v75, v63, v91
	v_fma_f32 v72, v72, v60, v88
	v_fma_f32 v73, v73, v61, v89
	s_waitcnt vmcnt(0)
	v_fma_f32 v78, v78, v58, v94
	v_fma_f32 v79, v79, v59, v95
	v_fma_f32 v76, v76, v56, v92
	v_fma_f32 v77, v77, v57, v93
	v_cvt_pk_bf16_f32 v72, v72, v73
	v_cvt_pk_bf16_f32 v73, v74, v75
	v_lshlrev_b64 v[88:89], 11, v[96:97]
	v_cvt_pk_bf16_f32 v74, v76, v77
	v_cvt_pk_bf16_f32 v75, v78, v79
	global_store_dwordx4 v[104:105], v[72:75], off offset:256
	global_load_dwordx4 v[72:75], v[98:99], off
	global_load_dwordx4 v[76:79], v[98:99], off offset:16
	v_lshl_add_u64 v[88:89], s[14:15], 0, v[88:89]
	v_lshl_add_u64 v[88:89], v[88:89], 0, v[150:151]
	s_waitcnt vmcnt(1)
	v_fma_f32 v74, v82, v42, v74
	v_fma_f32 v75, v83, v43, v75
	v_fma_f32 v72, v80, v40, v72
	v_fma_f32 v73, v81, v41, v73
	s_waitcnt vmcnt(0)
	v_fma_f32 v78, v86, v46, v78
	v_fma_f32 v79, v87, v47, v79
	v_fma_f32 v76, v84, v44, v76
	v_fma_f32 v77, v85, v45, v77
	v_cvt_pk_bf16_f32 v72, v72, v73
	v_cvt_pk_bf16_f32 v73, v74, v75
	v_add_u32_e32 v80, 0x90, v152
	v_cvt_pk_bf16_f32 v74, v76, v77
	v_cvt_pk_bf16_f32 v75, v78, v79
	global_store_dwordx4 v[88:89], v[72:75], off
	global_load_dwordx4 v[72:75], v[98:99], off offset:512
	s_nop 0
	global_load_dwordx4 v[76:79], v[98:99], off offset:528
	v_ashrrev_i32_e32 v81, 31, v80
	v_lshlrev_b64 v[82:83], 12, v[80:81]
	v_lshl_add_u64 v[82:83], s[8:9], 0, v[82:83]
	v_lshl_add_u64 v[84:85], v[154:155], 0, s[30:31]
	v_cndmask_b32_e64 v83, v85, v83, s[2:3]
	v_cndmask_b32_e64 v82, v84, v82, s[2:3]
	v_lshl_add_u64 v[82:83], v[82:83], 0, v[148:149]
	s_waitcnt vmcnt(1)
	v_fma_f32 v66, v66, v62, v74
	v_fma_f32 v67, v67, v63, v75
	v_fma_f32 v64, v64, v60, v72
	v_fma_f32 v65, v65, v61, v73
	s_waitcnt vmcnt(0)
	v_fma_f32 v70, v70, v58, v78
	v_fma_f32 v71, v71, v59, v79
	v_fma_f32 v68, v68, v56, v76
	v_fma_f32 v69, v69, v57, v77
	v_cvt_pk_bf16_f32 v64, v64, v65
	v_cvt_pk_bf16_f32 v65, v66, v67
	v_lshlrev_b64 v[72:73], 11, v[80:81]
	v_cvt_pk_bf16_f32 v66, v68, v69
	v_cvt_pk_bf16_f32 v67, v70, v71
	global_store_dwordx4 v[88:89], v[64:67], off offset:256
	global_load_dwordx4 v[64:67], v[82:83], off
	global_load_dwordx4 v[68:71], v[82:83], off offset:16
	v_lshl_add_u64 v[72:73], s[14:15], 0, v[72:73]
	v_lshl_add_u64 v[72:73], v[72:73], 0, v[150:151]
	s_waitcnt vmcnt(1)
	v_fma_f32 v50, v50, v42, v66
	v_fma_f32 v51, v51, v43, v67
	v_fma_f32 v48, v48, v40, v64
	v_fma_f32 v49, v49, v41, v65
	s_waitcnt vmcnt(0)
	v_fma_f32 v54, v54, v46, v70
	v_fma_f32 v55, v55, v47, v71
	v_fma_f32 v52, v52, v44, v68
	v_fma_f32 v53, v53, v45, v69
	v_cvt_pk_bf16_f32 v48, v48, v49
	v_cvt_pk_bf16_f32 v49, v50, v51
	v_add_u32_e32 v64, 0xa0, v152
	v_cvt_pk_bf16_f32 v50, v52, v53
	v_cvt_pk_bf16_f32 v51, v54, v55
	global_store_dwordx4 v[72:73], v[48:51], off
	global_load_dwordx4 v[48:51], v[82:83], off offset:512
	s_nop 0
	global_load_dwordx4 v[52:55], v[82:83], off offset:528
	v_ashrrev_i32_e32 v65, 31, v64
	v_lshlrev_b64 v[66:67], 12, v[64:65]
	v_lshl_add_u64 v[66:67], s[8:9], 0, v[66:67]
	v_lshl_add_u64 v[68:69], v[154:155], 0, s[34:35]
	v_cndmask_b32_e64 v67, v69, v67, s[2:3]
	v_cndmask_b32_e64 v66, v68, v66, s[2:3]
	v_lshl_add_u64 v[66:67], v[66:67], 0, v[148:149]
	s_waitcnt vmcnt(1)
	v_fma_f32 v34, v34, v62, v50
	v_fma_f32 v35, v35, v63, v51
	v_fma_f32 v32, v32, v60, v48
	v_fma_f32 v33, v33, v61, v49
	s_waitcnt vmcnt(0)
	v_fma_f32 v38, v38, v58, v54
	v_fma_f32 v39, v39, v59, v55
	v_fma_f32 v36, v36, v56, v52
	v_fma_f32 v37, v37, v57, v53
	v_cvt_pk_bf16_f32 v32, v32, v33
	v_cvt_pk_bf16_f32 v33, v34, v35
	v_lshlrev_b64 v[48:49], 11, v[64:65]
	v_cvt_pk_bf16_f32 v34, v36, v37
	v_cvt_pk_bf16_f32 v35, v38, v39
	global_store_dwordx4 v[72:73], v[32:35], off offset:256
	global_load_dwordx4 v[32:35], v[66:67], off
	global_load_dwordx4 v[36:39], v[66:67], off offset:16
	v_lshl_add_u64 v[48:49], s[14:15], 0, v[48:49]
	v_lshl_add_u64 v[48:49], v[48:49], 0, v[150:151]
	s_waitcnt vmcnt(1)
	v_fma_f32 v26, v26, v42, v34
	v_fma_f32 v27, v27, v43, v35
	v_fma_f32 v24, v24, v40, v32
	v_fma_f32 v25, v25, v41, v33
	s_waitcnt vmcnt(0)
	v_fma_f32 v30, v30, v46, v38
	v_fma_f32 v31, v31, v47, v39
	v_fma_f32 v28, v28, v44, v36
	v_fma_f32 v29, v29, v45, v37
	v_cvt_pk_bf16_f32 v24, v24, v25
	v_cvt_pk_bf16_f32 v25, v26, v27
	v_add_u32_e32 v32, 0xb0, v152
	v_cvt_pk_bf16_f32 v26, v28, v29
	v_cvt_pk_bf16_f32 v27, v30, v31
	global_store_dwordx4 v[48:49], v[24:27], off
	global_load_dwordx4 v[24:27], v[66:67], off offset:512
	s_nop 0
	global_load_dwordx4 v[28:31], v[66:67], off offset:528
	v_ashrrev_i32_e32 v33, 31, v32
	v_lshlrev_b64 v[34:35], 12, v[32:33]
	v_lshl_add_u64 v[34:35], s[8:9], 0, v[34:35]
	v_lshl_add_u64 v[36:37], v[154:155], 0, s[36:37]
	v_cndmask_b32_e64 v35, v37, v35, s[2:3]
	v_cndmask_b32_e64 v34, v36, v34, s[2:3]
	v_lshl_add_u64 v[34:35], v[34:35], 0, v[148:149]
	s_waitcnt vmcnt(1)
	v_fma_f32 v18, v18, v62, v26
	v_fma_f32 v19, v19, v63, v27
	v_fma_f32 v16, v16, v60, v24
	v_fma_f32 v17, v17, v61, v25
	s_waitcnt vmcnt(0)
	v_fma_f32 v22, v22, v58, v30
	v_fma_f32 v23, v23, v59, v31
	v_fma_f32 v20, v20, v56, v28
	v_fma_f32 v21, v21, v57, v29
	v_cvt_pk_bf16_f32 v16, v16, v17
	v_cvt_pk_bf16_f32 v17, v18, v19
	v_lshlrev_b64 v[24:25], 11, v[32:33]
	v_cvt_pk_bf16_f32 v18, v20, v21
	v_cvt_pk_bf16_f32 v19, v22, v23
	global_store_dwordx4 v[48:49], v[16:19], off offset:256
	global_load_dwordx4 v[16:19], v[34:35], off
	global_load_dwordx4 v[20:23], v[34:35], off offset:16
	v_lshl_add_u64 v[24:25], s[14:15], 0, v[24:25]
	v_lshl_add_u64 v[24:25], v[24:25], 0, v[150:151]
	s_waitcnt vmcnt(1)
	v_fma_f32 v6, v6, v42, v18
	v_fma_f32 v7, v7, v43, v19
	v_fma_f32 v4, v4, v40, v16
	v_fma_f32 v5, v5, v41, v17
	s_waitcnt vmcnt(0)
	v_fma_f32 v10, v10, v46, v22
	v_fma_f32 v11, v11, v47, v23
	v_fma_f32 v8, v8, v44, v20
	v_fma_f32 v9, v9, v45, v21
	v_cvt_pk_bf16_f32 v4, v4, v5
	v_cvt_pk_bf16_f32 v5, v6, v7
	s_nop 0
	v_cvt_pk_bf16_f32 v6, v8, v9
	v_cvt_pk_bf16_f32 v7, v10, v11
	global_store_dwordx4 v[24:25], v[4:7], off
	global_load_dwordx4 v[4:7], v[34:35], off offset:512
	s_nop 0
	global_load_dwordx4 v[8:11], v[34:35], off offset:528
	s_waitcnt vmcnt(1)
	v_fma_f32 v6, v14, v62, v6
	v_fma_f32 v7, v15, v63, v7
	s_waitcnt vmcnt(0)
	v_fma_f32 v10, v2, v58, v10
	v_fma_f32 v11, v3, v59, v11
	v_fma_f32 v2, v0, v56, v8
	v_fma_f32 v3, v1, v57, v9
	v_fma_f32 v4, v12, v60, v4
	v_fma_f32 v5, v13, v61, v5
	s_nop 0
	v_cvt_pk_bf16_f32 v0, v4, v5
	v_cvt_pk_bf16_f32 v1, v6, v7
	v_cvt_pk_bf16_f32 v2, v2, v3
	v_cvt_pk_bf16_f32 v3, v10, v11
	global_store_dwordx4 v[24:25], v[0:3], off offset:256
	s_cbranch_vccnz .LBB0_491
	s_andn2_b64 vcc, exec, s[12:13]
	s_cbranch_vccnz .LBB0_490
	s_barrier
	s_branch .LBB0_490

.LBB0_887:
	s_lshl_b32 s12, s69, 7
	s_or_b32 s12, s12, s58
	v_lshl_or_b32 v0, v0, 3, s12
	v_or_b32_e32 v18, s57, v1
	v_lshl_add_u32 v1, v0, 2, 0
	v_add_u32_e32 v2, 0x21000, v1
	v_add_u32_e32 v1, 0x22000, v1
	ds_read_b128 v[4:7], v2
	ds_read_b128 v[8:11], v1
	ds_read_b128 v[12:15], v2 offset:16
	ds_read_b128 v[20:23], v1 offset:16
	v_ashrrev_i32_e32 v1, 31, v0
	v_cmp_gt_i32_e32 vcc, s67, v18
	s_waitcnt lgkmcnt(0)
	v_fma_f32 v2, v8, 4.0, 4.0
	v_fma_f32 v3, v9, 4.0, 4.0
	v_fma_f32 v8, v10, 4.0, 4.0
	v_fma_f32 v9, v11, 4.0, 4.0
	v_mul_f32_e64 v16, v14, s20
	v_mul_f32_e64 v17, v15, s20
	v_fma_f32 v10, v20, 4.0, 4.0
	v_fma_f32 v11, v21, 4.0, 4.0
	v_fma_f32 v14, v22, 4.0, 4.0
	v_fma_f32 v15, v23, 4.0, 4.0
	v_mul_f32_e64 v4, v4, s20
	v_mul_f32_e64 v5, v5, s20
	v_mul_f32_e64 v6, v6, s20
	v_mul_f32_e64 v7, v7, s20
	v_mul_f32_e64 v2, v2, s22
	v_mul_f32_e64 v3, v3, s22
	v_mul_f32_e64 v8, v8, s22
	v_mul_f32_e64 v9, v9, s22
	v_mul_f32_e64 v12, v12, s20
	v_mul_f32_e64 v13, v13, s20
	v_mul_f32_e64 v10, v10, s22
	v_mul_f32_e64 v11, v11, s22
	v_mul_f32_e64 v14, v14, s22
	v_mul_f32_e64 v15, v15, s22
	s_and_saveexec_b64 s[34:35], vcc
	s_cbranch_execz .LBB0_889
	v_fma_f32 v20, -v154, s26, v16
	v_fma_f32 v21, -v155, s26, v17
	v_fma_f32 v26, -v152, s26, v12
	v_fma_f32 v27, -v153, s26, v13
	v_max_f32_e32 v20, 0xc1898193, v20
	v_max_f32_e32 v21, 0xc1898193, v21
	v_exp_f32_e32 v22, v20
	v_exp_f32_e32 v23, v21
	v_max_f32_e32 v26, 0xc1898193, v26
	v_max_f32_e32 v27, 0xc1898193, v27
	v_exp_f32_e32 v28, v26
	v_add_f32_e64 v22, v22, 1.0
	v_add_f32_e64 v23, v23, 1.0
	v_exp_f32_e32 v29, v27
	v_rcp_f32_e32 v22, v22
	v_rcp_f32_e32 v23, v23
	v_fma_f32 v30, -v144, s26, v4
	v_fma_f32 v31, -v145, s26, v5
	v_fma_f32 v24, -v158, s24, v14
	v_fma_f32 v25, -v159, s24, v15
	v_max_f32_e32 v30, 0xc1898193, v30
	v_mul_f32_e64 v20, v20, v22
	v_mul_f32_e64 v21, v21, v23
	v_add_f32_e64 v22, v28, 1.0
	v_add_f32_e64 v23, v29, 1.0
	v_max_f32_e32 v31, 0xc1898193, v31
	v_rcp_f32_e32 v22, v22
	v_rcp_f32_e32 v23, v23
	v_exp_f32_e32 v144, v30
	v_exp_f32_e32 v145, v31
	v_med3_f32 v24, v24, s65, v178
	v_mul_f32_e64 v22, v26, v22
	v_mul_f32_e64 v23, v27, v23
	v_fma_f32 v26, -v146, s26, v6
	v_fma_f32 v27, -v147, s26, v7
	v_add_f32_e64 v144, v144, 1.0
	v_add_f32_e64 v145, v145, 1.0
	v_max_f32_e32 v26, 0xc1898193, v26
	v_max_f32_e32 v27, 0xc1898193, v27
	v_exp_f32_e32 v28, v26
	v_exp_f32_e32 v29, v27
	v_rcp_f32_e32 v144, v144
	v_rcp_f32_e32 v145, v145
	v_med3_f32 v25, v25, s65, v178
	v_mul_f32_e64 v20, v24, v20
	v_mul_f32_e64 v21, v25, v21
	v_fma_f32 v24, -v156, s24, v10
	v_fma_f32 v25, -v157, s24, v11
	v_add_f32_e64 v28, v28, 1.0
	v_add_f32_e64 v29, v29, 1.0
	v_med3_f32 v24, v24, s65, v178
	v_med3_f32 v25, v25, s65, v178
	v_fma_f32 v146, -v148, s24, v2
	v_fma_f32 v147, -v149, s24, v3
	v_mul_f32_e64 v22, v24, v22
	v_mul_f32_e64 v23, v25, v23
	v_rcp_f32_e32 v28, v28
	v_rcp_f32_e32 v29, v29
	v_med3_f32 v146, v146, s65, v178
	v_med3_f32 v147, v147, s65, v178
	v_mul_f32_e64 v30, v30, v144
	v_mul_f32_e64 v31, v31, v145
	v_mov_b32_e32 v145, v161
	v_mul_f32_e64 v30, v146, v30
	v_mul_f32_e64 v31, v147, v31
	v_mov_b32_e32 v144, v161
	v_cvt_pk_fp8_f32 v145, v22, v23
	v_cvt_pk_fp8_f32 v144, v30, v31
	v_fma_f32 v24, -v150, s24, v8
	v_fma_f32 v25, -v151, s24, v9
	v_mul_f32_e64 v22, v26, v28
	v_mul_f32_e64 v23, v27, v29
	v_med3_f32 v24, v24, s65, v178
	v_med3_f32 v25, v25, s65, v178
	v_mul_f32_e64 v22, v24, v22
	v_mul_f32_e64 v23, v25, v23
	v_cvt_pk_fp8_f32 v145, v20, v21 op_sel:[0,0,1]
	v_add_u32_e32 v20, s66, v18
	v_cvt_pk_fp8_f32 v144, v22, v23 op_sel:[0,0,1]
	v_ashrrev_i32_e32 v21, 31, v20
	v_lshlrev_b64 v[20:21], 10, v[20:21]
	v_lshl_add_u64 v[20:21], s[14:15], 0, v[20:21]
	v_lshl_add_u64 v[20:21], v[20:21], 0, v[0:1]
	global_store_dwordx2 v[20:21], v[144:145], off
.LBB0_889:
	s_or_b64 exec, exec, s[34:35]
	v_or_b32_e32 v19, 16, v18
	v_cmp_gt_i32_e32 vcc, s67, v19
	s_and_saveexec_b64 s[34:35], vcc
	s_cbranch_execz .LBB0_891
	v_fma_f32 v20, -v138, s26, v16
	v_fma_f32 v21, -v139, s26, v17
	v_fma_f32 v26, -v136, s26, v12
	v_fma_f32 v27, -v137, s26, v13
	v_max_f32_e32 v20, 0xc1898193, v20
	v_max_f32_e32 v21, 0xc1898193, v21
	v_exp_f32_e32 v22, v20
	v_exp_f32_e32 v23, v21
	v_max_f32_e32 v26, 0xc1898193, v26
	v_max_f32_e32 v27, 0xc1898193, v27
	v_exp_f32_e32 v28, v26
	v_add_f32_e64 v22, v22, 1.0
	v_add_f32_e64 v23, v23, 1.0
	v_exp_f32_e32 v29, v27
	v_rcp_f32_e32 v22, v22
	v_rcp_f32_e32 v23, v23
	v_fma_f32 v30, -v128, s26, v4
	v_fma_f32 v31, -v129, s26, v5
	v_fma_f32 v24, -v142, s24, v14
	v_fma_f32 v25, -v143, s24, v15
	v_max_f32_e32 v30, 0xc1898193, v30
	v_mul_f32_e64 v20, v20, v22
	v_mul_f32_e64 v21, v21, v23
	v_add_f32_e64 v22, v28, 1.0
	v_add_f32_e64 v23, v29, 1.0
	v_max_f32_e32 v31, 0xc1898193, v31
	v_rcp_f32_e32 v22, v22
	v_rcp_f32_e32 v23, v23
	v_exp_f32_e32 v128, v30
	v_exp_f32_e32 v129, v31
	v_med3_f32 v24, v24, s65, v178
	v_mul_f32_e64 v22, v26, v22
	v_mul_f32_e64 v23, v27, v23
	v_fma_f32 v26, -v130, s26, v6
	v_fma_f32 v27, -v131, s26, v7
	v_add_f32_e64 v128, v128, 1.0
	v_add_f32_e64 v129, v129, 1.0
	v_max_f32_e32 v26, 0xc1898193, v26
	v_max_f32_e32 v27, 0xc1898193, v27
	v_exp_f32_e32 v28, v26
	v_exp_f32_e32 v29, v27
	v_rcp_f32_e32 v128, v128
	v_rcp_f32_e32 v129, v129
	v_med3_f32 v25, v25, s65, v178
	v_mul_f32_e64 v20, v24, v20
	v_mul_f32_e64 v21, v25, v21
	v_fma_f32 v24, -v140, s24, v10
	v_fma_f32 v25, -v141, s24, v11
	v_add_f32_e64 v28, v28, 1.0
	v_add_f32_e64 v29, v29, 1.0
	v_med3_f32 v24, v24, s65, v178
	v_med3_f32 v25, v25, s65, v178
	v_fma_f32 v130, -v132, s24, v2
	v_fma_f32 v131, -v133, s24, v3
	v_mul_f32_e64 v22, v24, v22
	v_mul_f32_e64 v23, v25, v23
	v_rcp_f32_e32 v28, v28
	v_rcp_f32_e32 v29, v29
	v_med3_f32 v130, v130, s65, v178
	v_med3_f32 v131, v131, s65, v178
	v_mul_f32_e64 v30, v30, v128
	v_mul_f32_e64 v31, v31, v129
	v_mov_b32_e32 v129, v161
	v_mul_f32_e64 v30, v130, v30
	v_mul_f32_e64 v31, v131, v31
	v_mov_b32_e32 v128, v161
	v_cvt_pk_fp8_f32 v129, v22, v23
	v_cvt_pk_fp8_f32 v128, v30, v31
	v_fma_f32 v24, -v134, s24, v8
	v_fma_f32 v25, -v135, s24, v9
	v_mul_f32_e64 v22, v26, v28
	v_mul_f32_e64 v23, v27, v29
	v_med3_f32 v24, v24, s65, v178
	v_med3_f32 v25, v25, s65, v178
	v_mul_f32_e64 v22, v24, v22
	v_mul_f32_e64 v23, v25, v23
	v_cvt_pk_fp8_f32 v129, v20, v21 op_sel:[0,0,1]
	v_add_u32_e32 v20, s66, v19
	v_cvt_pk_fp8_f32 v128, v22, v23 op_sel:[0,0,1]
	v_ashrrev_i32_e32 v21, 31, v20
	v_lshlrev_b64 v[20:21], 10, v[20:21]
	v_lshl_add_u64 v[20:21], s[14:15], 0, v[20:21]
	v_lshl_add_u64 v[20:21], v[20:21], 0, v[0:1]
	global_store_dwordx2 v[20:21], v[128:129], off
.LBB0_891:
	s_or_b64 exec, exec, s[34:35]
	v_or_b32_e32 v19, 32, v18
	v_cmp_gt_i32_e32 vcc, s67, v19
	s_and_saveexec_b64 s[34:35], vcc
	s_cbranch_execz .LBB0_893
	v_fma_f32 v20, -v122, s26, v16
	v_fma_f32 v21, -v123, s26, v17
	v_fma_f32 v26, -v120, s26, v12
	v_fma_f32 v27, -v121, s26, v13
	v_max_f32_e32 v20, 0xc1898193, v20
	v_max_f32_e32 v21, 0xc1898193, v21
	v_exp_f32_e32 v22, v20
	v_exp_f32_e32 v23, v21
	v_max_f32_e32 v26, 0xc1898193, v26
	v_max_f32_e32 v27, 0xc1898193, v27
	v_exp_f32_e32 v28, v26
	v_add_f32_e64 v22, v22, 1.0
	v_add_f32_e64 v23, v23, 1.0
	v_exp_f32_e32 v29, v27
	v_rcp_f32_e32 v22, v22
	v_rcp_f32_e32 v23, v23
	v_fma_f32 v30, -v112, s26, v4
	v_fma_f32 v31, -v113, s26, v5
	v_fma_f32 v24, -v126, s24, v14
	v_fma_f32 v25, -v127, s24, v15
	v_max_f32_e32 v30, 0xc1898193, v30
	v_mul_f32_e64 v20, v20, v22
	v_mul_f32_e64 v21, v21, v23
	v_add_f32_e64 v22, v28, 1.0
	v_add_f32_e64 v23, v29, 1.0
	v_max_f32_e32 v31, 0xc1898193, v31
	v_rcp_f32_e32 v22, v22
	v_rcp_f32_e32 v23, v23
	v_exp_f32_e32 v112, v30
	v_exp_f32_e32 v113, v31
	v_med3_f32 v24, v24, s65, v178
	v_mul_f32_e64 v22, v26, v22
	v_mul_f32_e64 v23, v27, v23
	v_fma_f32 v26, -v114, s26, v6
	v_fma_f32 v27, -v115, s26, v7
	v_add_f32_e64 v112, v112, 1.0
	v_add_f32_e64 v113, v113, 1.0
	v_max_f32_e32 v26, 0xc1898193, v26
	v_max_f32_e32 v27, 0xc1898193, v27
	v_exp_f32_e32 v28, v26
	v_exp_f32_e32 v29, v27
	v_rcp_f32_e32 v112, v112
	v_rcp_f32_e32 v113, v113
	v_med3_f32 v25, v25, s65, v178
	v_mul_f32_e64 v20, v24, v20
	v_mul_f32_e64 v21, v25, v21
	v_fma_f32 v24, -v124, s24, v10
	v_fma_f32 v25, -v125, s24, v11
	v_add_f32_e64 v28, v28, 1.0
	v_add_f32_e64 v29, v29, 1.0
	v_med3_f32 v24, v24, s65, v178
	v_med3_f32 v25, v25, s65, v178
	v_fma_f32 v114, -v116, s24, v2
	v_fma_f32 v115, -v117, s24, v3
	v_mul_f32_e64 v22, v24, v22
	v_mul_f32_e64 v23, v25, v23
	v_rcp_f32_e32 v28, v28
	v_rcp_f32_e32 v29, v29
	v_med3_f32 v114, v114, s65, v178
	v_med3_f32 v115, v115, s65, v178
	v_mul_f32_e64 v30, v30, v112
	v_mul_f32_e64 v31, v31, v113
	v_mov_b32_e32 v113, v161
	v_mul_f32_e64 v30, v114, v30
	v_mul_f32_e64 v31, v115, v31
	v_mov_b32_e32 v112, v161
	v_cvt_pk_fp8_f32 v113, v22, v23
	v_cvt_pk_fp8_f32 v112, v30, v31
	v_fma_f32 v24, -v118, s24, v8
	v_fma_f32 v25, -v119, s24, v9
	v_mul_f32_e64 v22, v26, v28
	v_mul_f32_e64 v23, v27, v29
	v_med3_f32 v24, v24, s65, v178
	v_med3_f32 v25, v25, s65, v178
	v_mul_f32_e64 v22, v24, v22
	v_mul_f32_e64 v23, v25, v23
	v_cvt_pk_fp8_f32 v113, v20, v21 op_sel:[0,0,1]
	v_add_u32_e32 v20, s66, v19
	v_cvt_pk_fp8_f32 v112, v22, v23 op_sel:[0,0,1]
	v_ashrrev_i32_e32 v21, 31, v20
	v_lshlrev_b64 v[20:21], 10, v[20:21]
	v_lshl_add_u64 v[20:21], s[14:15], 0, v[20:21]
	v_lshl_add_u64 v[20:21], v[20:21], 0, v[0:1]
	global_store_dwordx2 v[20:21], v[112:113], off
.LBB0_893:
	s_or_b64 exec, exec, s[34:35]
	v_or_b32_e32 v19, 48, v18
	v_cmp_gt_i32_e32 vcc, s67, v19
	s_and_saveexec_b64 s[34:35], vcc
	s_cbranch_execz .LBB0_895
	v_fma_f32 v20, -v106, s26, v16
	v_fma_f32 v21, -v107, s26, v17
	v_fma_f32 v26, -v104, s26, v12
	v_fma_f32 v27, -v105, s26, v13
	v_max_f32_e32 v20, 0xc1898193, v20
	v_max_f32_e32 v21, 0xc1898193, v21
	v_exp_f32_e32 v22, v20
	v_exp_f32_e32 v23, v21
	v_max_f32_e32 v26, 0xc1898193, v26
	v_max_f32_e32 v27, 0xc1898193, v27
	v_exp_f32_e32 v28, v26
	v_add_f32_e64 v22, v22, 1.0
	v_add_f32_e64 v23, v23, 1.0
	v_exp_f32_e32 v29, v27
	v_rcp_f32_e32 v22, v22
	v_rcp_f32_e32 v23, v23
	v_fma_f32 v30, -v88, s26, v4
	v_fma_f32 v31, -v89, s26, v5
	v_fma_f32 v24, -v110, s24, v14
	v_fma_f32 v25, -v111, s24, v15
	v_max_f32_e32 v30, 0xc1898193, v30
	v_mul_f32_e64 v20, v20, v22
	v_mul_f32_e64 v21, v21, v23
	v_add_f32_e64 v22, v28, 1.0
	v_add_f32_e64 v23, v29, 1.0
	v_max_f32_e32 v31, 0xc1898193, v31
	v_rcp_f32_e32 v22, v22
	v_rcp_f32_e32 v23, v23
	v_exp_f32_e32 v88, v30
	v_exp_f32_e32 v89, v31
	v_med3_f32 v24, v24, s65, v178
	v_mul_f32_e64 v22, v26, v22
	v_mul_f32_e64 v23, v27, v23
	v_fma_f32 v26, -v90, s26, v6
	v_fma_f32 v27, -v91, s26, v7
	v_add_f32_e64 v88, v88, 1.0
	v_add_f32_e64 v89, v89, 1.0
	v_max_f32_e32 v26, 0xc1898193, v26
	v_max_f32_e32 v27, 0xc1898193, v27
	v_exp_f32_e32 v28, v26
	v_exp_f32_e32 v29, v27
	v_rcp_f32_e32 v88, v88
	v_rcp_f32_e32 v89, v89
	v_med3_f32 v25, v25, s65, v178
	v_mul_f32_e64 v20, v24, v20
	v_mul_f32_e64 v21, v25, v21
	v_fma_f32 v24, -v108, s24, v10
	v_fma_f32 v25, -v109, s24, v11
	v_add_f32_e64 v28, v28, 1.0
	v_add_f32_e64 v29, v29, 1.0
	v_med3_f32 v24, v24, s65, v178
	v_med3_f32 v25, v25, s65, v178
	v_fma_f32 v90, -v96, s24, v2
	v_fma_f32 v91, -v97, s24, v3
	v_mul_f32_e64 v22, v24, v22
	v_mul_f32_e64 v23, v25, v23
	v_rcp_f32_e32 v28, v28
	v_rcp_f32_e32 v29, v29
	v_med3_f32 v90, v90, s65, v178
	v_med3_f32 v91, v91, s65, v178
	v_mul_f32_e64 v30, v30, v88
	v_mul_f32_e64 v31, v31, v89
	v_mov_b32_e32 v89, v161
	v_mul_f32_e64 v30, v90, v30
	v_mul_f32_e64 v31, v91, v31
	v_mov_b32_e32 v88, v161
	v_cvt_pk_fp8_f32 v89, v22, v23
	v_cvt_pk_fp8_f32 v88, v30, v31
	v_fma_f32 v24, -v98, s24, v8
	v_fma_f32 v25, -v99, s24, v9
	v_mul_f32_e64 v22, v26, v28
	v_mul_f32_e64 v23, v27, v29
	v_med3_f32 v24, v24, s65, v178
	v_med3_f32 v25, v25, s65, v178
	v_mul_f32_e64 v22, v24, v22
	v_mul_f32_e64 v23, v25, v23
	v_cvt_pk_fp8_f32 v89, v20, v21 op_sel:[0,0,1]
	v_add_u32_e32 v20, s66, v19
	v_cvt_pk_fp8_f32 v88, v22, v23 op_sel:[0,0,1]
	v_ashrrev_i32_e32 v21, 31, v20
	v_lshlrev_b64 v[20:21], 10, v[20:21]
	v_lshl_add_u64 v[20:21], s[14:15], 0, v[20:21]
	v_lshl_add_u64 v[20:21], v[20:21], 0, v[0:1]
	global_store_dwordx2 v[20:21], v[88:89], off
.LBB0_895:
	s_or_b64 exec, exec, s[34:35]
	v_add_u32_e32 v19, 0x80, v18
	v_cmp_gt_i32_e32 vcc, s67, v19
	s_and_saveexec_b64 s[34:35], vcc
	s_cbranch_execz .LBB0_897
	v_fma_f32 v20, -v94, s26, v16
	v_fma_f32 v21, -v95, s26, v17
	v_fma_f32 v26, -v92, s26, v12
	v_fma_f32 v27, -v93, s26, v13
	v_max_f32_e32 v20, 0xc1898193, v20
	v_max_f32_e32 v21, 0xc1898193, v21
	v_exp_f32_e32 v22, v20
	v_exp_f32_e32 v23, v21
	v_max_f32_e32 v26, 0xc1898193, v26
	v_max_f32_e32 v27, 0xc1898193, v27
	v_exp_f32_e32 v28, v26
	v_add_f32_e64 v22, v22, 1.0
	v_add_f32_e64 v23, v23, 1.0
	v_exp_f32_e32 v29, v27
	v_rcp_f32_e32 v22, v22
	v_rcp_f32_e32 v23, v23
	v_fma_f32 v30, -v80, s26, v4
	v_fma_f32 v31, -v81, s26, v5
	v_fma_f32 v24, -v102, s24, v14
	v_fma_f32 v25, -v103, s24, v15
	v_max_f32_e32 v30, 0xc1898193, v30
	v_mul_f32_e64 v20, v20, v22
	v_mul_f32_e64 v21, v21, v23
	v_add_f32_e64 v22, v28, 1.0
	v_add_f32_e64 v23, v29, 1.0
	v_max_f32_e32 v31, 0xc1898193, v31
	v_rcp_f32_e32 v22, v22
	v_rcp_f32_e32 v23, v23
	v_exp_f32_e32 v80, v30
	v_exp_f32_e32 v81, v31
	v_med3_f32 v24, v24, s65, v178
	v_mul_f32_e64 v22, v26, v22
	v_mul_f32_e64 v23, v27, v23
	v_fma_f32 v26, -v82, s26, v6
	v_fma_f32 v27, -v83, s26, v7
	v_add_f32_e64 v80, v80, 1.0
	v_add_f32_e64 v81, v81, 1.0
	v_max_f32_e32 v26, 0xc1898193, v26
	v_max_f32_e32 v27, 0xc1898193, v27
	v_exp_f32_e32 v28, v26
	v_exp_f32_e32 v29, v27
	v_rcp_f32_e32 v80, v80
	v_rcp_f32_e32 v81, v81
	v_med3_f32 v25, v25, s65, v178
	v_mul_f32_e64 v20, v24, v20
	v_mul_f32_e64 v21, v25, v21
	v_fma_f32 v24, -v100, s24, v10
	v_fma_f32 v25, -v101, s24, v11
	v_add_f32_e64 v28, v28, 1.0
	v_add_f32_e64 v29, v29, 1.0
	v_med3_f32 v24, v24, s65, v178
	v_med3_f32 v25, v25, s65, v178
	v_fma_f32 v82, -v84, s24, v2
	v_fma_f32 v83, -v85, s24, v3
	v_mul_f32_e64 v22, v24, v22
	v_mul_f32_e64 v23, v25, v23
	v_rcp_f32_e32 v28, v28
	v_rcp_f32_e32 v29, v29
	v_med3_f32 v82, v82, s65, v178
	v_med3_f32 v83, v83, s65, v178
	v_mul_f32_e64 v30, v30, v80
	v_mul_f32_e64 v31, v31, v81
	v_mov_b32_e32 v81, v161
	v_mul_f32_e64 v30, v82, v30
	v_mul_f32_e64 v31, v83, v31
	v_mov_b32_e32 v80, v161
	v_cvt_pk_fp8_f32 v81, v22, v23
	v_cvt_pk_fp8_f32 v80, v30, v31
	v_fma_f32 v24, -v86, s24, v8
	v_fma_f32 v25, -v87, s24, v9
	v_mul_f32_e64 v22, v26, v28
	v_mul_f32_e64 v23, v27, v29
	v_med3_f32 v24, v24, s65, v178
	v_med3_f32 v25, v25, s65, v178
	v_mul_f32_e64 v22, v24, v22
	v_mul_f32_e64 v23, v25, v23
	v_cvt_pk_fp8_f32 v81, v20, v21 op_sel:[0,0,1]
	v_add_u32_e32 v20, s66, v19
	v_cvt_pk_fp8_f32 v80, v22, v23 op_sel:[0,0,1]
	v_ashrrev_i32_e32 v21, 31, v20
	v_lshlrev_b64 v[20:21], 10, v[20:21]
	v_lshl_add_u64 v[20:21], s[14:15], 0, v[20:21]
	v_lshl_add_u64 v[20:21], v[20:21], 0, v[0:1]
	global_store_dwordx2 v[20:21], v[80:81], off
.LBB0_897:
	s_or_b64 exec, exec, s[34:35]
	v_add_u32_e32 v19, 0x90, v18
	v_cmp_gt_i32_e32 vcc, s67, v19
	s_and_saveexec_b64 s[34:35], vcc
	s_cbranch_execz .LBB0_899
	v_fma_f32 v20, -v74, s26, v16
	v_fma_f32 v21, -v75, s26, v17
	v_fma_f32 v26, -v72, s26, v12
	v_fma_f32 v27, -v73, s26, v13
	v_max_f32_e32 v20, 0xc1898193, v20
	v_max_f32_e32 v21, 0xc1898193, v21
	v_exp_f32_e32 v22, v20
	v_exp_f32_e32 v23, v21
	v_max_f32_e32 v26, 0xc1898193, v26
	v_max_f32_e32 v27, 0xc1898193, v27
	v_exp_f32_e32 v28, v26
	v_add_f32_e64 v22, v22, 1.0
	v_add_f32_e64 v23, v23, 1.0
	v_exp_f32_e32 v29, v27
	v_rcp_f32_e32 v22, v22
	v_rcp_f32_e32 v23, v23
	v_fma_f32 v30, -v64, s26, v4
	v_fma_f32 v31, -v65, s26, v5
	v_fma_f32 v24, -v78, s24, v14
	v_fma_f32 v25, -v79, s24, v15
	v_max_f32_e32 v30, 0xc1898193, v30
	v_mul_f32_e64 v20, v20, v22
	v_mul_f32_e64 v21, v21, v23
	v_add_f32_e64 v22, v28, 1.0
	v_add_f32_e64 v23, v29, 1.0
	v_max_f32_e32 v31, 0xc1898193, v31
	v_rcp_f32_e32 v22, v22
	v_rcp_f32_e32 v23, v23
	v_exp_f32_e32 v64, v30
	v_exp_f32_e32 v65, v31
	v_med3_f32 v24, v24, s65, v178
	v_mul_f32_e64 v22, v26, v22
	v_mul_f32_e64 v23, v27, v23
	v_fma_f32 v26, -v66, s26, v6
	v_fma_f32 v27, -v67, s26, v7
	v_add_f32_e64 v64, v64, 1.0
	v_add_f32_e64 v65, v65, 1.0
	v_max_f32_e32 v26, 0xc1898193, v26
	v_max_f32_e32 v27, 0xc1898193, v27
	v_exp_f32_e32 v28, v26
	v_exp_f32_e32 v29, v27
	v_rcp_f32_e32 v64, v64
	v_rcp_f32_e32 v65, v65
	v_med3_f32 v25, v25, s65, v178
	v_mul_f32_e64 v20, v24, v20
	v_mul_f32_e64 v21, v25, v21
	v_fma_f32 v24, -v76, s24, v10
	v_fma_f32 v25, -v77, s24, v11
	v_add_f32_e64 v28, v28, 1.0
	v_add_f32_e64 v29, v29, 1.0
	v_med3_f32 v24, v24, s65, v178
	v_med3_f32 v25, v25, s65, v178
	v_fma_f32 v66, -v68, s24, v2
	v_fma_f32 v67, -v69, s24, v3
	v_mul_f32_e64 v22, v24, v22
	v_mul_f32_e64 v23, v25, v23
	v_rcp_f32_e32 v28, v28
	v_rcp_f32_e32 v29, v29
	v_med3_f32 v66, v66, s65, v178
	v_med3_f32 v67, v67, s65, v178
	v_mul_f32_e64 v30, v30, v64
	v_mul_f32_e64 v31, v31, v65
	v_mov_b32_e32 v65, v161
	v_mul_f32_e64 v30, v66, v30
	v_mul_f32_e64 v31, v67, v31
	v_mov_b32_e32 v64, v161
	v_cvt_pk_fp8_f32 v65, v22, v23
	v_cvt_pk_fp8_f32 v64, v30, v31
	v_fma_f32 v24, -v70, s24, v8
	v_fma_f32 v25, -v71, s24, v9
	v_mul_f32_e64 v22, v26, v28
	v_mul_f32_e64 v23, v27, v29
	v_med3_f32 v24, v24, s65, v178
	v_med3_f32 v25, v25, s65, v178
	v_mul_f32_e64 v22, v24, v22
	v_mul_f32_e64 v23, v25, v23
	v_cvt_pk_fp8_f32 v65, v20, v21 op_sel:[0,0,1]
	v_add_u32_e32 v20, s66, v19
	v_cvt_pk_fp8_f32 v64, v22, v23 op_sel:[0,0,1]
	v_ashrrev_i32_e32 v21, 31, v20
	v_lshlrev_b64 v[20:21], 10, v[20:21]
	v_lshl_add_u64 v[20:21], s[14:15], 0, v[20:21]
	v_lshl_add_u64 v[20:21], v[20:21], 0, v[0:1]
	global_store_dwordx2 v[20:21], v[64:65], off
.LBB0_899:
	s_or_b64 exec, exec, s[34:35]
	v_add_u32_e32 v19, 0xa0, v18
	v_cmp_gt_i32_e32 vcc, s67, v19
	s_and_saveexec_b64 s[34:35], vcc
	s_cbranch_execz .LBB0_901
	v_fma_f32 v20, -v58, s26, v16
	v_fma_f32 v21, -v59, s26, v17
	v_fma_f32 v26, -v56, s26, v12
	v_fma_f32 v27, -v57, s26, v13
	v_max_f32_e32 v20, 0xc1898193, v20
	v_max_f32_e32 v21, 0xc1898193, v21
	v_exp_f32_e32 v22, v20
	v_exp_f32_e32 v23, v21
	v_max_f32_e32 v26, 0xc1898193, v26
	v_max_f32_e32 v27, 0xc1898193, v27
	v_exp_f32_e32 v28, v26
	v_add_f32_e64 v22, v22, 1.0
	v_add_f32_e64 v23, v23, 1.0
	v_exp_f32_e32 v29, v27
	v_rcp_f32_e32 v22, v22
	v_rcp_f32_e32 v23, v23
	v_fma_f32 v30, -v48, s26, v4
	v_fma_f32 v31, -v49, s26, v5
	v_fma_f32 v24, -v62, s24, v14
	v_fma_f32 v25, -v63, s24, v15
	v_max_f32_e32 v30, 0xc1898193, v30
	v_mul_f32_e64 v20, v20, v22
	v_mul_f32_e64 v21, v21, v23
	v_add_f32_e64 v22, v28, 1.0
	v_add_f32_e64 v23, v29, 1.0
	v_max_f32_e32 v31, 0xc1898193, v31
	v_rcp_f32_e32 v22, v22
	v_rcp_f32_e32 v23, v23
	v_exp_f32_e32 v48, v30
	v_exp_f32_e32 v49, v31
	v_med3_f32 v24, v24, s65, v178
	v_mul_f32_e64 v22, v26, v22
	v_mul_f32_e64 v23, v27, v23
	v_fma_f32 v26, -v50, s26, v6
	v_fma_f32 v27, -v51, s26, v7
	v_add_f32_e64 v48, v48, 1.0
	v_add_f32_e64 v49, v49, 1.0
	v_max_f32_e32 v26, 0xc1898193, v26
	v_max_f32_e32 v27, 0xc1898193, v27
	v_exp_f32_e32 v28, v26
	v_exp_f32_e32 v29, v27
	v_rcp_f32_e32 v48, v48
	v_rcp_f32_e32 v49, v49
	v_med3_f32 v25, v25, s65, v178
	v_mul_f32_e64 v20, v24, v20
	v_mul_f32_e64 v21, v25, v21
	v_fma_f32 v24, -v60, s24, v10
	v_fma_f32 v25, -v61, s24, v11
	v_add_f32_e64 v28, v28, 1.0
	v_add_f32_e64 v29, v29, 1.0
	v_med3_f32 v24, v24, s65, v178
	v_med3_f32 v25, v25, s65, v178
	v_fma_f32 v50, -v52, s24, v2
	v_fma_f32 v51, -v53, s24, v3
	v_mul_f32_e64 v22, v24, v22
	v_mul_f32_e64 v23, v25, v23
	v_rcp_f32_e32 v28, v28
	v_rcp_f32_e32 v29, v29
	v_med3_f32 v50, v50, s65, v178
	v_med3_f32 v51, v51, s65, v178
	v_mul_f32_e64 v30, v30, v48
	v_mul_f32_e64 v31, v31, v49
	v_mov_b32_e32 v49, v161
	v_mul_f32_e64 v30, v50, v30
	v_mul_f32_e64 v31, v51, v31
	v_mov_b32_e32 v48, v161
	v_cvt_pk_fp8_f32 v49, v22, v23
	v_cvt_pk_fp8_f32 v48, v30, v31
	v_fma_f32 v24, -v54, s24, v8
	v_fma_f32 v25, -v55, s24, v9
	v_mul_f32_e64 v22, v26, v28
	v_mul_f32_e64 v23, v27, v29
	v_med3_f32 v24, v24, s65, v178
	v_med3_f32 v25, v25, s65, v178
	v_mul_f32_e64 v22, v24, v22
	v_mul_f32_e64 v23, v25, v23
	v_cvt_pk_fp8_f32 v49, v20, v21 op_sel:[0,0,1]
	v_add_u32_e32 v20, s66, v19
	v_cvt_pk_fp8_f32 v48, v22, v23 op_sel:[0,0,1]
	v_ashrrev_i32_e32 v21, 31, v20
	v_lshlrev_b64 v[20:21], 10, v[20:21]
	v_lshl_add_u64 v[20:21], s[14:15], 0, v[20:21]
	v_lshl_add_u64 v[20:21], v[20:21], 0, v[0:1]
	global_store_dwordx2 v[20:21], v[48:49], off
.LBB0_901:
	s_or_b64 exec, exec, s[34:35]
	v_add_u32_e32 v18, 0xb0, v18
	v_cmp_gt_i32_e32 vcc, s67, v18
	s_and_saveexec_b64 s[34:35], vcc
	s_cbranch_execz .LBB0_903
	v_fma_f32 v16, -v46, s26, v16
	v_fma_f32 v17, -v47, s26, v17
	v_fma_f32 v12, -v44, s26, v12
	v_fma_f32 v13, -v45, s26, v13
	v_max_f32_e32 v16, 0xc1898193, v16
	v_max_f32_e32 v17, 0xc1898193, v17
	v_exp_f32_e32 v20, v16
	v_exp_f32_e32 v21, v17
	v_max_f32_e32 v12, 0xc1898193, v12
	v_max_f32_e32 v13, 0xc1898193, v13
	v_exp_f32_e32 v22, v12
	v_add_f32_e64 v20, v20, 1.0
	v_add_f32_e64 v21, v21, 1.0
	v_exp_f32_e32 v23, v13
	v_rcp_f32_e32 v20, v20
	v_rcp_f32_e32 v21, v21
	v_fma_f32 v14, -v42, s24, v14
	v_fma_f32 v15, -v43, s24, v15
	v_fma_f32 v4, -v36, s26, v4
	v_fma_f32 v5, -v37, s26, v5
	v_med3_f32 v14, v14, s65, v178
	v_med3_f32 v15, v15, s65, v178
	v_mul_f32_e64 v16, v16, v20
	v_mul_f32_e64 v17, v17, v21
	v_max_f32_e32 v4, 0xc1898193, v4
	v_mul_f32_e64 v14, v14, v16
	v_mul_f32_e64 v15, v15, v17
	v_add_f32_e64 v16, v22, 1.0
	v_add_f32_e64 v17, v23, 1.0
	v_max_f32_e32 v5, 0xc1898193, v5
	v_rcp_f32_e32 v16, v16
	v_rcp_f32_e32 v17, v17
	v_fma_f32 v10, -v40, s24, v10
	v_fma_f32 v11, -v41, s24, v11
	v_fma_f32 v6, -v38, s26, v6
	v_fma_f32 v7, -v39, s26, v7
	v_med3_f32 v10, v10, s65, v178
	v_mul_f32_e64 v12, v12, v16
	v_mul_f32_e64 v13, v13, v17
	v_exp_f32_e32 v16, v4
	v_exp_f32_e32 v17, v5
	v_med3_f32 v11, v11, s65, v178
	v_max_f32_e32 v6, 0xc1898193, v6
	v_max_f32_e32 v7, 0xc1898193, v7
	v_mul_f32_e64 v10, v10, v12
	v_mul_f32_e64 v11, v11, v13
	v_exp_f32_e32 v12, v6
	v_exp_f32_e32 v13, v7
	v_add_f32_e64 v16, v16, 1.0
	v_add_f32_e64 v17, v17, 1.0
	v_fma_f32 v2, -v32, s24, v2
	v_fma_f32 v3, -v33, s24, v3
	v_rcp_f32_e32 v16, v16
	v_rcp_f32_e32 v17, v17
	v_add_f32_e64 v12, v12, 1.0
	v_add_f32_e64 v13, v13, 1.0
	v_med3_f32 v2, v2, s65, v178
	v_rcp_f32_e32 v12, v12
	v_rcp_f32_e32 v13, v13
	v_med3_f32 v3, v3, s65, v178
	v_mul_f32_e64 v4, v4, v16
	v_mul_f32_e64 v5, v5, v17
	v_fma_f32 v8, -v34, s24, v8
	v_fma_f32 v9, -v35, s24, v9
	v_mul_f32_e64 v2, v2, v4
	v_mul_f32_e64 v3, v3, v5
	v_mov_b32_e32 v4, v161
	v_cvt_pk_fp8_f32 v4, v2, v3
	v_mov_b32_e32 v5, v161
	v_cvt_pk_fp8_f32 v5, v10, v11
	v_med3_f32 v8, v8, s65, v178
	v_med3_f32 v9, v9, s65, v178
	v_mul_f32_e64 v2, v6, v12
	v_mul_f32_e64 v3, v7, v13
	v_cvt_pk_fp8_f32 v5, v14, v15 op_sel:[0,0,1]
	v_mul_f32_e64 v2, v8, v2
	v_mul_f32_e64 v3, v9, v3
	s_nop 0
	v_cvt_pk_fp8_f32 v4, v2, v3 op_sel:[0,0,1]
	v_add_u32_e32 v2, s66, v18
	v_ashrrev_i32_e32 v3, 31, v2
	v_lshlrev_b64 v[2:3], 10, v[2:3]
	v_lshl_add_u64 v[2:3], s[14:15], 0, v[2:3]
	v_lshl_add_u64 v[0:1], v[2:3], 0, v[0:1]
	global_store_dwordx2 v[0:1], v[4:5], off

.LBB0_1097:
	s_lshl_b32 s22, s58, 8
	s_or_b32 s22, s22, s50
	v_or_b32_e32 v0, s22, v0
	v_lshl_add_u32 v2, v0, 2, 0
	v_add_u32_e32 v10, 0x21000, v2
	ds_read_b128 v[2:5], v10
	ds_read_b128 v[6:9], v10 offset:16
	ds_read_b128 v[20:23], v10 offset:32
	ds_read_b128 v[24:27], v10 offset:48
	v_or_b32_e32 v18, s46, v1
	v_ashrrev_i32_e32 v1, 31, v0
	s_waitcnt lgkmcnt(0)
	v_mul_f32_e64 v12, v6, s10
	v_mul_f32_e64 v13, v7, s10
	v_mul_f32_e64 v16, v2, s10
	v_mul_f32_e64 v17, v3, s10
	v_mul_f32_e64 v14, v4, s10
	v_mul_f32_e64 v15, v5, s10
	v_mul_f32_e64 v10, v8, s10
	v_mul_f32_e64 v11, v9, s10
	v_mul_f32_e64 v8, v20, s10
	v_mul_f32_e64 v9, v21, s10
	v_mul_f32_e64 v6, v22, s10
	v_mul_f32_e64 v7, v23, s10
	v_mul_f32_e64 v4, v24, s10
	v_mul_f32_e64 v5, v25, s10
	v_mul_f32_e64 v2, v26, s10
	v_mul_f32_e64 v3, v27, s10
	v_cmp_gt_i32_e32 vcc, s56, v18
	s_and_saveexec_b64 s[22:23], vcc
	s_cbranch_execz .LBB0_1099
	v_fma_f32 v20, v148, s12, v16
	v_fma_f32 v21, v149, s12, v17
	v_fma_f32 v22, v150, s12, v14
	v_fma_f32 v23, v151, s12, v15
	v_med3_f32 v19, v20, s54, v170
	v_med3_f32 v21, v21, s54, v170
	v_mov_b32_e32 v20, 0
	v_cvt_pk_fp8_f32 v20, v19, v21
	v_med3_f32 v19, v22, s54, v170
	v_med3_f32 v21, v23, s54, v170
	v_fma_f32 v22, v144, s12, v12
	v_fma_f32 v23, v145, s12, v13
	v_cvt_pk_fp8_f32 v20, v19, v21 op_sel:[0,0,1]
	v_med3_f32 v19, v22, s54, v170
	v_med3_f32 v22, v23, s54, v170
	v_mov_b32_e32 v21, 0
	v_cvt_pk_fp8_f32 v21, v19, v22
	v_fma_f32 v22, v146, s12, v10
	v_fma_f32 v23, v147, s12, v11
	v_fma_f32 v24, v158, s12, v6
	v_fma_f32 v25, v159, s12, v7
	v_med3_f32 v19, v22, s54, v170
	v_med3_f32 v22, v23, s54, v170
	v_cvt_pk_fp8_f32 v21, v19, v22 op_sel:[0,0,1]
	v_fma_f32 v22, v156, s12, v8
	v_fma_f32 v23, v157, s12, v9
	s_nop 0
	v_med3_f32 v19, v22, s54, v170
	v_med3_f32 v23, v23, s54, v170
	v_mov_b32_e32 v22, 0
	v_cvt_pk_fp8_f32 v22, v19, v23
	v_med3_f32 v19, v24, s54, v170
	v_med3_f32 v23, v25, s54, v170
	v_fma_f32 v24, v152, s12, v4
	v_fma_f32 v25, v153, s12, v5
	v_cvt_pk_fp8_f32 v22, v19, v23 op_sel:[0,0,1]
	v_med3_f32 v19, v24, s54, v170
	v_med3_f32 v24, v25, s54, v170
	v_mov_b32_e32 v23, 0
	v_cvt_pk_fp8_f32 v23, v19, v24
	v_fma_f32 v24, v154, s12, v2
	v_fma_f32 v25, v155, s12, v3
	s_nop 0
	v_med3_f32 v19, v24, s54, v170
	v_med3_f32 v24, v25, s54, v170
	v_cvt_pk_fp8_f32 v23, v19, v24 op_sel:[0,0,1]
	v_add_u32_e32 v24, s55, v18
	v_ashrrev_i32_e32 v25, 31, v24
	v_lshlrev_b64 v[24:25], 10, v[24:25]
	v_lshl_add_u64 v[24:25], s[6:7], 0, v[24:25]
	v_lshl_add_u64 v[24:25], v[24:25], 0, v[0:1]
	global_store_dwordx4 v[24:25], v[20:23], off
.LBB0_1099:
	s_or_b64 exec, exec, s[22:23]
	v_or_b32_e32 v19, 16, v18
	v_cmp_gt_i32_e32 vcc, s56, v19
	s_and_saveexec_b64 s[22:23], vcc
	s_cbranch_execz .LBB0_1101
	v_fma_f32 v20, v136, s12, v16
	v_fma_f32 v21, v137, s12, v17
	s_nop 0
	v_med3_f32 v22, v20, s54, v170
	v_med3_f32 v21, v21, s54, v170
	v_mov_b32_e32 v20, 0
	v_cvt_pk_fp8_f32 v20, v22, v21
	v_fma_f32 v22, v138, s12, v14
	v_fma_f32 v23, v139, s12, v15
	s_nop 0
	v_med3_f32 v21, v22, s54, v170
	v_med3_f32 v22, v23, s54, v170
	v_cvt_pk_fp8_f32 v20, v21, v22 op_sel:[0,0,1]
	v_fma_f32 v22, v128, s12, v12
	v_fma_f32 v23, v129, s12, v13
	v_mov_b32_e32 v21, 0
	v_med3_f32 v22, v22, s54, v170
	v_med3_f32 v23, v23, s54, v170
	v_cvt_pk_fp8_f32 v21, v22, v23
	v_fma_f32 v22, v130, s12, v10
	v_fma_f32 v23, v131, s12, v11
	s_nop 0
	v_med3_f32 v22, v22, s54, v170
	v_med3_f32 v23, v23, s54, v170
	v_cvt_pk_fp8_f32 v21, v22, v23 op_sel:[0,0,1]
	v_fma_f32 v22, v140, s12, v8
	v_fma_f32 v23, v141, s12, v9
	s_nop 0
	v_med3_f32 v24, v22, s54, v170
	v_med3_f32 v23, v23, s54, v170
	v_mov_b32_e32 v22, 0
	v_cvt_pk_fp8_f32 v22, v24, v23
	v_fma_f32 v24, v142, s12, v6
	v_fma_f32 v25, v143, s12, v7
	s_nop 0
	v_med3_f32 v23, v24, s54, v170
	v_med3_f32 v24, v25, s54, v170
	v_cvt_pk_fp8_f32 v22, v23, v24 op_sel:[0,0,1]
	v_fma_f32 v24, v132, s12, v4
	v_fma_f32 v25, v133, s12, v5
	v_mov_b32_e32 v23, 0
	v_med3_f32 v24, v24, s54, v170
	v_med3_f32 v25, v25, s54, v170
	v_cvt_pk_fp8_f32 v23, v24, v25
	v_fma_f32 v24, v134, s12, v2
	v_fma_f32 v25, v135, s12, v3
	s_nop 0
	v_med3_f32 v24, v24, s54, v170
	v_med3_f32 v25, v25, s54, v170
	v_cvt_pk_fp8_f32 v23, v24, v25 op_sel:[0,0,1]
	v_add_u32_e32 v24, s55, v19
	v_ashrrev_i32_e32 v25, 31, v24
	v_lshlrev_b64 v[24:25], 10, v[24:25]
	v_lshl_add_u64 v[24:25], s[6:7], 0, v[24:25]
	v_lshl_add_u64 v[24:25], v[24:25], 0, v[0:1]
	global_store_dwordx4 v[24:25], v[20:23], off
.LBB0_1101:
	s_or_b64 exec, exec, s[22:23]
	v_or_b32_e32 v19, 32, v18
	v_cmp_gt_i32_e32 vcc, s56, v19
	s_and_saveexec_b64 s[22:23], vcc
	s_cbranch_execz .LBB0_1103
	v_fma_f32 v20, v120, s12, v16
	v_fma_f32 v21, v121, s12, v17
	s_nop 0
	v_med3_f32 v22, v20, s54, v170
	v_med3_f32 v21, v21, s54, v170
	v_mov_b32_e32 v20, 0
	v_cvt_pk_fp8_f32 v20, v22, v21
	v_fma_f32 v22, v122, s12, v14
	v_fma_f32 v23, v123, s12, v15
	s_nop 0
	v_med3_f32 v21, v22, s54, v170
	v_med3_f32 v22, v23, s54, v170
	v_cvt_pk_fp8_f32 v20, v21, v22 op_sel:[0,0,1]
	v_fma_f32 v22, v112, s12, v12
	v_fma_f32 v23, v113, s12, v13
	v_mov_b32_e32 v21, 0
	v_med3_f32 v22, v22, s54, v170
	v_med3_f32 v23, v23, s54, v170
	v_cvt_pk_fp8_f32 v21, v22, v23
	v_fma_f32 v22, v114, s12, v10
	v_fma_f32 v23, v115, s12, v11
	s_nop 0
	v_med3_f32 v22, v22, s54, v170
	v_med3_f32 v23, v23, s54, v170
	v_cvt_pk_fp8_f32 v21, v22, v23 op_sel:[0,0,1]
	v_fma_f32 v22, v124, s12, v8
	v_fma_f32 v23, v125, s12, v9
	s_nop 0
	v_med3_f32 v24, v22, s54, v170
	v_med3_f32 v23, v23, s54, v170
	v_mov_b32_e32 v22, 0
	v_cvt_pk_fp8_f32 v22, v24, v23
	v_fma_f32 v24, v126, s12, v6
	v_fma_f32 v25, v127, s12, v7
	s_nop 0
	v_med3_f32 v23, v24, s54, v170
	v_med3_f32 v24, v25, s54, v170
	v_cvt_pk_fp8_f32 v22, v23, v24 op_sel:[0,0,1]
	v_fma_f32 v24, v116, s12, v4
	v_fma_f32 v25, v117, s12, v5
	v_mov_b32_e32 v23, 0
	v_med3_f32 v24, v24, s54, v170
	v_med3_f32 v25, v25, s54, v170
	v_cvt_pk_fp8_f32 v23, v24, v25
	v_fma_f32 v24, v118, s12, v2
	v_fma_f32 v25, v119, s12, v3
	s_nop 0
	v_med3_f32 v24, v24, s54, v170
	v_med3_f32 v25, v25, s54, v170
	v_cvt_pk_fp8_f32 v23, v24, v25 op_sel:[0,0,1]
	v_add_u32_e32 v24, s55, v19
	v_ashrrev_i32_e32 v25, 31, v24
	v_lshlrev_b64 v[24:25], 10, v[24:25]
	v_lshl_add_u64 v[24:25], s[6:7], 0, v[24:25]
	v_lshl_add_u64 v[24:25], v[24:25], 0, v[0:1]
	global_store_dwordx4 v[24:25], v[20:23], off
.LBB0_1103:
	s_or_b64 exec, exec, s[22:23]
	v_or_b32_e32 v19, 48, v18
	v_cmp_gt_i32_e32 vcc, s56, v19
	s_and_saveexec_b64 s[22:23], vcc
	s_cbranch_execz .LBB0_1105
	v_fma_f32 v20, v108, s12, v16
	v_fma_f32 v21, v109, s12, v17
	s_nop 0
	v_med3_f32 v22, v20, s54, v170
	v_med3_f32 v21, v21, s54, v170
	v_mov_b32_e32 v20, 0
	v_cvt_pk_fp8_f32 v20, v22, v21
	v_fma_f32 v22, v110, s12, v14
	v_fma_f32 v23, v111, s12, v15
	s_nop 0
	v_med3_f32 v21, v22, s54, v170
	v_med3_f32 v22, v23, s54, v170
	v_cvt_pk_fp8_f32 v20, v21, v22 op_sel:[0,0,1]
	v_fma_f32 v22, v92, s12, v12
	v_fma_f32 v23, v93, s12, v13
	v_mov_b32_e32 v21, 0
	v_med3_f32 v22, v22, s54, v170
	v_med3_f32 v23, v23, s54, v170
	v_cvt_pk_fp8_f32 v21, v22, v23
	v_fma_f32 v22, v94, s12, v10
	v_fma_f32 v23, v95, s12, v11
	s_nop 0
	v_med3_f32 v22, v22, s54, v170
	v_med3_f32 v23, v23, s54, v170
	v_cvt_pk_fp8_f32 v21, v22, v23 op_sel:[0,0,1]
	v_fma_f32 v22, v96, s12, v8
	v_fma_f32 v23, v97, s12, v9
	s_nop 0
	v_med3_f32 v24, v22, s54, v170
	v_med3_f32 v23, v23, s54, v170
	v_mov_b32_e32 v22, 0
	v_cvt_pk_fp8_f32 v22, v24, v23
	v_fma_f32 v24, v98, s12, v6
	v_fma_f32 v25, v99, s12, v7
	s_nop 0
	v_med3_f32 v23, v24, s54, v170
	v_med3_f32 v24, v25, s54, v170
	v_cvt_pk_fp8_f32 v22, v23, v24 op_sel:[0,0,1]
	v_fma_f32 v24, v80, s12, v4
	v_fma_f32 v25, v81, s12, v5
	v_mov_b32_e32 v23, 0
	v_med3_f32 v24, v24, s54, v170
	v_med3_f32 v25, v25, s54, v170
	v_cvt_pk_fp8_f32 v23, v24, v25
	v_fma_f32 v24, v82, s12, v2
	v_fma_f32 v25, v83, s12, v3
	s_nop 0
	v_med3_f32 v24, v24, s54, v170
	v_med3_f32 v25, v25, s54, v170
	v_cvt_pk_fp8_f32 v23, v24, v25 op_sel:[0,0,1]
	v_add_u32_e32 v24, s55, v19
	v_ashrrev_i32_e32 v25, 31, v24
	v_lshlrev_b64 v[24:25], 10, v[24:25]
	v_lshl_add_u64 v[24:25], s[6:7], 0, v[24:25]
	v_lshl_add_u64 v[24:25], v[24:25], 0, v[0:1]
	global_store_dwordx4 v[24:25], v[20:23], off
.LBB0_1105:
	s_or_b64 exec, exec, s[22:23]
	v_add_u32_e32 v19, 0x80, v18
	v_cmp_gt_i32_e32 vcc, s56, v19
	s_and_saveexec_b64 s[22:23], vcc
	s_cbranch_execz .LBB0_1107
	v_fma_f32 v20, v100, s12, v16
	v_fma_f32 v21, v101, s12, v17
	s_nop 0
	v_med3_f32 v22, v20, s54, v170
	v_med3_f32 v21, v21, s54, v170
	v_mov_b32_e32 v20, 0
	v_cvt_pk_fp8_f32 v20, v22, v21
	v_fma_f32 v22, v102, s12, v14
	v_fma_f32 v23, v103, s12, v15
	s_nop 0
	v_med3_f32 v21, v22, s54, v170
	v_med3_f32 v22, v23, s54, v170
	v_cvt_pk_fp8_f32 v20, v21, v22 op_sel:[0,0,1]
	v_fma_f32 v22, v84, s12, v12
	v_fma_f32 v23, v85, s12, v13
	v_mov_b32_e32 v21, 0
	v_med3_f32 v22, v22, s54, v170
	v_med3_f32 v23, v23, s54, v170
	v_cvt_pk_fp8_f32 v21, v22, v23
	v_fma_f32 v22, v86, s12, v10
	v_fma_f32 v23, v87, s12, v11
	s_nop 0
	v_med3_f32 v22, v22, s54, v170
	v_med3_f32 v23, v23, s54, v170
	v_cvt_pk_fp8_f32 v21, v22, v23 op_sel:[0,0,1]
	v_fma_f32 v22, v104, s12, v8
	v_fma_f32 v23, v105, s12, v9
	s_nop 0
	v_med3_f32 v24, v22, s54, v170
	v_med3_f32 v23, v23, s54, v170
	v_mov_b32_e32 v22, 0
	v_cvt_pk_fp8_f32 v22, v24, v23
	v_fma_f32 v24, v106, s12, v6
	v_fma_f32 v25, v107, s12, v7
	s_nop 0
	v_med3_f32 v23, v24, s54, v170
	v_med3_f32 v24, v25, s54, v170
	v_cvt_pk_fp8_f32 v22, v23, v24 op_sel:[0,0,1]
	v_fma_f32 v24, v88, s12, v4
	v_fma_f32 v25, v89, s12, v5
	v_mov_b32_e32 v23, 0
	v_med3_f32 v24, v24, s54, v170
	v_med3_f32 v25, v25, s54, v170
	v_cvt_pk_fp8_f32 v23, v24, v25
	v_fma_f32 v24, v90, s12, v2
	v_fma_f32 v25, v91, s12, v3
	s_nop 0
	v_med3_f32 v24, v24, s54, v170
	v_med3_f32 v25, v25, s54, v170
	v_cvt_pk_fp8_f32 v23, v24, v25 op_sel:[0,0,1]
	v_add_u32_e32 v24, s55, v19
	v_ashrrev_i32_e32 v25, 31, v24
	v_lshlrev_b64 v[24:25], 10, v[24:25]
	v_lshl_add_u64 v[24:25], s[6:7], 0, v[24:25]
	v_lshl_add_u64 v[24:25], v[24:25], 0, v[0:1]
	global_store_dwordx4 v[24:25], v[20:23], off
.LBB0_1107:
	s_or_b64 exec, exec, s[22:23]
	v_add_u32_e32 v19, 0x90, v18
	v_cmp_gt_i32_e32 vcc, s56, v19
	s_and_saveexec_b64 s[22:23], vcc
	s_cbranch_execz .LBB0_1109
	v_fma_f32 v20, v76, s12, v16
	v_fma_f32 v21, v77, s12, v17
	s_nop 0
	v_med3_f32 v22, v20, s54, v170
	v_med3_f32 v21, v21, s54, v170
	v_mov_b32_e32 v20, 0
	v_cvt_pk_fp8_f32 v20, v22, v21
	v_fma_f32 v22, v78, s12, v14
	v_fma_f32 v23, v79, s12, v15
	s_nop 0
	v_med3_f32 v21, v22, s54, v170
	v_med3_f32 v22, v23, s54, v170
	v_cvt_pk_fp8_f32 v20, v21, v22 op_sel:[0,0,1]
	v_fma_f32 v22, v68, s12, v12
	v_fma_f32 v23, v69, s12, v13
	v_mov_b32_e32 v21, 0
	v_med3_f32 v22, v22, s54, v170
	v_med3_f32 v23, v23, s54, v170
	v_cvt_pk_fp8_f32 v21, v22, v23
	v_fma_f32 v22, v70, s12, v10
	v_fma_f32 v23, v71, s12, v11
	s_nop 0
	v_med3_f32 v22, v22, s54, v170
	v_med3_f32 v23, v23, s54, v170
	v_cvt_pk_fp8_f32 v21, v22, v23 op_sel:[0,0,1]
	v_fma_f32 v22, v72, s12, v8
	v_fma_f32 v23, v73, s12, v9
	s_nop 0
	v_med3_f32 v24, v22, s54, v170
	v_med3_f32 v23, v23, s54, v170
	v_mov_b32_e32 v22, 0
	v_cvt_pk_fp8_f32 v22, v24, v23
	v_fma_f32 v24, v74, s12, v6
	v_fma_f32 v25, v75, s12, v7
	s_nop 0
	v_med3_f32 v23, v24, s54, v170
	v_med3_f32 v24, v25, s54, v170
	v_cvt_pk_fp8_f32 v22, v23, v24 op_sel:[0,0,1]
	v_fma_f32 v24, v64, s12, v4
	v_fma_f32 v25, v65, s12, v5
	v_mov_b32_e32 v23, 0
	v_med3_f32 v24, v24, s54, v170
	v_med3_f32 v25, v25, s54, v170
	v_cvt_pk_fp8_f32 v23, v24, v25
	v_fma_f32 v24, v66, s12, v2
	v_fma_f32 v25, v67, s12, v3
	s_nop 0
	v_med3_f32 v24, v24, s54, v170
	v_med3_f32 v25, v25, s54, v170
	v_cvt_pk_fp8_f32 v23, v24, v25 op_sel:[0,0,1]
	v_add_u32_e32 v24, s55, v19
	v_ashrrev_i32_e32 v25, 31, v24
	v_lshlrev_b64 v[24:25], 10, v[24:25]
	v_lshl_add_u64 v[24:25], s[6:7], 0, v[24:25]
	v_lshl_add_u64 v[24:25], v[24:25], 0, v[0:1]
	global_store_dwordx4 v[24:25], v[20:23], off
.LBB0_1109:
	s_or_b64 exec, exec, s[22:23]
	v_add_u32_e32 v19, 0xa0, v18
	v_cmp_gt_i32_e32 vcc, s56, v19
	s_and_saveexec_b64 s[22:23], vcc
	s_cbranch_execz .LBB0_1111
	v_fma_f32 v20, v60, s12, v16
	v_fma_f32 v21, v61, s12, v17
	s_nop 0
	v_med3_f32 v22, v20, s54, v170
	v_med3_f32 v21, v21, s54, v170
	v_mov_b32_e32 v20, 0
	v_cvt_pk_fp8_f32 v20, v22, v21
	v_fma_f32 v22, v62, s12, v14
	v_fma_f32 v23, v63, s12, v15
	s_nop 0
	v_med3_f32 v21, v22, s54, v170
	v_med3_f32 v22, v23, s54, v170
	v_cvt_pk_fp8_f32 v20, v21, v22 op_sel:[0,0,1]
	v_fma_f32 v22, v52, s12, v12
	v_fma_f32 v23, v53, s12, v13
	v_mov_b32_e32 v21, 0
	v_med3_f32 v22, v22, s54, v170
	v_med3_f32 v23, v23, s54, v170
	v_cvt_pk_fp8_f32 v21, v22, v23
	v_fma_f32 v22, v54, s12, v10
	v_fma_f32 v23, v55, s12, v11
	s_nop 0
	v_med3_f32 v22, v22, s54, v170
	v_med3_f32 v23, v23, s54, v170
	v_cvt_pk_fp8_f32 v21, v22, v23 op_sel:[0,0,1]
	v_fma_f32 v22, v56, s12, v8
	v_fma_f32 v23, v57, s12, v9
	s_nop 0
	v_med3_f32 v24, v22, s54, v170
	v_med3_f32 v23, v23, s54, v170
	v_mov_b32_e32 v22, 0
	v_cvt_pk_fp8_f32 v22, v24, v23
	v_fma_f32 v24, v58, s12, v6
	v_fma_f32 v25, v59, s12, v7
	s_nop 0
	v_med3_f32 v23, v24, s54, v170
	v_med3_f32 v24, v25, s54, v170
	v_cvt_pk_fp8_f32 v22, v23, v24 op_sel:[0,0,1]
	v_fma_f32 v24, v48, s12, v4
	v_fma_f32 v25, v49, s12, v5
	v_mov_b32_e32 v23, 0
	v_med3_f32 v24, v24, s54, v170
	v_med3_f32 v25, v25, s54, v170
	v_cvt_pk_fp8_f32 v23, v24, v25
	v_fma_f32 v24, v50, s12, v2
	v_fma_f32 v25, v51, s12, v3
	s_nop 0
	v_med3_f32 v24, v24, s54, v170
	v_med3_f32 v25, v25, s54, v170
	v_cvt_pk_fp8_f32 v23, v24, v25 op_sel:[0,0,1]
	v_add_u32_e32 v24, s55, v19
	v_ashrrev_i32_e32 v25, 31, v24
	v_lshlrev_b64 v[24:25], 10, v[24:25]
	v_lshl_add_u64 v[24:25], s[6:7], 0, v[24:25]
	v_lshl_add_u64 v[24:25], v[24:25], 0, v[0:1]
	global_store_dwordx4 v[24:25], v[20:23], off
.LBB0_1111:
	s_or_b64 exec, exec, s[22:23]
	v_add_u32_e32 v18, 0xb0, v18
	v_cmp_gt_i32_e32 vcc, s56, v18
	s_and_saveexec_b64 s[22:23], vcc
	s_cbranch_execz .LBB0_1113
	v_fma_f32 v4, v32, s12, v4
	v_fma_f32 v5, v33, s12, v5
	v_fma_f32 v16, v44, s12, v16
	v_fma_f32 v17, v45, s12, v17
	v_fma_f32 v12, v40, s12, v12
	v_fma_f32 v13, v41, s12, v13
	v_fma_f32 v8, v36, s12, v8
	v_fma_f32 v9, v37, s12, v9
	v_med3_f32 v4, v4, s54, v170
	v_med3_f32 v5, v5, s54, v170
	v_mov_b32_e32 v23, 0
	v_med3_f32 v16, v16, s54, v170
	v_med3_f32 v17, v17, s54, v170
	v_mov_b32_e32 v20, 0
	v_med3_f32 v12, v12, s54, v170
	v_med3_f32 v13, v13, s54, v170
	v_mov_b32_e32 v21, 0
	v_med3_f32 v8, v8, s54, v170
	v_med3_f32 v9, v9, s54, v170
	v_mov_b32_e32 v22, 0
	v_cvt_pk_fp8_f32 v23, v4, v5
	v_cvt_pk_fp8_f32 v20, v16, v17
	v_cvt_pk_fp8_f32 v21, v12, v13
	v_cvt_pk_fp8_f32 v22, v8, v9
	v_fma_f32 v2, v34, s12, v2
	v_fma_f32 v3, v35, s12, v3
	v_fma_f32 v14, v46, s12, v14
	v_fma_f32 v15, v47, s12, v15
	v_fma_f32 v10, v42, s12, v10
	v_fma_f32 v11, v43, s12, v11
	v_fma_f32 v6, v38, s12, v6
	v_fma_f32 v7, v39, s12, v7
	v_med3_f32 v2, v2, s54, v170
	v_med3_f32 v3, v3, s54, v170
	v_med3_f32 v14, v14, s54, v170
	v_med3_f32 v15, v15, s54, v170
	v_med3_f32 v10, v10, s54, v170
	v_med3_f32 v11, v11, s54, v170
	v_med3_f32 v6, v6, s54, v170
	v_med3_f32 v7, v7, s54, v170
	v_cvt_pk_fp8_f32 v23, v2, v3 op_sel:[0,0,1]
	v_add_u32_e32 v2, s55, v18
	v_cvt_pk_fp8_f32 v20, v14, v15 op_sel:[0,0,1]
	v_cvt_pk_fp8_f32 v21, v10, v11 op_sel:[0,0,1]
	v_cvt_pk_fp8_f32 v22, v6, v7 op_sel:[0,0,1]
	v_ashrrev_i32_e32 v3, 31, v2
	v_lshlrev_b64 v[2:3], 10, v[2:3]
	v_lshl_add_u64 v[2:3], s[6:7], 0, v[2:3]
	v_lshl_add_u64 v[0:1], v[2:3], 0, v[0:1]
	global_store_dwordx4 v[0:1], v[20:23], off

.LBB0_1283:
	s_cmp_lt_i32 s61, 4
	s_cselect_b64 s[24:25], -1, 0
	s_cmp_gt_i32 s61, 3
	s_cbranch_scc1 .LBB0_1285
	v_mul_f32_e32 v135, 0x3d372713, v120
	v_mul_f32_e32 v135, v120, v135
	v_mul_f32_e32 v136, 0x3d372713, v125
	v_fma_f32 v135, v120, v135, v120
	v_mul_f32_e32 v136, v125, v136
	v_mul_f32_e32 v135, 0xbfcc422a, v135
	v_fma_f32 v136, v125, v136, v125
	v_mul_f32_e32 v135, 0x3fb8aa3b, v135
	v_mul_f32_e32 v136, 0xbfcc422a, v136
	v_exp_f32_e32 v135, v135
	v_mul_f32_e32 v136, 0x3fb8aa3b, v136
	v_exp_f32_e32 v137, v136
	v_mul_f32_e32 v139, 0x3d372713, v122
	v_add_f32_e32 v135, 1.0, v135
	v_mul_f32_e32 v134, 0x3d372713, v124
	v_rcp_f32_e32 v136, v135
	v_add_f32_e32 v135, 1.0, v137
	v_mul_f32_e32 v137, 0x3d372713, v121
	v_mul_f32_e32 v138, 0x3d372713, v126
	v_mul_f32_e32 v139, v122, v139
	v_mul_f32_e32 v149, 0x3d372713, v127
	v_mul_f32_e32 v150, 0x3d372713, v123
	v_mul_f32_e32 v134, v124, v134
	v_mul_f32_e32 v137, v121, v137
	v_mul_f32_e32 v138, v126, v138
	v_fma_f32 v139, v122, v139, v122
	v_mul_f32_e32 v149, v127, v149
	v_mul_f32_e32 v150, v123, v150
	v_fma_f32 v134, v124, v134, v124
	v_fma_f32 v137, v121, v137, v121
	v_fma_f32 v138, v126, v138, v126
	v_mul_f32_e32 v139, 0xbfcc422a, v139
	v_fma_f32 v149, v127, v149, v127
	v_fma_f32 v150, v123, v150, v123
	v_mul_f32_e32 v134, 0xbfcc422a, v134
	v_mul_f32_e32 v137, 0xbfcc422a, v137
	v_mul_f32_e32 v138, 0xbfcc422a, v138
	v_mul_f32_e32 v139, 0x3fb8aa3b, v139
	v_mul_f32_e32 v149, 0xbfcc422a, v149
	v_mul_f32_e32 v150, 0xbfcc422a, v150
	v_mul_f32_e32 v134, 0x3fb8aa3b, v134
	v_mul_f32_e32 v137, 0x3fb8aa3b, v137
	v_mul_f32_e32 v138, 0x3fb8aa3b, v138
	v_exp_f32_e32 v139, v139
	v_mul_f32_e32 v149, 0x3fb8aa3b, v149
	v_mul_f32_e32 v150, 0x3fb8aa3b, v150
	v_exp_f32_e32 v134, v134
	v_exp_f32_e32 v137, v137
	v_exp_f32_e32 v138, v138
	v_exp_f32_e32 v149, v149
	v_exp_f32_e32 v151, v150
	v_add_f32_e32 v139, 1.0, v139
	v_add_f32_e32 v134, 1.0, v134
	v_add_f32_e32 v137, 1.0, v137
	v_add_f32_e32 v138, 1.0, v138
	v_rcp_f32_e32 v150, v139
	v_add_f32_e32 v139, 1.0, v149
	v_add_f32_e32 v149, 1.0, v151
	v_rcp_f32_e32 v134, v134
	v_rcp_f32_e32 v135, v135
	v_rcp_f32_e32 v138, v138
	v_rcp_f32_e32 v139, v139
	v_rcp_f32_e32 v151, v149
	v_rcp_f32_e32 v137, v137
	v_mul_f32_e64 v124, v124, v134
	v_mul_f32_e64 v125, v125, v135
	v_mul_f32_e64 v126, v126, v138
	v_mul_f32_e64 v127, v127, v139
	v_mul_f32_e64 v122, v122, v150
	v_mul_f32_e64 v123, v123, v151
	v_mul_f32_e64 v120, v120, v136
	v_mul_f32_e64 v121, v121, v137
.LBB0_1285:
	s_lshl_b32 s2, s60, 8
	s_add_i32 s2, s2, s49
	v_and_or_b32 v134, v128, 15, s2
	s_and_b64 s[2:3], s[24:25], exec
	s_cselect_b32 s2, s58, 0x17100000
	s_add_u32 s2, s6, s2
	s_addc_u32 s3, s7, 0
	s_lshl_b32 s26, s61, 8
	s_and_b32 s26, s26, 0x300
	v_lshrrev_b32_e32 v128, 1, v128
	v_and_or_b32 v128, v128, 24, s26
	v_or_b32_e32 v128, s50, v128
	v_lshlrev_b32_e32 v128, 1, v128
	v_ashrrev_i32_e32 v135, 31, v134
	v_lshl_add_u64 v[136:137], s[2:3], 0, v[128:129]
	v_lshlrev_b64 v[138:139], 11, v[134:135]
	v_cvt_pk_bf16_f32 v124, v124, v125
	v_cvt_pk_bf16_f32 v125, v126, v127
	v_cvt_pk_bf16_f32 v126, v120, v121
	v_cndmask_b32_e64 v120, 0, 1, s[24:25]
	v_lshl_add_u64 v[138:139], v[136:137], 0, v[138:139]
	v_cmp_ne_u32_e64 s[2:3], 1, v120
	s_andn2_b64 vcc, exec, s[24:25]
	v_cvt_pk_bf16_f32 v127, v122, v123
	global_store_dwordx4 v[138:139], v[124:127], off
	s_cbranch_vccnz .LBB0_1287
	v_mul_f32_e32 v121, 0x3d372713, v112
	v_mul_f32_e32 v121, v112, v121
	v_mul_f32_e32 v122, 0x3d372713, v117
	v_fma_f32 v121, v112, v121, v112
	v_mul_f32_e32 v122, v117, v122
	v_mul_f32_e32 v121, 0xbfcc422a, v121
	v_fma_f32 v122, v117, v122, v117
	v_mul_f32_e32 v121, 0x3fb8aa3b, v121
	v_mul_f32_e32 v122, 0xbfcc422a, v122
	v_exp_f32_e32 v121, v121
	v_mul_f32_e32 v122, 0x3fb8aa3b, v122
	v_mul_f32_e32 v126, 0x3d372713, v119
	v_exp_f32_e32 v123, v122
	v_mul_f32_e32 v126, v119, v126
	v_fma_f32 v126, v119, v126, v119
	v_mul_f32_e32 v126, 0xbfcc422a, v126
	v_add_f32_e32 v121, 1.0, v121
	v_mul_f32_e32 v125, 0x3d372713, v114
	v_mul_f32_e32 v126, 0x3fb8aa3b, v126
	v_mul_f32_e32 v120, 0x3d372713, v116
	v_rcp_f32_e32 v122, v121
	v_add_f32_e32 v121, 1.0, v123
	v_mul_f32_e32 v123, 0x3d372713, v113
	v_mul_f32_e32 v124, 0x3d372713, v118
	v_mul_f32_e32 v125, v114, v125
	v_exp_f32_e32 v127, v126
	v_mul_f32_e32 v126, 0x3d372713, v115
	v_mul_f32_e32 v120, v116, v120
	v_mul_f32_e32 v123, v113, v123
	v_mul_f32_e32 v124, v118, v124
	v_fma_f32 v125, v114, v125, v114
	v_mul_f32_e32 v126, v115, v126
	v_fma_f32 v120, v116, v120, v116
	v_fma_f32 v123, v113, v123, v113
	v_fma_f32 v124, v118, v124, v118
	v_mul_f32_e32 v125, 0xbfcc422a, v125
	v_fma_f32 v126, v115, v126, v115
	v_mul_f32_e32 v120, 0xbfcc422a, v120
	v_mul_f32_e32 v123, 0xbfcc422a, v123
	v_mul_f32_e32 v124, 0xbfcc422a, v124
	v_mul_f32_e32 v125, 0x3fb8aa3b, v125
	v_mul_f32_e32 v126, 0xbfcc422a, v126
	v_mul_f32_e32 v120, 0x3fb8aa3b, v120
	v_mul_f32_e32 v123, 0x3fb8aa3b, v123
	v_mul_f32_e32 v124, 0x3fb8aa3b, v124
	v_exp_f32_e32 v125, v125
	v_mul_f32_e32 v126, 0x3fb8aa3b, v126
	v_exp_f32_e32 v120, v120
	v_exp_f32_e32 v123, v123
	v_exp_f32_e32 v124, v124
	v_exp_f32_e32 v128, v126
	v_add_f32_e32 v125, 1.0, v125
	v_add_f32_e32 v120, 1.0, v120
	v_add_f32_e32 v123, 1.0, v123
	v_add_f32_e32 v124, 1.0, v124
	v_rcp_f32_e32 v126, v125
	v_add_f32_e32 v125, 1.0, v127
	v_add_f32_e32 v127, 1.0, v128
	v_rcp_f32_e32 v120, v120
	v_rcp_f32_e32 v121, v121
	v_rcp_f32_e32 v124, v124
	v_rcp_f32_e32 v125, v125
	v_rcp_f32_e32 v127, v127
	v_rcp_f32_e32 v123, v123
	v_mul_f32_e64 v116, v116, v120
	v_mul_f32_e64 v117, v117, v121
	v_mul_f32_e64 v118, v118, v124
	v_mul_f32_e64 v119, v119, v125
	v_mul_f32_e64 v114, v114, v126
	v_mul_f32_e64 v115, v115, v127
	v_mul_f32_e64 v112, v112, v122
	v_mul_f32_e64 v113, v113, v123
.LBB0_1287:
	s_and_b64 vcc, exec, s[2:3]
	v_cvt_pk_bf16_f32 v116, v116, v117
	v_cvt_pk_bf16_f32 v117, v118, v119
	v_cvt_pk_bf16_f32 v118, v112, v113
	v_cvt_pk_bf16_f32 v119, v114, v115
	global_store_dwordx4 v[138:139], v[116:119], off offset:256
	s_cbranch_vccnz .LBB0_1289
	v_mul_f32_e32 v113, 0x3d372713, v104
	v_mul_f32_e32 v113, v104, v113
	v_mul_f32_e32 v114, 0x3d372713, v109
	v_fma_f32 v113, v104, v113, v104
	v_mul_f32_e32 v114, v109, v114
	v_mul_f32_e32 v113, 0xbfcc422a, v113
	v_fma_f32 v114, v109, v114, v109
	v_mul_f32_e32 v113, 0x3fb8aa3b, v113
	v_mul_f32_e32 v114, 0xbfcc422a, v114
	v_exp_f32_e32 v113, v113
	v_mul_f32_e32 v114, 0x3fb8aa3b, v114
	v_mul_f32_e32 v118, 0x3d372713, v111
	v_exp_f32_e32 v115, v114
	v_mul_f32_e32 v118, v111, v118
	v_fma_f32 v118, v111, v118, v111
	v_mul_f32_e32 v118, 0xbfcc422a, v118
	v_add_f32_e32 v113, 1.0, v113
	v_mul_f32_e32 v117, 0x3d372713, v106
	v_mul_f32_e32 v118, 0x3fb8aa3b, v118
	v_mul_f32_e32 v112, 0x3d372713, v108
	v_rcp_f32_e32 v114, v113
	v_add_f32_e32 v113, 1.0, v115
	v_mul_f32_e32 v115, 0x3d372713, v105
	v_mul_f32_e32 v116, 0x3d372713, v110
	v_mul_f32_e32 v117, v106, v117
	v_exp_f32_e32 v119, v118
	v_mul_f32_e32 v118, 0x3d372713, v107
	v_mul_f32_e32 v112, v108, v112
	v_mul_f32_e32 v115, v105, v115
	v_mul_f32_e32 v116, v110, v116
	v_fma_f32 v117, v106, v117, v106
	v_mul_f32_e32 v118, v107, v118
	v_fma_f32 v112, v108, v112, v108
	v_fma_f32 v115, v105, v115, v105
	v_fma_f32 v116, v110, v116, v110
	v_mul_f32_e32 v117, 0xbfcc422a, v117
	v_fma_f32 v118, v107, v118, v107
	v_mul_f32_e32 v112, 0xbfcc422a, v112
	v_mul_f32_e32 v115, 0xbfcc422a, v115
	v_mul_f32_e32 v116, 0xbfcc422a, v116
	v_mul_f32_e32 v117, 0x3fb8aa3b, v117
	v_mul_f32_e32 v118, 0xbfcc422a, v118
	v_mul_f32_e32 v112, 0x3fb8aa3b, v112
	v_mul_f32_e32 v115, 0x3fb8aa3b, v115
	v_mul_f32_e32 v116, 0x3fb8aa3b, v116
	v_exp_f32_e32 v117, v117
	v_mul_f32_e32 v118, 0x3fb8aa3b, v118
	v_exp_f32_e32 v112, v112
	v_exp_f32_e32 v115, v115
	v_exp_f32_e32 v116, v116
	v_exp_f32_e32 v120, v118
	v_add_f32_e32 v117, 1.0, v117
	v_add_f32_e32 v112, 1.0, v112
	v_add_f32_e32 v115, 1.0, v115
	v_add_f32_e32 v116, 1.0, v116
	v_rcp_f32_e32 v118, v117
	v_add_f32_e32 v117, 1.0, v119
	v_add_f32_e32 v119, 1.0, v120
	v_rcp_f32_e32 v112, v112
	v_rcp_f32_e32 v113, v113
	v_rcp_f32_e32 v116, v116
	v_rcp_f32_e32 v117, v117
	v_rcp_f32_e32 v119, v119
	v_rcp_f32_e32 v115, v115
	v_mul_f32_e64 v108, v108, v112
	v_mul_f32_e64 v109, v109, v113
	v_mul_f32_e64 v110, v110, v116
	v_mul_f32_e64 v111, v111, v117
	v_mul_f32_e64 v106, v106, v118
	v_mul_f32_e64 v107, v107, v119
	v_mul_f32_e64 v104, v104, v114
	v_mul_f32_e64 v105, v105, v115
.LBB0_1289:
	v_or_b32_e32 v112, 16, v134
	v_ashrrev_i32_e32 v113, 31, v112
	v_lshlrev_b64 v[112:113], 11, v[112:113]
	v_lshl_add_u64 v[112:113], v[136:137], 0, v[112:113]
	s_and_b64 vcc, exec, s[2:3]
	v_cvt_pk_bf16_f32 v108, v108, v109
	v_cvt_pk_bf16_f32 v109, v110, v111
	v_cvt_pk_bf16_f32 v110, v104, v105
	v_cvt_pk_bf16_f32 v111, v106, v107
	global_store_dwordx4 v[112:113], v[108:111], off
	s_cbranch_vccnz .LBB0_1291
	v_mul_f32_e32 v105, 0x3d372713, v96
	v_mul_f32_e32 v105, v96, v105
	v_mul_f32_e32 v106, 0x3d372713, v101
	v_fma_f32 v105, v96, v105, v96
	v_mul_f32_e32 v106, v101, v106
	v_mul_f32_e32 v105, 0xbfcc422a, v105
	v_fma_f32 v106, v101, v106, v101
	v_mul_f32_e32 v105, 0x3fb8aa3b, v105
	v_mul_f32_e32 v106, 0xbfcc422a, v106
	v_exp_f32_e32 v105, v105
	v_mul_f32_e32 v106, 0x3fb8aa3b, v106
	v_mul_f32_e32 v110, 0x3d372713, v103
	v_exp_f32_e32 v107, v106
	v_mul_f32_e32 v110, v103, v110
	v_fma_f32 v110, v103, v110, v103
	v_mul_f32_e32 v110, 0xbfcc422a, v110
	v_add_f32_e32 v105, 1.0, v105
	v_mul_f32_e32 v109, 0x3d372713, v98
	v_mul_f32_e32 v110, 0x3fb8aa3b, v110
	v_mul_f32_e32 v104, 0x3d372713, v100
	v_rcp_f32_e32 v106, v105
	v_add_f32_e32 v105, 1.0, v107
	v_mul_f32_e32 v107, 0x3d372713, v97
	v_mul_f32_e32 v108, 0x3d372713, v102
	v_mul_f32_e32 v109, v98, v109
	v_exp_f32_e32 v111, v110
	v_mul_f32_e32 v110, 0x3d372713, v99
	v_mul_f32_e32 v104, v100, v104
	v_mul_f32_e32 v107, v97, v107
	v_mul_f32_e32 v108, v102, v108
	v_fma_f32 v109, v98, v109, v98
	v_mul_f32_e32 v110, v99, v110
	v_fma_f32 v104, v100, v104, v100
	v_fma_f32 v107, v97, v107, v97
	v_fma_f32 v108, v102, v108, v102
	v_mul_f32_e32 v109, 0xbfcc422a, v109
	v_fma_f32 v110, v99, v110, v99
	v_mul_f32_e32 v104, 0xbfcc422a, v104
	v_mul_f32_e32 v107, 0xbfcc422a, v107
	v_mul_f32_e32 v108, 0xbfcc422a, v108
	v_mul_f32_e32 v109, 0x3fb8aa3b, v109
	v_mul_f32_e32 v110, 0xbfcc422a, v110
	v_mul_f32_e32 v104, 0x3fb8aa3b, v104
	v_mul_f32_e32 v107, 0x3fb8aa3b, v107
	v_mul_f32_e32 v108, 0x3fb8aa3b, v108
	v_exp_f32_e32 v109, v109
	v_mul_f32_e32 v110, 0x3fb8aa3b, v110
	v_exp_f32_e32 v104, v104
	v_exp_f32_e32 v107, v107
	v_exp_f32_e32 v108, v108
	v_exp_f32_e32 v114, v110
	v_add_f32_e32 v109, 1.0, v109
	v_add_f32_e32 v104, 1.0, v104
	v_add_f32_e32 v107, 1.0, v107
	v_add_f32_e32 v108, 1.0, v108
	v_rcp_f32_e32 v110, v109
	v_add_f32_e32 v109, 1.0, v111
	v_add_f32_e32 v111, 1.0, v114
	v_rcp_f32_e32 v104, v104
	v_rcp_f32_e32 v105, v105
	v_rcp_f32_e32 v108, v108
	v_rcp_f32_e32 v109, v109
	v_rcp_f32_e32 v111, v111
	v_rcp_f32_e32 v107, v107
	v_mul_f32_e64 v100, v100, v104
	v_mul_f32_e64 v101, v101, v105
	v_mul_f32_e64 v102, v102, v108
	v_mul_f32_e64 v103, v103, v109
	v_mul_f32_e64 v98, v98, v110
	v_mul_f32_e64 v99, v99, v111
	v_mul_f32_e64 v96, v96, v106
	v_mul_f32_e64 v97, v97, v107
.LBB0_1291:
	s_and_b64 vcc, exec, s[2:3]
	v_cvt_pk_bf16_f32 v100, v100, v101
	v_cvt_pk_bf16_f32 v101, v102, v103
	v_cvt_pk_bf16_f32 v102, v96, v97
	v_cvt_pk_bf16_f32 v103, v98, v99
	global_store_dwordx4 v[112:113], v[100:103], off offset:256
	s_cbranch_vccnz .LBB0_1293
	v_mul_f32_e32 v97, 0x3d372713, v88
	v_mul_f32_e32 v97, v88, v97
	v_mul_f32_e32 v98, 0x3d372713, v93
	v_fma_f32 v97, v88, v97, v88
	v_mul_f32_e32 v98, v93, v98
	v_mul_f32_e32 v97, 0xbfcc422a, v97
	v_fma_f32 v98, v93, v98, v93
	v_mul_f32_e32 v97, 0x3fb8aa3b, v97
	v_mul_f32_e32 v98, 0xbfcc422a, v98
	v_exp_f32_e32 v97, v97
	v_mul_f32_e32 v98, 0x3fb8aa3b, v98
	v_mul_f32_e32 v102, 0x3d372713, v95
	v_exp_f32_e32 v99, v98
	v_mul_f32_e32 v102, v95, v102
	v_fma_f32 v102, v95, v102, v95
	v_mul_f32_e32 v102, 0xbfcc422a, v102
	v_add_f32_e32 v97, 1.0, v97
	v_mul_f32_e32 v101, 0x3d372713, v90
	v_mul_f32_e32 v102, 0x3fb8aa3b, v102
	v_mul_f32_e32 v96, 0x3d372713, v92
	v_rcp_f32_e32 v98, v97
	v_add_f32_e32 v97, 1.0, v99
	v_mul_f32_e32 v99, 0x3d372713, v89
	v_mul_f32_e32 v100, 0x3d372713, v94
	v_mul_f32_e32 v101, v90, v101
	v_exp_f32_e32 v103, v102
	v_mul_f32_e32 v102, 0x3d372713, v91
	v_mul_f32_e32 v96, v92, v96
	v_mul_f32_e32 v99, v89, v99
	v_mul_f32_e32 v100, v94, v100
	v_fma_f32 v101, v90, v101, v90
	v_mul_f32_e32 v102, v91, v102
	v_fma_f32 v96, v92, v96, v92
	v_fma_f32 v99, v89, v99, v89
	v_fma_f32 v100, v94, v100, v94
	v_mul_f32_e32 v101, 0xbfcc422a, v101
	v_fma_f32 v102, v91, v102, v91
	v_mul_f32_e32 v96, 0xbfcc422a, v96
	v_mul_f32_e32 v99, 0xbfcc422a, v99
	v_mul_f32_e32 v100, 0xbfcc422a, v100
	v_mul_f32_e32 v101, 0x3fb8aa3b, v101
	v_mul_f32_e32 v102, 0xbfcc422a, v102
	v_mul_f32_e32 v96, 0x3fb8aa3b, v96
	v_mul_f32_e32 v99, 0x3fb8aa3b, v99
	v_mul_f32_e32 v100, 0x3fb8aa3b, v100
	v_exp_f32_e32 v101, v101
	v_mul_f32_e32 v102, 0x3fb8aa3b, v102
	v_exp_f32_e32 v96, v96
	v_exp_f32_e32 v99, v99
	v_exp_f32_e32 v100, v100
	v_exp_f32_e32 v104, v102
	v_add_f32_e32 v101, 1.0, v101
	v_add_f32_e32 v96, 1.0, v96
	v_add_f32_e32 v99, 1.0, v99
	v_add_f32_e32 v100, 1.0, v100
	v_rcp_f32_e32 v102, v101
	v_add_f32_e32 v101, 1.0, v103
	v_add_f32_e32 v103, 1.0, v104
	v_rcp_f32_e32 v96, v96
	v_rcp_f32_e32 v97, v97
	v_rcp_f32_e32 v100, v100
	v_rcp_f32_e32 v101, v101
	v_rcp_f32_e32 v103, v103
	v_rcp_f32_e32 v99, v99
	v_mul_f32_e64 v92, v92, v96
	v_mul_f32_e64 v93, v93, v97
	v_mul_f32_e64 v94, v94, v100
	v_mul_f32_e64 v95, v95, v101
	v_mul_f32_e64 v90, v90, v102
	v_mul_f32_e64 v91, v91, v103
	v_mul_f32_e64 v88, v88, v98
	v_mul_f32_e64 v89, v89, v99
.LBB0_1293:
	v_or_b32_e32 v96, 32, v134
	v_ashrrev_i32_e32 v97, 31, v96
	v_lshlrev_b64 v[96:97], 11, v[96:97]
	v_lshl_add_u64 v[96:97], v[136:137], 0, v[96:97]
	s_and_b64 vcc, exec, s[2:3]
	v_cvt_pk_bf16_f32 v92, v92, v93
	v_cvt_pk_bf16_f32 v93, v94, v95
	v_cvt_pk_bf16_f32 v94, v88, v89
	v_cvt_pk_bf16_f32 v95, v90, v91
	global_store_dwordx4 v[96:97], v[92:95], off
	s_cbranch_vccnz .LBB0_1295
	v_mul_f32_e32 v89, 0x3d372713, v80
	v_mul_f32_e32 v89, v80, v89
	v_mul_f32_e32 v90, 0x3d372713, v85
	v_fma_f32 v89, v80, v89, v80
	v_mul_f32_e32 v90, v85, v90
	v_mul_f32_e32 v89, 0xbfcc422a, v89
	v_fma_f32 v90, v85, v90, v85
	v_mul_f32_e32 v89, 0x3fb8aa3b, v89
	v_mul_f32_e32 v90, 0xbfcc422a, v90
	v_exp_f32_e32 v89, v89
	v_mul_f32_e32 v90, 0x3fb8aa3b, v90
	v_mul_f32_e32 v94, 0x3d372713, v87
	v_exp_f32_e32 v91, v90
	v_mul_f32_e32 v94, v87, v94
	v_fma_f32 v94, v87, v94, v87
	v_mul_f32_e32 v94, 0xbfcc422a, v94
	v_add_f32_e32 v89, 1.0, v89
	v_mul_f32_e32 v93, 0x3d372713, v82
	v_mul_f32_e32 v94, 0x3fb8aa3b, v94
	v_mul_f32_e32 v88, 0x3d372713, v84
	v_rcp_f32_e32 v90, v89
	v_add_f32_e32 v89, 1.0, v91
	v_mul_f32_e32 v91, 0x3d372713, v81
	v_mul_f32_e32 v92, 0x3d372713, v86
	v_mul_f32_e32 v93, v82, v93
	v_exp_f32_e32 v95, v94
	v_mul_f32_e32 v94, 0x3d372713, v83
	v_mul_f32_e32 v88, v84, v88
	v_mul_f32_e32 v91, v81, v91
	v_mul_f32_e32 v92, v86, v92
	v_fma_f32 v93, v82, v93, v82
	v_mul_f32_e32 v94, v83, v94
	v_fma_f32 v88, v84, v88, v84
	v_fma_f32 v91, v81, v91, v81
	v_fma_f32 v92, v86, v92, v86
	v_mul_f32_e32 v93, 0xbfcc422a, v93
	v_fma_f32 v94, v83, v94, v83
	v_mul_f32_e32 v88, 0xbfcc422a, v88
	v_mul_f32_e32 v91, 0xbfcc422a, v91
	v_mul_f32_e32 v92, 0xbfcc422a, v92
	v_mul_f32_e32 v93, 0x3fb8aa3b, v93
	v_mul_f32_e32 v94, 0xbfcc422a, v94
	v_mul_f32_e32 v88, 0x3fb8aa3b, v88
	v_mul_f32_e32 v91, 0x3fb8aa3b, v91
	v_mul_f32_e32 v92, 0x3fb8aa3b, v92
	v_exp_f32_e32 v93, v93
	v_mul_f32_e32 v94, 0x3fb8aa3b, v94
	v_exp_f32_e32 v88, v88
	v_exp_f32_e32 v91, v91
	v_exp_f32_e32 v92, v92
	v_exp_f32_e32 v98, v94
	v_add_f32_e32 v93, 1.0, v93
	v_add_f32_e32 v88, 1.0, v88
	v_add_f32_e32 v91, 1.0, v91
	v_add_f32_e32 v92, 1.0, v92
	v_rcp_f32_e32 v94, v93
	v_add_f32_e32 v93, 1.0, v95
	v_add_f32_e32 v95, 1.0, v98
	v_rcp_f32_e32 v88, v88
	v_rcp_f32_e32 v89, v89
	v_rcp_f32_e32 v92, v92
	v_rcp_f32_e32 v93, v93
	v_rcp_f32_e32 v95, v95
	v_rcp_f32_e32 v91, v91
	v_mul_f32_e64 v84, v84, v88
	v_mul_f32_e64 v85, v85, v89
	v_mul_f32_e64 v86, v86, v92
	v_mul_f32_e64 v87, v87, v93
	v_mul_f32_e64 v82, v82, v94
	v_mul_f32_e64 v83, v83, v95
	v_mul_f32_e64 v80, v80, v90
	v_mul_f32_e64 v81, v81, v91
.LBB0_1295:
	s_and_b64 vcc, exec, s[2:3]
	v_cvt_pk_bf16_f32 v84, v84, v85
	v_cvt_pk_bf16_f32 v85, v86, v87
	v_cvt_pk_bf16_f32 v86, v80, v81
	v_cvt_pk_bf16_f32 v87, v82, v83
	global_store_dwordx4 v[96:97], v[84:87], off offset:256
	s_cbranch_vccnz .LBB0_1297
	v_mul_f32_e32 v81, 0x3d372713, v72
	v_mul_f32_e32 v81, v72, v81
	v_mul_f32_e32 v82, 0x3d372713, v77
	v_fma_f32 v81, v72, v81, v72
	v_mul_f32_e32 v82, v77, v82
	v_mul_f32_e32 v81, 0xbfcc422a, v81
	v_fma_f32 v82, v77, v82, v77
	v_mul_f32_e32 v81, 0x3fb8aa3b, v81
	v_mul_f32_e32 v82, 0xbfcc422a, v82
	v_exp_f32_e32 v81, v81
	v_mul_f32_e32 v82, 0x3fb8aa3b, v82
	v_mul_f32_e32 v86, 0x3d372713, v79
	v_exp_f32_e32 v83, v82
	v_mul_f32_e32 v86, v79, v86
	v_fma_f32 v86, v79, v86, v79
	v_mul_f32_e32 v86, 0xbfcc422a, v86
	v_add_f32_e32 v81, 1.0, v81
	v_mul_f32_e32 v85, 0x3d372713, v74
	v_mul_f32_e32 v86, 0x3fb8aa3b, v86
	v_mul_f32_e32 v80, 0x3d372713, v76
	v_rcp_f32_e32 v82, v81
	v_add_f32_e32 v81, 1.0, v83
	v_mul_f32_e32 v83, 0x3d372713, v73
	v_mul_f32_e32 v84, 0x3d372713, v78
	v_mul_f32_e32 v85, v74, v85
	v_exp_f32_e32 v87, v86
	v_mul_f32_e32 v86, 0x3d372713, v75
	v_mul_f32_e32 v80, v76, v80
	v_mul_f32_e32 v83, v73, v83
	v_mul_f32_e32 v84, v78, v84
	v_fma_f32 v85, v74, v85, v74
	v_mul_f32_e32 v86, v75, v86
	v_fma_f32 v80, v76, v80, v76
	v_fma_f32 v83, v73, v83, v73
	v_fma_f32 v84, v78, v84, v78
	v_mul_f32_e32 v85, 0xbfcc422a, v85
	v_fma_f32 v86, v75, v86, v75
	v_mul_f32_e32 v80, 0xbfcc422a, v80
	v_mul_f32_e32 v83, 0xbfcc422a, v83
	v_mul_f32_e32 v84, 0xbfcc422a, v84
	v_mul_f32_e32 v85, 0x3fb8aa3b, v85
	v_mul_f32_e32 v86, 0xbfcc422a, v86
	v_mul_f32_e32 v80, 0x3fb8aa3b, v80
	v_mul_f32_e32 v83, 0x3fb8aa3b, v83
	v_mul_f32_e32 v84, 0x3fb8aa3b, v84
	v_exp_f32_e32 v85, v85
	v_mul_f32_e32 v86, 0x3fb8aa3b, v86
	v_exp_f32_e32 v80, v80
	v_exp_f32_e32 v83, v83
	v_exp_f32_e32 v84, v84
	v_exp_f32_e32 v88, v86
	v_add_f32_e32 v85, 1.0, v85
	v_add_f32_e32 v80, 1.0, v80
	v_add_f32_e32 v83, 1.0, v83
	v_add_f32_e32 v84, 1.0, v84
	v_rcp_f32_e32 v86, v85
	v_add_f32_e32 v85, 1.0, v87
	v_add_f32_e32 v87, 1.0, v88
	v_rcp_f32_e32 v80, v80
	v_rcp_f32_e32 v81, v81
	v_rcp_f32_e32 v84, v84
	v_rcp_f32_e32 v85, v85
	v_rcp_f32_e32 v87, v87
	v_rcp_f32_e32 v83, v83
	v_mul_f32_e64 v76, v76, v80
	v_mul_f32_e64 v77, v77, v81
	v_mul_f32_e64 v78, v78, v84
	v_mul_f32_e64 v79, v79, v85
	v_mul_f32_e64 v74, v74, v86
	v_mul_f32_e64 v75, v75, v87
	v_mul_f32_e64 v72, v72, v82
	v_mul_f32_e64 v73, v73, v83
.LBB0_1297:
	v_or_b32_e32 v80, 48, v134
	v_ashrrev_i32_e32 v81, 31, v80
	v_lshlrev_b64 v[80:81], 11, v[80:81]
	v_lshl_add_u64 v[80:81], v[136:137], 0, v[80:81]
	s_and_b64 vcc, exec, s[2:3]
	v_cvt_pk_bf16_f32 v76, v76, v77
	v_cvt_pk_bf16_f32 v77, v78, v79
	v_cvt_pk_bf16_f32 v78, v72, v73
	v_cvt_pk_bf16_f32 v79, v74, v75
	global_store_dwordx4 v[80:81], v[76:79], off
	s_cbranch_vccnz .LBB0_1299
	v_mul_f32_e32 v73, 0x3d372713, v64
	v_mul_f32_e32 v73, v64, v73
	v_mul_f32_e32 v74, 0x3d372713, v69
	v_fma_f32 v73, v64, v73, v64
	v_mul_f32_e32 v74, v69, v74
	v_mul_f32_e32 v73, 0xbfcc422a, v73
	v_fma_f32 v74, v69, v74, v69
	v_mul_f32_e32 v73, 0x3fb8aa3b, v73
	v_mul_f32_e32 v74, 0xbfcc422a, v74
	v_exp_f32_e32 v73, v73
	v_mul_f32_e32 v74, 0x3fb8aa3b, v74
	v_mul_f32_e32 v78, 0x3d372713, v71
	v_exp_f32_e32 v75, v74
	v_mul_f32_e32 v78, v71, v78
	v_fma_f32 v78, v71, v78, v71
	v_mul_f32_e32 v78, 0xbfcc422a, v78
	v_add_f32_e32 v73, 1.0, v73
	v_mul_f32_e32 v77, 0x3d372713, v66
	v_mul_f32_e32 v78, 0x3fb8aa3b, v78
	v_mul_f32_e32 v72, 0x3d372713, v68
	v_rcp_f32_e32 v74, v73
	v_add_f32_e32 v73, 1.0, v75
	v_mul_f32_e32 v75, 0x3d372713, v65
	v_mul_f32_e32 v76, 0x3d372713, v70
	v_mul_f32_e32 v77, v66, v77
	v_exp_f32_e32 v79, v78
	v_mul_f32_e32 v78, 0x3d372713, v67
	v_mul_f32_e32 v72, v68, v72
	v_mul_f32_e32 v75, v65, v75
	v_mul_f32_e32 v76, v70, v76
	v_fma_f32 v77, v66, v77, v66
	v_mul_f32_e32 v78, v67, v78
	v_fma_f32 v72, v68, v72, v68
	v_fma_f32 v75, v65, v75, v65
	v_fma_f32 v76, v70, v76, v70
	v_mul_f32_e32 v77, 0xbfcc422a, v77
	v_fma_f32 v78, v67, v78, v67
	v_mul_f32_e32 v72, 0xbfcc422a, v72
	v_mul_f32_e32 v75, 0xbfcc422a, v75
	v_mul_f32_e32 v76, 0xbfcc422a, v76
	v_mul_f32_e32 v77, 0x3fb8aa3b, v77
	v_mul_f32_e32 v78, 0xbfcc422a, v78
	v_mul_f32_e32 v72, 0x3fb8aa3b, v72
	v_mul_f32_e32 v75, 0x3fb8aa3b, v75
	v_mul_f32_e32 v76, 0x3fb8aa3b, v76
	v_exp_f32_e32 v77, v77
	v_mul_f32_e32 v78, 0x3fb8aa3b, v78
	v_exp_f32_e32 v72, v72
	v_exp_f32_e32 v75, v75
	v_exp_f32_e32 v76, v76
	v_exp_f32_e32 v82, v78
	v_add_f32_e32 v77, 1.0, v77
	v_add_f32_e32 v72, 1.0, v72
	v_add_f32_e32 v75, 1.0, v75
	v_add_f32_e32 v76, 1.0, v76
	v_rcp_f32_e32 v78, v77
	v_add_f32_e32 v77, 1.0, v79
	v_add_f32_e32 v79, 1.0, v82
	v_rcp_f32_e32 v72, v72
	v_rcp_f32_e32 v73, v73
	v_rcp_f32_e32 v76, v76
	v_rcp_f32_e32 v77, v77
	v_rcp_f32_e32 v79, v79
	v_rcp_f32_e32 v75, v75
	v_mul_f32_e64 v68, v68, v72
	v_mul_f32_e64 v69, v69, v73
	v_mul_f32_e64 v70, v70, v76
	v_mul_f32_e64 v71, v71, v77
	v_mul_f32_e64 v66, v66, v78
	v_mul_f32_e64 v67, v67, v79
	v_mul_f32_e64 v64, v64, v74
	v_mul_f32_e64 v65, v65, v75
.LBB0_1299:
	s_and_b64 vcc, exec, s[2:3]
	v_cvt_pk_bf16_f32 v68, v68, v69
	v_cvt_pk_bf16_f32 v69, v70, v71
	v_cvt_pk_bf16_f32 v70, v64, v65
	v_cvt_pk_bf16_f32 v71, v66, v67
	global_store_dwordx4 v[80:81], v[68:71], off offset:256
	s_cbranch_vccnz .LBB0_1301
	v_mul_f32_e32 v65, 0x3d372713, v56
	v_mul_f32_e32 v65, v56, v65
	v_mul_f32_e32 v66, 0x3d372713, v61
	v_fma_f32 v65, v56, v65, v56
	v_mul_f32_e32 v66, v61, v66
	v_mul_f32_e32 v65, 0xbfcc422a, v65
	v_fma_f32 v66, v61, v66, v61
	v_mul_f32_e32 v65, 0x3fb8aa3b, v65
	v_mul_f32_e32 v66, 0xbfcc422a, v66
	v_exp_f32_e32 v65, v65
	v_mul_f32_e32 v66, 0x3fb8aa3b, v66
	v_mul_f32_e32 v70, 0x3d372713, v63
	v_exp_f32_e32 v67, v66
	v_mul_f32_e32 v70, v63, v70
	v_fma_f32 v70, v63, v70, v63
	v_mul_f32_e32 v70, 0xbfcc422a, v70
	v_add_f32_e32 v65, 1.0, v65
	v_mul_f32_e32 v69, 0x3d372713, v58
	v_mul_f32_e32 v70, 0x3fb8aa3b, v70
	v_mul_f32_e32 v64, 0x3d372713, v60
	v_rcp_f32_e32 v66, v65
	v_add_f32_e32 v65, 1.0, v67
	v_mul_f32_e32 v67, 0x3d372713, v57
	v_mul_f32_e32 v68, 0x3d372713, v62
	v_mul_f32_e32 v69, v58, v69
	v_exp_f32_e32 v71, v70
	v_mul_f32_e32 v70, 0x3d372713, v59
	v_mul_f32_e32 v64, v60, v64
	v_mul_f32_e32 v67, v57, v67
	v_mul_f32_e32 v68, v62, v68
	v_fma_f32 v69, v58, v69, v58
	v_mul_f32_e32 v70, v59, v70
	v_fma_f32 v64, v60, v64, v60
	v_fma_f32 v67, v57, v67, v57
	v_fma_f32 v68, v62, v68, v62
	v_mul_f32_e32 v69, 0xbfcc422a, v69
	v_fma_f32 v70, v59, v70, v59
	v_mul_f32_e32 v64, 0xbfcc422a, v64
	v_mul_f32_e32 v67, 0xbfcc422a, v67
	v_mul_f32_e32 v68, 0xbfcc422a, v68
	v_mul_f32_e32 v69, 0x3fb8aa3b, v69
	v_mul_f32_e32 v70, 0xbfcc422a, v70
	v_mul_f32_e32 v64, 0x3fb8aa3b, v64
	v_mul_f32_e32 v67, 0x3fb8aa3b, v67
	v_mul_f32_e32 v68, 0x3fb8aa3b, v68
	v_exp_f32_e32 v69, v69
	v_mul_f32_e32 v70, 0x3fb8aa3b, v70
	v_exp_f32_e32 v64, v64
	v_exp_f32_e32 v67, v67
	v_exp_f32_e32 v68, v68
	v_exp_f32_e32 v72, v70
	v_add_f32_e32 v69, 1.0, v69
	v_add_f32_e32 v64, 1.0, v64
	v_add_f32_e32 v67, 1.0, v67
	v_add_f32_e32 v68, 1.0, v68
	v_rcp_f32_e32 v70, v69
	v_add_f32_e32 v69, 1.0, v71
	v_add_f32_e32 v71, 1.0, v72
	v_rcp_f32_e32 v64, v64
	v_rcp_f32_e32 v65, v65
	v_rcp_f32_e32 v68, v68
	v_rcp_f32_e32 v69, v69
	v_rcp_f32_e32 v71, v71
	v_rcp_f32_e32 v67, v67
	v_mul_f32_e64 v60, v60, v64
	v_mul_f32_e64 v61, v61, v65
	v_mul_f32_e64 v62, v62, v68
	v_mul_f32_e64 v63, v63, v69
	v_mul_f32_e64 v58, v58, v70
	v_mul_f32_e64 v59, v59, v71
	v_mul_f32_e64 v56, v56, v66
	v_mul_f32_e64 v57, v57, v67
.LBB0_1301:
	v_lshlrev_b64 v[64:65], 11, v[134:135]
	v_lshl_add_u64 v[64:65], v[136:137], 0, v[64:65]
	v_cvt_pk_bf16_f32 v60, v60, v61
	v_cvt_pk_bf16_f32 v61, v62, v63
	v_cvt_pk_bf16_f32 v62, v56, v57
	v_add_co_u32_e32 v56, vcc, 0x40000, v64
	v_cvt_pk_bf16_f32 v63, v58, v59
	s_nop 1
	v_addc_co_u32_e32 v57, vcc, 0, v65, vcc
	s_and_b64 vcc, exec, s[2:3]
	global_store_dwordx4 v[56:57], v[60:63], off
	s_cbranch_vccnz .LBB0_1303
	v_mul_f32_e32 v57, 0x3d372713, v48
	v_mul_f32_e32 v57, v48, v57
	v_mul_f32_e32 v58, 0x3d372713, v53
	v_fma_f32 v57, v48, v57, v48
	v_mul_f32_e32 v58, v53, v58
	v_mul_f32_e32 v57, 0xbfcc422a, v57
	v_fma_f32 v58, v53, v58, v53
	v_mul_f32_e32 v57, 0x3fb8aa3b, v57
	v_mul_f32_e32 v58, 0xbfcc422a, v58
	v_exp_f32_e32 v57, v57
	v_mul_f32_e32 v58, 0x3fb8aa3b, v58
	v_mul_f32_e32 v62, 0x3d372713, v55
	v_exp_f32_e32 v59, v58
	v_mul_f32_e32 v62, v55, v62
	v_fma_f32 v62, v55, v62, v55
	v_mul_f32_e32 v62, 0xbfcc422a, v62
	v_add_f32_e32 v57, 1.0, v57
	v_mul_f32_e32 v61, 0x3d372713, v50
	v_mul_f32_e32 v62, 0x3fb8aa3b, v62
	v_mul_f32_e32 v56, 0x3d372713, v52
	v_rcp_f32_e32 v58, v57
	v_add_f32_e32 v57, 1.0, v59
	v_mul_f32_e32 v59, 0x3d372713, v49
	v_mul_f32_e32 v60, 0x3d372713, v54
	v_mul_f32_e32 v61, v50, v61
	v_exp_f32_e32 v63, v62
	v_mul_f32_e32 v62, 0x3d372713, v51
	v_mul_f32_e32 v56, v52, v56
	v_mul_f32_e32 v59, v49, v59
	v_mul_f32_e32 v60, v54, v60
	v_fma_f32 v61, v50, v61, v50
	v_mul_f32_e32 v62, v51, v62
	v_fma_f32 v56, v52, v56, v52
	v_fma_f32 v59, v49, v59, v49
	v_fma_f32 v60, v54, v60, v54
	v_mul_f32_e32 v61, 0xbfcc422a, v61
	v_fma_f32 v62, v51, v62, v51
	v_mul_f32_e32 v56, 0xbfcc422a, v56
	v_mul_f32_e32 v59, 0xbfcc422a, v59
	v_mul_f32_e32 v60, 0xbfcc422a, v60
	v_mul_f32_e32 v61, 0x3fb8aa3b, v61
	v_mul_f32_e32 v62, 0xbfcc422a, v62
	v_mul_f32_e32 v56, 0x3fb8aa3b, v56
	v_mul_f32_e32 v59, 0x3fb8aa3b, v59
	v_mul_f32_e32 v60, 0x3fb8aa3b, v60
	v_exp_f32_e32 v61, v61
	v_mul_f32_e32 v62, 0x3fb8aa3b, v62
	v_exp_f32_e32 v56, v56
	v_exp_f32_e32 v59, v59
	v_exp_f32_e32 v60, v60
	v_exp_f32_e32 v66, v62
	v_add_f32_e32 v61, 1.0, v61
	v_add_f32_e32 v56, 1.0, v56
	v_add_f32_e32 v59, 1.0, v59
	v_add_f32_e32 v60, 1.0, v60
	v_rcp_f32_e32 v62, v61
	v_add_f32_e32 v61, 1.0, v63
	v_add_f32_e32 v63, 1.0, v66
	v_rcp_f32_e32 v56, v56
	v_rcp_f32_e32 v57, v57
	v_rcp_f32_e32 v60, v60
	v_rcp_f32_e32 v61, v61
	v_rcp_f32_e32 v63, v63
	v_rcp_f32_e32 v59, v59
	v_mul_f32_e64 v52, v52, v56
	v_mul_f32_e64 v53, v53, v57
	v_mul_f32_e64 v54, v54, v60
	v_mul_f32_e64 v55, v55, v61
	v_mul_f32_e64 v50, v50, v62
	v_mul_f32_e64 v51, v51, v63
	v_mul_f32_e64 v48, v48, v58
	v_mul_f32_e64 v49, v49, v59
.LBB0_1303:
	v_lshl_add_u64 v[56:57], v[64:65], 0, s[10:11]
	s_and_b64 vcc, exec, s[2:3]
	v_cvt_pk_bf16_f32 v52, v52, v53
	v_cvt_pk_bf16_f32 v53, v54, v55
	v_cvt_pk_bf16_f32 v54, v48, v49
	v_cvt_pk_bf16_f32 v55, v50, v51
	global_store_dwordx4 v[56:57], v[52:55], off offset:256
	s_cbranch_vccnz .LBB0_1305
	v_mul_f32_e32 v49, 0x3d372713, v40
	v_mul_f32_e32 v49, v40, v49
	v_mul_f32_e32 v50, 0x3d372713, v45
	v_fma_f32 v49, v40, v49, v40
	v_mul_f32_e32 v50, v45, v50
	v_mul_f32_e32 v49, 0xbfcc422a, v49
	v_fma_f32 v50, v45, v50, v45
	v_mul_f32_e32 v49, 0x3fb8aa3b, v49
	v_mul_f32_e32 v50, 0xbfcc422a, v50
	v_exp_f32_e32 v49, v49
	v_mul_f32_e32 v50, 0x3fb8aa3b, v50
	v_mul_f32_e32 v54, 0x3d372713, v47
	v_exp_f32_e32 v51, v50
	v_mul_f32_e32 v54, v47, v54
	v_fma_f32 v54, v47, v54, v47
	v_mul_f32_e32 v54, 0xbfcc422a, v54
	v_add_f32_e32 v49, 1.0, v49
	v_mul_f32_e32 v53, 0x3d372713, v42
	v_mul_f32_e32 v54, 0x3fb8aa3b, v54
	v_mul_f32_e32 v48, 0x3d372713, v44
	v_rcp_f32_e32 v50, v49
	v_add_f32_e32 v49, 1.0, v51
	v_mul_f32_e32 v51, 0x3d372713, v41
	v_mul_f32_e32 v52, 0x3d372713, v46
	v_mul_f32_e32 v53, v42, v53
	v_exp_f32_e32 v55, v54
	v_mul_f32_e32 v54, 0x3d372713, v43
	v_mul_f32_e32 v48, v44, v48
	v_mul_f32_e32 v51, v41, v51
	v_mul_f32_e32 v52, v46, v52
	v_fma_f32 v53, v42, v53, v42
	v_mul_f32_e32 v54, v43, v54
	v_fma_f32 v48, v44, v48, v44
	v_fma_f32 v51, v41, v51, v41
	v_fma_f32 v52, v46, v52, v46
	v_mul_f32_e32 v53, 0xbfcc422a, v53
	v_fma_f32 v54, v43, v54, v43
	v_mul_f32_e32 v48, 0xbfcc422a, v48
	v_mul_f32_e32 v51, 0xbfcc422a, v51
	v_mul_f32_e32 v52, 0xbfcc422a, v52
	v_mul_f32_e32 v53, 0x3fb8aa3b, v53
	v_mul_f32_e32 v54, 0xbfcc422a, v54
	v_mul_f32_e32 v48, 0x3fb8aa3b, v48
	v_mul_f32_e32 v51, 0x3fb8aa3b, v51
	v_mul_f32_e32 v52, 0x3fb8aa3b, v52
	v_exp_f32_e32 v53, v53
	v_mul_f32_e32 v54, 0x3fb8aa3b, v54
	v_exp_f32_e32 v48, v48
	v_exp_f32_e32 v51, v51
	v_exp_f32_e32 v52, v52
	v_exp_f32_e32 v56, v54
	v_add_f32_e32 v53, 1.0, v53
	v_add_f32_e32 v48, 1.0, v48
	v_add_f32_e32 v51, 1.0, v51
	v_add_f32_e32 v52, 1.0, v52
	v_rcp_f32_e32 v54, v53
	v_add_f32_e32 v53, 1.0, v55
	v_add_f32_e32 v55, 1.0, v56
	v_rcp_f32_e32 v48, v48
	v_rcp_f32_e32 v49, v49
	v_rcp_f32_e32 v52, v52
	v_rcp_f32_e32 v53, v53
	v_rcp_f32_e32 v55, v55
	v_rcp_f32_e32 v51, v51
	v_mul_f32_e64 v44, v44, v48
	v_mul_f32_e64 v45, v45, v49
	v_mul_f32_e64 v46, v46, v52
	v_mul_f32_e64 v47, v47, v53
	v_mul_f32_e64 v42, v42, v54
	v_mul_f32_e64 v43, v43, v55
	v_mul_f32_e64 v40, v40, v50
	v_mul_f32_e64 v41, v41, v51
.LBB0_1305:
	v_lshlrev_b64 v[48:49], 11, v[134:135]
	v_lshl_add_u64 v[48:49], v[136:137], 0, v[48:49]
	v_cvt_pk_bf16_f32 v44, v44, v45
	v_cvt_pk_bf16_f32 v45, v46, v47
	v_cvt_pk_bf16_f32 v46, v40, v41
	v_add_co_u32_e32 v40, vcc, 0x48000, v48
	v_cvt_pk_bf16_f32 v47, v42, v43
	s_nop 1
	v_addc_co_u32_e32 v41, vcc, 0, v49, vcc
	s_and_b64 vcc, exec, s[2:3]
	global_store_dwordx4 v[40:41], v[44:47], off
	s_cbranch_vccnz .LBB0_1307
	v_mul_f32_e32 v41, 0x3d372713, v32
	v_mul_f32_e32 v41, v32, v41
	v_mul_f32_e32 v42, 0x3d372713, v37
	v_fma_f32 v41, v32, v41, v32
	v_mul_f32_e32 v42, v37, v42
	v_mul_f32_e32 v41, 0xbfcc422a, v41
	v_fma_f32 v42, v37, v42, v37
	v_mul_f32_e32 v41, 0x3fb8aa3b, v41
	v_mul_f32_e32 v42, 0xbfcc422a, v42
	v_exp_f32_e32 v41, v41
	v_mul_f32_e32 v42, 0x3fb8aa3b, v42
	v_mul_f32_e32 v46, 0x3d372713, v39
	v_exp_f32_e32 v43, v42
	v_mul_f32_e32 v46, v39, v46
	v_fma_f32 v46, v39, v46, v39
	v_mul_f32_e32 v46, 0xbfcc422a, v46
	v_add_f32_e32 v41, 1.0, v41
	v_mul_f32_e32 v45, 0x3d372713, v34
	v_mul_f32_e32 v46, 0x3fb8aa3b, v46
	v_mul_f32_e32 v40, 0x3d372713, v36
	v_rcp_f32_e32 v42, v41
	v_add_f32_e32 v41, 1.0, v43
	v_mul_f32_e32 v43, 0x3d372713, v33
	v_mul_f32_e32 v44, 0x3d372713, v38
	v_mul_f32_e32 v45, v34, v45
	v_exp_f32_e32 v47, v46
	v_mul_f32_e32 v46, 0x3d372713, v35
	v_mul_f32_e32 v40, v36, v40
	v_mul_f32_e32 v43, v33, v43
	v_mul_f32_e32 v44, v38, v44
	v_fma_f32 v45, v34, v45, v34
	v_mul_f32_e32 v46, v35, v46
	v_fma_f32 v40, v36, v40, v36
	v_fma_f32 v43, v33, v43, v33
	v_fma_f32 v44, v38, v44, v38
	v_mul_f32_e32 v45, 0xbfcc422a, v45
	v_fma_f32 v46, v35, v46, v35
	v_mul_f32_e32 v40, 0xbfcc422a, v40
	v_mul_f32_e32 v43, 0xbfcc422a, v43
	v_mul_f32_e32 v44, 0xbfcc422a, v44
	v_mul_f32_e32 v45, 0x3fb8aa3b, v45
	v_mul_f32_e32 v46, 0xbfcc422a, v46
	v_mul_f32_e32 v40, 0x3fb8aa3b, v40
	v_mul_f32_e32 v43, 0x3fb8aa3b, v43
	v_mul_f32_e32 v44, 0x3fb8aa3b, v44
	v_exp_f32_e32 v45, v45
	v_mul_f32_e32 v46, 0x3fb8aa3b, v46
	v_exp_f32_e32 v40, v40
	v_exp_f32_e32 v43, v43
	v_exp_f32_e32 v44, v44
	v_exp_f32_e32 v50, v46
	v_add_f32_e32 v45, 1.0, v45
	v_add_f32_e32 v40, 1.0, v40
	v_add_f32_e32 v43, 1.0, v43
	v_add_f32_e32 v44, 1.0, v44
	v_rcp_f32_e32 v46, v45
	v_add_f32_e32 v45, 1.0, v47
	v_add_f32_e32 v47, 1.0, v50
	v_rcp_f32_e32 v40, v40
	v_rcp_f32_e32 v41, v41
	v_rcp_f32_e32 v44, v44
	v_rcp_f32_e32 v45, v45
	v_rcp_f32_e32 v47, v47
	v_rcp_f32_e32 v43, v43
	v_mul_f32_e64 v36, v36, v40
	v_mul_f32_e64 v37, v37, v41
	v_mul_f32_e64 v38, v38, v44
	v_mul_f32_e64 v39, v39, v45
	v_mul_f32_e64 v34, v34, v46
	v_mul_f32_e64 v35, v35, v47
	v_mul_f32_e64 v32, v32, v42
	v_mul_f32_e64 v33, v33, v43
.LBB0_1307:
	v_lshl_add_u64 v[40:41], v[48:49], 0, s[14:15]
	s_and_b64 vcc, exec, s[2:3]
	v_cvt_pk_bf16_f32 v36, v36, v37
	v_cvt_pk_bf16_f32 v37, v38, v39
	v_cvt_pk_bf16_f32 v38, v32, v33
	v_cvt_pk_bf16_f32 v39, v34, v35
	global_store_dwordx4 v[40:41], v[36:39], off offset:256
	s_cbranch_vccnz .LBB0_1309
	v_mul_f32_e32 v33, 0x3d372713, v24
	v_mul_f32_e32 v33, v24, v33
	v_mul_f32_e32 v34, 0x3d372713, v29
	v_fma_f32 v33, v24, v33, v24
	v_mul_f32_e32 v34, v29, v34
	v_mul_f32_e32 v33, 0xbfcc422a, v33
	v_fma_f32 v34, v29, v34, v29
	v_mul_f32_e32 v33, 0x3fb8aa3b, v33
	v_mul_f32_e32 v34, 0xbfcc422a, v34
	v_exp_f32_e32 v33, v33
	v_mul_f32_e32 v34, 0x3fb8aa3b, v34
	v_mul_f32_e32 v38, 0x3d372713, v31
	v_exp_f32_e32 v35, v34
	v_mul_f32_e32 v38, v31, v38
	v_fma_f32 v38, v31, v38, v31
	v_mul_f32_e32 v38, 0xbfcc422a, v38
	v_add_f32_e32 v33, 1.0, v33
	v_mul_f32_e32 v37, 0x3d372713, v26
	v_mul_f32_e32 v38, 0x3fb8aa3b, v38
	v_mul_f32_e32 v32, 0x3d372713, v28
	v_rcp_f32_e32 v34, v33
	v_add_f32_e32 v33, 1.0, v35
	v_mul_f32_e32 v35, 0x3d372713, v25
	v_mul_f32_e32 v36, 0x3d372713, v30
	v_mul_f32_e32 v37, v26, v37
	v_exp_f32_e32 v39, v38
	v_mul_f32_e32 v38, 0x3d372713, v27
	v_mul_f32_e32 v32, v28, v32
	v_mul_f32_e32 v35, v25, v35
	v_mul_f32_e32 v36, v30, v36
	v_fma_f32 v37, v26, v37, v26
	v_mul_f32_e32 v38, v27, v38
	v_fma_f32 v32, v28, v32, v28
	v_fma_f32 v35, v25, v35, v25
	v_fma_f32 v36, v30, v36, v30
	v_mul_f32_e32 v37, 0xbfcc422a, v37
	v_fma_f32 v38, v27, v38, v27
	v_mul_f32_e32 v32, 0xbfcc422a, v32
	v_mul_f32_e32 v35, 0xbfcc422a, v35
	v_mul_f32_e32 v36, 0xbfcc422a, v36
	v_mul_f32_e32 v37, 0x3fb8aa3b, v37
	v_mul_f32_e32 v38, 0xbfcc422a, v38
	v_mul_f32_e32 v32, 0x3fb8aa3b, v32
	v_mul_f32_e32 v35, 0x3fb8aa3b, v35
	v_mul_f32_e32 v36, 0x3fb8aa3b, v36
	v_exp_f32_e32 v37, v37
	v_mul_f32_e32 v38, 0x3fb8aa3b, v38
	v_exp_f32_e32 v32, v32
	v_exp_f32_e32 v35, v35
	v_exp_f32_e32 v36, v36
	v_exp_f32_e32 v40, v38
	v_add_f32_e32 v37, 1.0, v37
	v_add_f32_e32 v32, 1.0, v32
	v_add_f32_e32 v35, 1.0, v35
	v_add_f32_e32 v36, 1.0, v36
	v_rcp_f32_e32 v38, v37
	v_add_f32_e32 v37, 1.0, v39
	v_add_f32_e32 v39, 1.0, v40
	v_rcp_f32_e32 v32, v32
	v_rcp_f32_e32 v33, v33
	v_rcp_f32_e32 v36, v36
	v_rcp_f32_e32 v37, v37
	v_rcp_f32_e32 v39, v39
	v_rcp_f32_e32 v35, v35
	v_mul_f32_e64 v28, v28, v32
	v_mul_f32_e64 v29, v29, v33
	v_mul_f32_e64 v30, v30, v36
	v_mul_f32_e64 v31, v31, v37
	v_mul_f32_e64 v26, v26, v38
	v_mul_f32_e64 v27, v27, v39
	v_mul_f32_e64 v24, v24, v34
	v_mul_f32_e64 v25, v25, v35
.LBB0_1309:
	v_lshlrev_b64 v[32:33], 11, v[134:135]
	v_lshl_add_u64 v[32:33], v[136:137], 0, v[32:33]
	v_cvt_pk_bf16_f32 v28, v28, v29
	v_cvt_pk_bf16_f32 v29, v30, v31
	v_cvt_pk_bf16_f32 v30, v24, v25
	v_add_co_u32_e32 v24, vcc, 0x50000, v32
	v_cvt_pk_bf16_f32 v31, v26, v27
	s_nop 1
	v_addc_co_u32_e32 v25, vcc, 0, v33, vcc
	s_and_b64 vcc, exec, s[2:3]
	global_store_dwordx4 v[24:25], v[28:31], off
	s_cbranch_vccnz .LBB0_1311
	v_mul_f32_e32 v25, 0x3d372713, v16
	v_mul_f32_e32 v25, v16, v25
	v_mul_f32_e32 v26, 0x3d372713, v21
	v_fma_f32 v25, v16, v25, v16
	v_mul_f32_e32 v26, v21, v26
	v_mul_f32_e32 v25, 0xbfcc422a, v25
	v_fma_f32 v26, v21, v26, v21
	v_mul_f32_e32 v25, 0x3fb8aa3b, v25
	v_mul_f32_e32 v26, 0xbfcc422a, v26
	v_exp_f32_e32 v25, v25
	v_mul_f32_e32 v26, 0x3fb8aa3b, v26
	v_mul_f32_e32 v30, 0x3d372713, v23
	v_exp_f32_e32 v27, v26
	v_mul_f32_e32 v30, v23, v30
	v_fma_f32 v30, v23, v30, v23
	v_mul_f32_e32 v30, 0xbfcc422a, v30
	v_add_f32_e32 v25, 1.0, v25
	v_mul_f32_e32 v29, 0x3d372713, v18
	v_mul_f32_e32 v30, 0x3fb8aa3b, v30
	v_mul_f32_e32 v24, 0x3d372713, v20
	v_rcp_f32_e32 v26, v25
	v_add_f32_e32 v25, 1.0, v27
	v_mul_f32_e32 v27, 0x3d372713, v17
	v_mul_f32_e32 v28, 0x3d372713, v22
	v_mul_f32_e32 v29, v18, v29
	v_exp_f32_e32 v31, v30
	v_mul_f32_e32 v30, 0x3d372713, v19
	v_mul_f32_e32 v24, v20, v24
	v_mul_f32_e32 v27, v17, v27
	v_mul_f32_e32 v28, v22, v28
	v_fma_f32 v29, v18, v29, v18
	v_mul_f32_e32 v30, v19, v30
	v_fma_f32 v24, v20, v24, v20
	v_fma_f32 v27, v17, v27, v17
	v_fma_f32 v28, v22, v28, v22
	v_mul_f32_e32 v29, 0xbfcc422a, v29
	v_fma_f32 v30, v19, v30, v19
	v_mul_f32_e32 v24, 0xbfcc422a, v24
	v_mul_f32_e32 v27, 0xbfcc422a, v27
	v_mul_f32_e32 v28, 0xbfcc422a, v28
	v_mul_f32_e32 v29, 0x3fb8aa3b, v29
	v_mul_f32_e32 v30, 0xbfcc422a, v30
	v_mul_f32_e32 v24, 0x3fb8aa3b, v24
	v_mul_f32_e32 v27, 0x3fb8aa3b, v27
	v_mul_f32_e32 v28, 0x3fb8aa3b, v28
	v_exp_f32_e32 v29, v29
	v_mul_f32_e32 v30, 0x3fb8aa3b, v30
	v_exp_f32_e32 v24, v24
	v_exp_f32_e32 v27, v27
	v_exp_f32_e32 v28, v28
	v_exp_f32_e32 v34, v30
	v_add_f32_e32 v29, 1.0, v29
	v_add_f32_e32 v24, 1.0, v24
	v_add_f32_e32 v27, 1.0, v27
	v_add_f32_e32 v28, 1.0, v28
	v_rcp_f32_e32 v30, v29
	v_add_f32_e32 v29, 1.0, v31
	v_add_f32_e32 v31, 1.0, v34
	v_rcp_f32_e32 v24, v24
	v_rcp_f32_e32 v25, v25
	v_rcp_f32_e32 v28, v28
	v_rcp_f32_e32 v29, v29
	v_rcp_f32_e32 v31, v31
	v_rcp_f32_e32 v27, v27
	v_mul_f32_e64 v20, v20, v24
	v_mul_f32_e64 v21, v21, v25
	v_mul_f32_e64 v22, v22, v28
	v_mul_f32_e64 v23, v23, v29
	v_mul_f32_e64 v18, v18, v30
	v_mul_f32_e64 v19, v19, v31
	v_mul_f32_e64 v16, v16, v26
	v_mul_f32_e64 v17, v17, v27
.LBB0_1311:
	v_lshl_add_u64 v[24:25], v[32:33], 0, s[16:17]
	s_and_b64 vcc, exec, s[2:3]
	v_cvt_pk_bf16_f32 v20, v20, v21
	v_cvt_pk_bf16_f32 v21, v22, v23
	v_cvt_pk_bf16_f32 v22, v16, v17
	v_cvt_pk_bf16_f32 v23, v18, v19
	global_store_dwordx4 v[24:25], v[20:23], off offset:256
	s_cbranch_vccnz .LBB0_1313
	v_mul_f32_e32 v17, 0x3d372713, v8
	v_mul_f32_e32 v17, v8, v17
	v_mul_f32_e32 v18, 0x3d372713, v13
	v_fma_f32 v17, v8, v17, v8
	v_mul_f32_e32 v18, v13, v18
	v_mul_f32_e32 v17, 0xbfcc422a, v17
	v_fma_f32 v18, v13, v18, v13
	v_mul_f32_e32 v17, 0x3fb8aa3b, v17
	v_mul_f32_e32 v18, 0xbfcc422a, v18
	v_exp_f32_e32 v17, v17
	v_mul_f32_e32 v18, 0x3fb8aa3b, v18
	v_mul_f32_e32 v22, 0x3d372713, v15
	v_exp_f32_e32 v19, v18
	v_mul_f32_e32 v22, v15, v22
	v_fma_f32 v22, v15, v22, v15
	v_mul_f32_e32 v22, 0xbfcc422a, v22
	v_add_f32_e32 v17, 1.0, v17
	v_mul_f32_e32 v21, 0x3d372713, v10
	v_mul_f32_e32 v22, 0x3fb8aa3b, v22
	v_mul_f32_e32 v16, 0x3d372713, v12
	v_rcp_f32_e32 v18, v17
	v_add_f32_e32 v17, 1.0, v19
	v_mul_f32_e32 v19, 0x3d372713, v9
	v_mul_f32_e32 v20, 0x3d372713, v14
	v_mul_f32_e32 v21, v10, v21
	v_exp_f32_e32 v23, v22
	v_mul_f32_e32 v22, 0x3d372713, v11
	v_mul_f32_e32 v16, v12, v16
	v_mul_f32_e32 v19, v9, v19
	v_mul_f32_e32 v20, v14, v20
	v_fma_f32 v21, v10, v21, v10
	v_mul_f32_e32 v22, v11, v22
	v_fma_f32 v16, v12, v16, v12
	v_fma_f32 v19, v9, v19, v9
	v_fma_f32 v20, v14, v20, v14
	v_mul_f32_e32 v21, 0xbfcc422a, v21
	v_fma_f32 v22, v11, v22, v11
	v_mul_f32_e32 v16, 0xbfcc422a, v16
	v_mul_f32_e32 v19, 0xbfcc422a, v19
	v_mul_f32_e32 v20, 0xbfcc422a, v20
	v_mul_f32_e32 v21, 0x3fb8aa3b, v21
	v_mul_f32_e32 v22, 0xbfcc422a, v22
	v_mul_f32_e32 v16, 0x3fb8aa3b, v16
	v_mul_f32_e32 v19, 0x3fb8aa3b, v19
	v_mul_f32_e32 v20, 0x3fb8aa3b, v20
	v_exp_f32_e32 v21, v21
	v_mul_f32_e32 v22, 0x3fb8aa3b, v22
	v_exp_f32_e32 v16, v16
	v_exp_f32_e32 v19, v19
	v_exp_f32_e32 v20, v20
	v_exp_f32_e32 v24, v22
	v_add_f32_e32 v21, 1.0, v21
	v_add_f32_e32 v16, 1.0, v16
	v_add_f32_e32 v19, 1.0, v19
	v_add_f32_e32 v20, 1.0, v20
	v_rcp_f32_e32 v22, v21
	v_add_f32_e32 v21, 1.0, v23
	v_add_f32_e32 v23, 1.0, v24
	v_rcp_f32_e32 v16, v16
	v_rcp_f32_e32 v17, v17
	v_rcp_f32_e32 v20, v20
	v_rcp_f32_e32 v21, v21
	v_rcp_f32_e32 v23, v23
	v_rcp_f32_e32 v19, v19
	v_mul_f32_e64 v12, v12, v16
	v_mul_f32_e64 v13, v13, v17
	v_mul_f32_e64 v14, v14, v20
	v_mul_f32_e64 v15, v15, v21
	v_mul_f32_e64 v10, v10, v22
	v_mul_f32_e64 v11, v11, v23
	v_mul_f32_e64 v8, v8, v18
	v_mul_f32_e64 v9, v9, v19
.LBB0_1313:
	v_lshlrev_b64 v[16:17], 11, v[134:135]
	v_lshl_add_u64 v[16:17], v[136:137], 0, v[16:17]
	v_cvt_pk_bf16_f32 v12, v12, v13
	v_cvt_pk_bf16_f32 v13, v14, v15
	v_cvt_pk_bf16_f32 v14, v8, v9
	v_add_co_u32_e32 v8, vcc, 0x58000, v16
	v_cvt_pk_bf16_f32 v15, v10, v11
	s_nop 1
	v_addc_co_u32_e32 v9, vcc, 0, v17, vcc
	s_and_b64 vcc, exec, s[2:3]
	global_store_dwordx4 v[8:9], v[12:15], off
	s_cbranch_vccnz .LBB0_1315
	v_mul_f32_e32 v9, 0x3d372713, v0
	v_mul_f32_e32 v9, v0, v9
	v_mul_f32_e32 v10, 0x3d372713, v5
	v_fma_f32 v9, v0, v9, v0
	v_mul_f32_e32 v10, v5, v10
	v_mul_f32_e32 v9, 0xbfcc422a, v9
	v_fma_f32 v10, v5, v10, v5
	v_mul_f32_e32 v9, 0x3fb8aa3b, v9
	v_mul_f32_e32 v10, 0xbfcc422a, v10
	v_exp_f32_e32 v9, v9
	v_mul_f32_e32 v10, 0x3fb8aa3b, v10
	v_mul_f32_e32 v14, 0x3d372713, v7
	v_exp_f32_e32 v11, v10
	v_mul_f32_e32 v14, v7, v14
	v_fma_f32 v14, v7, v14, v7
	v_mul_f32_e32 v14, 0xbfcc422a, v14
	v_add_f32_e32 v9, 1.0, v9
	v_mul_f32_e32 v13, 0x3d372713, v2
	v_mul_f32_e32 v14, 0x3fb8aa3b, v14
	v_mul_f32_e32 v8, 0x3d372713, v4
	v_rcp_f32_e32 v10, v9
	v_add_f32_e32 v9, 1.0, v11
	v_mul_f32_e32 v11, 0x3d372713, v1
	v_mul_f32_e32 v12, 0x3d372713, v6
	v_mul_f32_e32 v13, v2, v13
	v_exp_f32_e32 v15, v14
	v_mul_f32_e32 v14, 0x3d372713, v3
	v_mul_f32_e32 v8, v4, v8
	v_mul_f32_e32 v11, v1, v11
	v_mul_f32_e32 v12, v6, v12
	v_fma_f32 v13, v2, v13, v2
	v_mul_f32_e32 v14, v3, v14
	v_fma_f32 v8, v4, v8, v4
	v_fma_f32 v11, v1, v11, v1
	v_fma_f32 v12, v6, v12, v6
	v_mul_f32_e32 v13, 0xbfcc422a, v13
	v_fma_f32 v14, v3, v14, v3
	v_mul_f32_e32 v8, 0xbfcc422a, v8
	v_mul_f32_e32 v11, 0xbfcc422a, v11
	v_mul_f32_e32 v12, 0xbfcc422a, v12
	v_mul_f32_e32 v13, 0x3fb8aa3b, v13
	v_mul_f32_e32 v14, 0xbfcc422a, v14
	v_mul_f32_e32 v8, 0x3fb8aa3b, v8
	v_mul_f32_e32 v11, 0x3fb8aa3b, v11
	v_mul_f32_e32 v12, 0x3fb8aa3b, v12
	v_exp_f32_e32 v13, v13
	v_mul_f32_e32 v14, 0x3fb8aa3b, v14
	v_exp_f32_e32 v8, v8
	v_exp_f32_e32 v11, v11
	v_exp_f32_e32 v12, v12
	v_exp_f32_e32 v18, v14
	v_add_f32_e32 v13, 1.0, v13
	v_add_f32_e32 v8, 1.0, v8
	v_add_f32_e32 v11, 1.0, v11
	v_add_f32_e32 v12, 1.0, v12
	v_rcp_f32_e32 v14, v13
	v_add_f32_e32 v13, 1.0, v15
	v_add_f32_e32 v15, 1.0, v18
	v_rcp_f32_e32 v8, v8
	v_rcp_f32_e32 v9, v9
	v_rcp_f32_e32 v12, v12
	v_rcp_f32_e32 v13, v13
	v_rcp_f32_e32 v15, v15
	v_rcp_f32_e32 v11, v11
	v_mul_f32_e64 v4, v4, v8
	v_mul_f32_e64 v5, v5, v9
	v_mul_f32_e64 v6, v6, v12
	v_mul_f32_e64 v7, v7, v13
	v_mul_f32_e64 v2, v2, v14
	v_mul_f32_e64 v3, v3, v15
	v_mul_f32_e64 v0, v0, v10
	v_mul_f32_e64 v1, v1, v11

.LBB0_1581:
	s_lshl_b32 s28, s65, 8
	v_lshrrev_b32_e32 v41, 1, v40
	s_add_i32 s28, s28, s51
	v_and_b32_e32 v41, 24, v41
	v_lshl_or_b32 v41, s64, 8, v41
	v_and_or_b32 v150, v40, 15, s28
	v_or_b32_e32 v42, s52, v41
	s_lshl_b64 s[26:27], s[26:27], 2
	v_ashrrev_i32_e32 v151, 31, v150
	s_add_u32 s26, s4, s26
	v_ashrrev_i32_e32 v43, 31, v42
	v_lshlrev_b64 v[40:41], 11, v[150:151]
	v_lshl_add_u64 v[40:41], s[10:11], 0, v[40:41]
	v_lshlrev_b64 v[152:153], 1, v[42:43]
	s_addc_u32 s27, s5, s27
	v_lshl_add_u64 v[148:149], v[40:41], 0, v[152:153]
	v_lshl_add_u64 v[40:41], v[42:43], 2, s[26:27]
	v_add_co_u32_e32 v42, vcc, s58, v40
	global_load_dwordx4 v[162:165], v[148:149], off
	s_nop 0
	v_addc_co_u32_e32 v43, vcc, 0, v41, vcc
	global_load_dwordx4 v[52:55], v[42:43], off
	v_lshl_add_u64 v[40:41], v[40:41], 0, s[14:15]
	global_load_dwordx4 v[48:51], v[40:41], off offset:16
	global_load_dwordx4 v[44:47], v[40:41], off offset:512
	s_nop 0
	global_load_dwordx4 v[40:43], v[40:41], off offset:528
	s_waitcnt vmcnt(0)
	v_lshlrev_b32_e32 v166, 16, v162
	v_and_b32_e32 v167, 0xffff0000, v162
	v_lshlrev_b32_e32 v162, 16, v163
	v_and_b32_e32 v163, 0xffff0000, v163
	v_lshlrev_b32_e32 v168, 16, v164
	v_and_b32_e32 v169, 0xffff0000, v164
	v_lshlrev_b32_e32 v164, 16, v165
	v_and_b32_e32 v165, 0xffff0000, v165
	v_fma_f32 v142, v142, v54, v162
	v_fma_f32 v143, v143, v55, v163
	v_fma_f32 v140, v140, v52, v166
	v_fma_f32 v141, v141, v53, v167
	v_fma_f32 v162, v138, v50, v164
	v_fma_f32 v163, v139, v51, v165
	v_fma_f32 v138, v136, v48, v168
	v_fma_f32 v139, v137, v49, v169
	v_cvt_pk_bf16_f32 v136, v140, v141
	v_cvt_pk_bf16_f32 v137, v142, v143
	s_nop 0
	v_cvt_pk_bf16_f32 v138, v138, v139
	v_cvt_pk_bf16_f32 v139, v162, v163
	global_load_dwordx4 v[140:143], v[148:149], off offset:256
	v_or_b32_e32 v162, 16, v150
	v_ashrrev_i32_e32 v163, 31, v162
	global_store_dwordx4 v[148:149], v[136:139], off
	v_lshlrev_b64 v[162:163], 11, v[162:163]
	v_lshl_add_u64 v[162:163], s[10:11], 0, v[162:163]
	v_lshl_add_u64 v[162:163], v[162:163], 0, v[152:153]
	s_waitcnt vmcnt(1)
	v_lshlrev_b32_e32 v136, 16, v140
	v_and_b32_e32 v137, 0xffff0000, v140
	v_lshlrev_b32_e32 v138, 16, v141
	v_and_b32_e32 v139, 0xffff0000, v141
	v_lshlrev_b32_e32 v140, 16, v142
	v_and_b32_e32 v141, 0xffff0000, v142
	v_lshlrev_b32_e32 v142, 16, v143
	v_and_b32_e32 v143, 0xffff0000, v143
	v_fma_f32 v130, v130, v46, v138
	v_fma_f32 v131, v131, v47, v139
	v_fma_f32 v128, v128, v44, v136
	v_fma_f32 v129, v129, v45, v137
	v_fma_f32 v134, v134, v42, v142
	v_fma_f32 v135, v135, v43, v143
	v_fma_f32 v132, v132, v40, v140
	v_fma_f32 v133, v133, v41, v141
	v_cvt_pk_bf16_f32 v128, v128, v129
	v_cvt_pk_bf16_f32 v129, v130, v131
	s_nop 0
	v_cvt_pk_bf16_f32 v130, v132, v133
	v_cvt_pk_bf16_f32 v131, v134, v135
	global_store_dwordx4 v[148:149], v[128:131], off offset:256
	global_load_dwordx4 v[128:131], v[162:163], off
	s_waitcnt vmcnt(0)
	v_lshlrev_b32_e32 v132, 16, v128
	v_and_b32_e32 v133, 0xffff0000, v128
	v_lshlrev_b32_e32 v128, 16, v129
	v_and_b32_e32 v129, 0xffff0000, v129
	v_lshlrev_b32_e32 v134, 16, v130
	v_and_b32_e32 v135, 0xffff0000, v130
	v_lshlrev_b32_e32 v130, 16, v131
	v_and_b32_e32 v131, 0xffff0000, v131
	v_fma_f32 v126, v126, v54, v128
	v_fma_f32 v127, v127, v55, v129
	v_fma_f32 v124, v124, v52, v132
	v_fma_f32 v125, v125, v53, v133
	v_fma_f32 v128, v122, v50, v130
	v_fma_f32 v129, v123, v51, v131
	v_fma_f32 v122, v120, v48, v134
	v_fma_f32 v123, v121, v49, v135
	v_cvt_pk_bf16_f32 v120, v124, v125
	v_cvt_pk_bf16_f32 v121, v126, v127
	s_nop 0
	v_cvt_pk_bf16_f32 v122, v122, v123
	v_cvt_pk_bf16_f32 v123, v128, v129
	global_load_dwordx4 v[124:127], v[162:163], off offset:256
	v_or_b32_e32 v128, 32, v150
	v_ashrrev_i32_e32 v129, 31, v128
	global_store_dwordx4 v[162:163], v[120:123], off
	v_lshlrev_b64 v[128:129], 11, v[128:129]
	v_lshl_add_u64 v[128:129], s[10:11], 0, v[128:129]
	v_lshl_add_u64 v[128:129], v[128:129], 0, v[152:153]
	s_waitcnt vmcnt(1)
	v_lshlrev_b32_e32 v120, 16, v124
	v_and_b32_e32 v121, 0xffff0000, v124
	v_lshlrev_b32_e32 v122, 16, v125
	v_and_b32_e32 v123, 0xffff0000, v125
	v_lshlrev_b32_e32 v124, 16, v126
	v_and_b32_e32 v125, 0xffff0000, v126
	v_lshlrev_b32_e32 v126, 16, v127
	v_and_b32_e32 v127, 0xffff0000, v127
	v_fma_f32 v114, v114, v46, v122
	v_fma_f32 v115, v115, v47, v123
	v_fma_f32 v112, v112, v44, v120
	v_fma_f32 v113, v113, v45, v121
	v_fma_f32 v118, v118, v42, v126
	v_fma_f32 v119, v119, v43, v127
	v_fma_f32 v116, v116, v40, v124
	v_fma_f32 v117, v117, v41, v125
	v_cvt_pk_bf16_f32 v112, v112, v113
	v_cvt_pk_bf16_f32 v113, v114, v115
	s_nop 0
	v_cvt_pk_bf16_f32 v114, v116, v117
	v_cvt_pk_bf16_f32 v115, v118, v119
	global_store_dwordx4 v[162:163], v[112:115], off offset:256
	global_load_dwordx4 v[112:115], v[128:129], off
	s_waitcnt vmcnt(0)
	v_lshlrev_b32_e32 v116, 16, v112
	v_and_b32_e32 v117, 0xffff0000, v112
	v_lshlrev_b32_e32 v112, 16, v113
	v_and_b32_e32 v113, 0xffff0000, v113
	v_lshlrev_b32_e32 v118, 16, v114
	v_and_b32_e32 v119, 0xffff0000, v114
	v_lshlrev_b32_e32 v114, 16, v115
	v_and_b32_e32 v115, 0xffff0000, v115
	v_fma_f32 v110, v110, v54, v112
	v_fma_f32 v111, v111, v55, v113
	v_fma_f32 v108, v108, v52, v116
	v_fma_f32 v109, v109, v53, v117
	v_fma_f32 v112, v106, v50, v114
	v_fma_f32 v113, v107, v51, v115
	v_fma_f32 v106, v104, v48, v118
	v_fma_f32 v107, v105, v49, v119
	v_cvt_pk_bf16_f32 v104, v108, v109
	v_cvt_pk_bf16_f32 v105, v110, v111
	s_nop 0
	v_cvt_pk_bf16_f32 v106, v106, v107
	v_cvt_pk_bf16_f32 v107, v112, v113
	global_load_dwordx4 v[108:111], v[128:129], off offset:256
	v_or_b32_e32 v112, 48, v150
	v_ashrrev_i32_e32 v113, 31, v112
	global_store_dwordx4 v[128:129], v[104:107], off
	v_lshlrev_b64 v[112:113], 11, v[112:113]
	v_lshl_add_u64 v[112:113], s[10:11], 0, v[112:113]
	v_lshl_add_u64 v[112:113], v[112:113], 0, v[152:153]
	s_waitcnt vmcnt(1)
	v_lshlrev_b32_e32 v104, 16, v108
	v_and_b32_e32 v105, 0xffff0000, v108
	v_lshlrev_b32_e32 v106, 16, v109
	v_and_b32_e32 v107, 0xffff0000, v109
	v_lshlrev_b32_e32 v108, 16, v110
	v_and_b32_e32 v109, 0xffff0000, v110
	v_lshlrev_b32_e32 v110, 16, v111
	v_and_b32_e32 v111, 0xffff0000, v111
	v_fma_f32 v98, v98, v46, v106
	v_fma_f32 v99, v99, v47, v107
	v_fma_f32 v96, v96, v44, v104
	v_fma_f32 v97, v97, v45, v105
	v_fma_f32 v102, v102, v42, v110
	v_fma_f32 v103, v103, v43, v111
	v_fma_f32 v100, v100, v40, v108
	v_fma_f32 v101, v101, v41, v109
	v_cvt_pk_bf16_f32 v96, v96, v97
	v_cvt_pk_bf16_f32 v97, v98, v99
	s_nop 0
	v_cvt_pk_bf16_f32 v98, v100, v101
	v_cvt_pk_bf16_f32 v99, v102, v103
	global_store_dwordx4 v[128:129], v[96:99], off offset:256
	global_load_dwordx4 v[96:99], v[112:113], off
	s_waitcnt vmcnt(0)
	v_lshlrev_b32_e32 v100, 16, v96
	v_and_b32_e32 v101, 0xffff0000, v96
	v_lshlrev_b32_e32 v96, 16, v97
	v_and_b32_e32 v97, 0xffff0000, v97
	v_lshlrev_b32_e32 v102, 16, v98
	v_and_b32_e32 v103, 0xffff0000, v98
	v_lshlrev_b32_e32 v98, 16, v99
	v_and_b32_e32 v99, 0xffff0000, v99
	v_fma_f32 v94, v94, v54, v96
	v_fma_f32 v95, v95, v55, v97
	v_fma_f32 v92, v92, v52, v100
	v_fma_f32 v93, v93, v53, v101
	v_fma_f32 v96, v90, v50, v98
	v_fma_f32 v97, v91, v51, v99
	v_fma_f32 v90, v88, v48, v102
	v_fma_f32 v91, v89, v49, v103
	v_cvt_pk_bf16_f32 v88, v92, v93
	v_cvt_pk_bf16_f32 v89, v94, v95
	s_nop 0
	v_cvt_pk_bf16_f32 v90, v90, v91
	v_cvt_pk_bf16_f32 v91, v96, v97
	global_load_dwordx4 v[92:95], v[112:113], off offset:256
	v_add_co_u32_e32 v96, vcc, s59, v148
	global_store_dwordx4 v[112:113], v[88:91], off
	s_nop 0
	v_addc_co_u32_e32 v97, vcc, 0, v149, vcc
	s_waitcnt vmcnt(1)
	v_lshlrev_b32_e32 v88, 16, v92
	v_and_b32_e32 v89, 0xffff0000, v92
	v_lshlrev_b32_e32 v90, 16, v93
	v_and_b32_e32 v91, 0xffff0000, v93
	v_lshlrev_b32_e32 v92, 16, v94
	v_and_b32_e32 v93, 0xffff0000, v94
	v_lshlrev_b32_e32 v94, 16, v95
	v_and_b32_e32 v95, 0xffff0000, v95
	v_fma_f32 v74, v74, v46, v90
	v_fma_f32 v75, v75, v47, v91
	v_fma_f32 v72, v72, v44, v88
	v_fma_f32 v73, v73, v45, v89
	v_fma_f32 v78, v78, v42, v94
	v_fma_f32 v79, v79, v43, v95
	v_fma_f32 v76, v76, v40, v92
	v_fma_f32 v77, v77, v41, v93
	v_cvt_pk_bf16_f32 v72, v72, v73
	v_cvt_pk_bf16_f32 v73, v74, v75
	v_lshl_add_u64 v[88:89], v[148:149], 0, s[8:9]
	v_cvt_pk_bf16_f32 v74, v76, v77
	v_cvt_pk_bf16_f32 v75, v78, v79
	global_store_dwordx4 v[112:113], v[72:75], off offset:256
	global_load_dwordx4 v[72:75], v[96:97], off
	s_waitcnt vmcnt(0)
	v_lshlrev_b32_e32 v76, 16, v72
	v_and_b32_e32 v77, 0xffff0000, v72
	v_lshlrev_b32_e32 v72, 16, v73
	v_and_b32_e32 v73, 0xffff0000, v73
	v_lshlrev_b32_e32 v78, 16, v74
	v_and_b32_e32 v79, 0xffff0000, v74
	v_lshlrev_b32_e32 v74, 16, v75
	v_and_b32_e32 v75, 0xffff0000, v75
	v_fma_f32 v86, v86, v54, v72
	v_fma_f32 v87, v87, v55, v73
	v_fma_f32 v72, v84, v52, v76
	v_fma_f32 v73, v85, v53, v77
	v_fma_f32 v76, v82, v50, v74
	v_fma_f32 v77, v83, v51, v75
	v_fma_f32 v74, v80, v48, v78
	v_fma_f32 v75, v81, v49, v79
	v_cvt_pk_bf16_f32 v72, v72, v73
	v_cvt_pk_bf16_f32 v73, v86, v87
	v_add_co_u32_e32 v80, vcc, s60, v148
	v_cvt_pk_bf16_f32 v74, v74, v75
	v_cvt_pk_bf16_f32 v75, v76, v77
	global_load_dwordx4 v[76:79], v[88:89], off offset:256
	s_nop 0
	v_addc_co_u32_e32 v81, vcc, 0, v149, vcc
	global_store_dwordx4 v[96:97], v[72:75], off
	s_waitcnt vmcnt(1)
	s_nop 0
	v_lshlrev_b32_e32 v72, 16, v76
	v_and_b32_e32 v73, 0xffff0000, v76
	v_lshlrev_b32_e32 v74, 16, v77
	v_and_b32_e32 v75, 0xffff0000, v77
	v_lshlrev_b32_e32 v76, 16, v78
	v_and_b32_e32 v77, 0xffff0000, v78
	v_lshlrev_b32_e32 v78, 16, v79
	v_and_b32_e32 v79, 0xffff0000, v79
	v_fma_f32 v66, v66, v46, v74
	v_fma_f32 v67, v67, v47, v75
	v_fma_f32 v64, v64, v44, v72
	v_fma_f32 v65, v65, v45, v73
	v_fma_f32 v70, v70, v42, v78
	v_fma_f32 v71, v71, v43, v79
	v_fma_f32 v68, v68, v40, v76
	v_fma_f32 v69, v69, v41, v77
	v_cvt_pk_bf16_f32 v64, v64, v65
	v_cvt_pk_bf16_f32 v65, v66, v67
	s_nop 0
	v_cvt_pk_bf16_f32 v66, v68, v69
	v_cvt_pk_bf16_f32 v67, v70, v71
	global_store_dwordx4 v[88:89], v[64:67], off offset:256
	global_load_dwordx4 v[64:67], v[80:81], off
	v_lshl_add_u64 v[68:69], v[148:149], 0, s[16:17]
	s_waitcnt vmcnt(0)
	v_lshlrev_b32_e32 v70, 16, v64
	v_and_b32_e32 v71, 0xffff0000, v64
	v_lshlrev_b32_e32 v64, 16, v65
	v_and_b32_e32 v65, 0xffff0000, v65
	v_lshlrev_b32_e32 v72, 16, v66
	v_and_b32_e32 v73, 0xffff0000, v66
	v_lshlrev_b32_e32 v66, 16, v67
	v_and_b32_e32 v67, 0xffff0000, v67
	v_fma_f32 v62, v62, v54, v64
	v_fma_f32 v63, v63, v55, v65
	v_fma_f32 v60, v60, v52, v70
	v_fma_f32 v61, v61, v53, v71
	v_fma_f32 v64, v58, v50, v66
	v_fma_f32 v65, v59, v51, v67
	v_fma_f32 v58, v56, v48, v72
	v_fma_f32 v59, v57, v49, v73
	v_cvt_pk_bf16_f32 v56, v60, v61
	v_cvt_pk_bf16_f32 v57, v62, v63
	s_nop 0
	v_cvt_pk_bf16_f32 v58, v58, v59
	v_cvt_pk_bf16_f32 v59, v64, v65
	global_load_dwordx4 v[60:63], v[68:69], off offset:256
	v_add_co_u32_e32 v64, vcc, s61, v148
	global_store_dwordx4 v[80:81], v[56:59], off
	s_nop 0
	v_addc_co_u32_e32 v65, vcc, 0, v149, vcc
	s_waitcnt vmcnt(1)
	v_lshlrev_b32_e32 v56, 16, v60
	v_and_b32_e32 v57, 0xffff0000, v60
	v_lshlrev_b32_e32 v58, 16, v61
	v_and_b32_e32 v59, 0xffff0000, v61
	v_lshlrev_b32_e32 v60, 16, v62
	v_and_b32_e32 v61, 0xffff0000, v62
	v_lshlrev_b32_e32 v62, 16, v63
	v_and_b32_e32 v63, 0xffff0000, v63
	v_fma_f32 v34, v34, v46, v58
	v_fma_f32 v35, v35, v47, v59
	v_fma_f32 v32, v32, v44, v56
	v_fma_f32 v33, v33, v45, v57
	v_fma_f32 v38, v38, v42, v62
	v_fma_f32 v39, v39, v43, v63
	v_fma_f32 v36, v36, v40, v60
	v_fma_f32 v37, v37, v41, v61
	v_cvt_pk_bf16_f32 v32, v32, v33
	v_cvt_pk_bf16_f32 v33, v34, v35
	s_nop 0
	v_cvt_pk_bf16_f32 v34, v36, v37
	v_cvt_pk_bf16_f32 v35, v38, v39
	global_store_dwordx4 v[68:69], v[32:35], off offset:256
	global_load_dwordx4 v[32:35], v[64:65], off
	v_lshl_add_u64 v[36:37], v[148:149], 0, s[18:19]
	s_waitcnt vmcnt(0)
	v_lshlrev_b32_e32 v38, 16, v32
	v_and_b32_e32 v39, 0xffff0000, v32
	v_lshlrev_b32_e32 v32, 16, v33
	v_and_b32_e32 v33, 0xffff0000, v33
	v_lshlrev_b32_e32 v56, 16, v34
	v_and_b32_e32 v57, 0xffff0000, v34
	v_lshlrev_b32_e32 v34, 16, v35
	v_and_b32_e32 v35, 0xffff0000, v35
	v_fma_f32 v30, v30, v54, v32
	v_fma_f32 v31, v31, v55, v33
	v_fma_f32 v28, v28, v52, v38
	v_fma_f32 v29, v29, v53, v39
	v_fma_f32 v32, v26, v50, v34
	v_fma_f32 v33, v27, v51, v35
	v_fma_f32 v26, v24, v48, v56
	v_fma_f32 v27, v25, v49, v57
	v_cvt_pk_bf16_f32 v24, v28, v29
	v_cvt_pk_bf16_f32 v25, v30, v31
	s_nop 0
	v_cvt_pk_bf16_f32 v26, v26, v27
	v_cvt_pk_bf16_f32 v27, v32, v33
	global_load_dwordx4 v[28:31], v[36:37], off offset:256
	v_add_co_u32_e32 v32, vcc, s62, v148
	global_store_dwordx4 v[64:65], v[24:27], off
	s_nop 0
	v_addc_co_u32_e32 v33, vcc, 0, v149, vcc
	s_andn2_b64 vcc, exec, s[0:1]
	s_mov_b64 s[0:1], -1
	s_waitcnt vmcnt(1)
	v_lshlrev_b32_e32 v24, 16, v28
	v_and_b32_e32 v25, 0xffff0000, v28
	v_lshlrev_b32_e32 v26, 16, v29
	v_and_b32_e32 v27, 0xffff0000, v29
	v_lshlrev_b32_e32 v28, 16, v30
	v_and_b32_e32 v29, 0xffff0000, v30
	v_lshlrev_b32_e32 v30, 16, v31
	v_and_b32_e32 v31, 0xffff0000, v31
	v_fma_f32 v18, v18, v46, v26
	v_fma_f32 v19, v19, v47, v27
	v_fma_f32 v16, v16, v44, v24
	v_fma_f32 v17, v17, v45, v25
	v_fma_f32 v22, v22, v42, v30
	v_fma_f32 v23, v23, v43, v31
	v_fma_f32 v20, v20, v40, v28
	v_fma_f32 v21, v21, v41, v29
	v_cvt_pk_bf16_f32 v16, v16, v17
	v_cvt_pk_bf16_f32 v17, v18, v19
	s_nop 0
	v_cvt_pk_bf16_f32 v18, v20, v21
	v_cvt_pk_bf16_f32 v19, v22, v23
	global_store_dwordx4 v[36:37], v[16:19], off offset:256
	global_load_dwordx4 v[16:19], v[32:33], off
	v_lshl_add_u64 v[20:21], v[148:149], 0, s[20:21]
	s_waitcnt vmcnt(0)
	v_lshlrev_b32_e32 v22, 16, v16
	v_and_b32_e32 v23, 0xffff0000, v16
	v_lshlrev_b32_e32 v16, 16, v17
	v_and_b32_e32 v17, 0xffff0000, v17
	v_lshlrev_b32_e32 v24, 16, v18
	v_and_b32_e32 v25, 0xffff0000, v18
	v_lshlrev_b32_e32 v18, 16, v19
	v_and_b32_e32 v19, 0xffff0000, v19
	v_fma_f32 v14, v14, v54, v16
	v_fma_f32 v15, v15, v55, v17
	v_fma_f32 v12, v12, v52, v22
	v_fma_f32 v13, v13, v53, v23
	v_fma_f32 v16, v10, v50, v18
	v_fma_f32 v17, v11, v51, v19
	v_fma_f32 v10, v8, v48, v24
	v_fma_f32 v11, v9, v49, v25
	v_cvt_pk_bf16_f32 v8, v12, v13
	v_cvt_pk_bf16_f32 v9, v14, v15
	s_nop 0
	v_cvt_pk_bf16_f32 v10, v10, v11
	v_cvt_pk_bf16_f32 v11, v16, v17
	global_load_dwordx4 v[12:15], v[20:21], off offset:256
	s_nop 0
	global_store_dwordx4 v[32:33], v[8:11], off
	s_waitcnt vmcnt(1)
	s_nop 0
	v_lshlrev_b32_e32 v8, 16, v12
	v_and_b32_e32 v9, 0xffff0000, v12
	v_lshlrev_b32_e32 v10, 16, v13
	v_and_b32_e32 v11, 0xffff0000, v13
	v_lshlrev_b32_e32 v12, 16, v14
	v_and_b32_e32 v13, 0xffff0000, v14
	v_lshlrev_b32_e32 v14, 16, v15
	v_and_b32_e32 v15, 0xffff0000, v15
	v_fma_f32 v4, v4, v44, v8
	v_fma_f32 v5, v5, v45, v9
	v_fma_f32 v8, v2, v42, v14
	v_fma_f32 v9, v3, v43, v15
	v_fma_f32 v2, v0, v40, v12
	v_fma_f32 v3, v1, v41, v13
	v_fma_f32 v6, v6, v46, v10
	v_fma_f32 v7, v7, v47, v11
	v_cvt_pk_bf16_f32 v0, v4, v5
	s_nop 0
	v_cvt_pk_bf16_f32 v1, v6, v7
	v_cvt_pk_bf16_f32 v2, v2, v3
	v_cvt_pk_bf16_f32 v3, v8, v9
	global_store_dwordx4 v[20:21], v[0:3], off offset:256
	s_cbranch_vccnz .LBB0_1562
	s_andn2_b64 vcc, exec, s[6:7]
	s_cbranch_vccnz .LBB0_1561
	s_barrier
	s_branch .LBB0_1561

.LBB0_2122:
	s_lshl_b32 s20, s58, 8
	s_or_b32 s20, s20, s50
	v_or_b32_e32 v0, s20, v0
	v_lshl_add_u32 v2, v0, 2, 0
	v_add_u32_e32 v10, 0x21000, v2
	ds_read_b128 v[2:5], v10
	ds_read_b128 v[6:9], v10 offset:16
	ds_read_b128 v[20:23], v10 offset:32
	ds_read_b128 v[24:27], v10 offset:48
	v_or_b32_e32 v18, s46, v1
	v_ashrrev_i32_e32 v1, 31, v0
	s_waitcnt lgkmcnt(0)
	v_mul_f32_e64 v12, v6, s8
	v_mul_f32_e64 v13, v7, s8
	v_mul_f32_e64 v16, v2, s8
	v_mul_f32_e64 v17, v3, s8
	v_mul_f32_e64 v14, v4, s8
	v_mul_f32_e64 v15, v5, s8
	v_mul_f32_e64 v10, v8, s8
	v_mul_f32_e64 v11, v9, s8
	v_mul_f32_e64 v8, v20, s8
	v_mul_f32_e64 v9, v21, s8
	v_mul_f32_e64 v6, v22, s8
	v_mul_f32_e64 v7, v23, s8
	v_mul_f32_e64 v4, v24, s8
	v_mul_f32_e64 v5, v25, s8
	v_mul_f32_e64 v2, v26, s8
	v_mul_f32_e64 v3, v27, s8
	v_cmp_gt_i32_e32 vcc, s56, v18
	s_and_saveexec_b64 s[20:21], vcc
	s_cbranch_execz .LBB0_2124
	v_fma_f32 v20, v148, s10, v16
	v_fma_f32 v21, v149, s10, v17
	v_fma_f32 v22, v150, s10, v14
	v_fma_f32 v23, v151, s10, v15
	v_med3_f32 v19, v20, s54, v170
	v_med3_f32 v21, v21, s54, v170
	v_mov_b32_e32 v20, 0
	v_cvt_pk_fp8_f32 v20, v19, v21
	v_med3_f32 v19, v22, s54, v170
	v_med3_f32 v21, v23, s54, v170
	v_fma_f32 v22, v144, s10, v12
	v_fma_f32 v23, v145, s10, v13
	v_cvt_pk_fp8_f32 v20, v19, v21 op_sel:[0,0,1]
	v_med3_f32 v19, v22, s54, v170
	v_med3_f32 v22, v23, s54, v170
	v_mov_b32_e32 v21, 0
	v_cvt_pk_fp8_f32 v21, v19, v22
	v_fma_f32 v22, v146, s10, v10
	v_fma_f32 v23, v147, s10, v11
	v_fma_f32 v24, v158, s10, v6
	v_fma_f32 v25, v159, s10, v7
	v_med3_f32 v19, v22, s54, v170
	v_med3_f32 v22, v23, s54, v170
	v_cvt_pk_fp8_f32 v21, v19, v22 op_sel:[0,0,1]
	v_fma_f32 v22, v156, s10, v8
	v_fma_f32 v23, v157, s10, v9
	s_nop 0
	v_med3_f32 v19, v22, s54, v170
	v_med3_f32 v23, v23, s54, v170
	v_mov_b32_e32 v22, 0
	v_cvt_pk_fp8_f32 v22, v19, v23
	v_med3_f32 v19, v24, s54, v170
	v_med3_f32 v23, v25, s54, v170
	v_fma_f32 v24, v152, s10, v4
	v_fma_f32 v25, v153, s10, v5
	v_cvt_pk_fp8_f32 v22, v19, v23 op_sel:[0,0,1]
	v_med3_f32 v19, v24, s54, v170
	v_med3_f32 v24, v25, s54, v170
	v_mov_b32_e32 v23, 0
	v_cvt_pk_fp8_f32 v23, v19, v24
	v_fma_f32 v24, v154, s10, v2
	v_fma_f32 v25, v155, s10, v3
	s_nop 0
	v_med3_f32 v19, v24, s54, v170
	v_med3_f32 v24, v25, s54, v170
	v_cvt_pk_fp8_f32 v23, v19, v24 op_sel:[0,0,1]
	v_add_u32_e32 v24, s55, v18
	v_ashrrev_i32_e32 v25, 31, v24
	v_lshlrev_b64 v[24:25], 10, v[24:25]
	v_lshl_add_u64 v[24:25], s[4:5], 0, v[24:25]
	v_lshl_add_u64 v[24:25], v[24:25], 0, v[0:1]
	global_store_dwordx4 v[24:25], v[20:23], off
.LBB0_2124:
	s_or_b64 exec, exec, s[20:21]
	v_or_b32_e32 v19, 16, v18
	v_cmp_gt_i32_e32 vcc, s56, v19
	s_and_saveexec_b64 s[20:21], vcc
	s_cbranch_execz .LBB0_2126
	v_fma_f32 v20, v136, s10, v16
	v_fma_f32 v21, v137, s10, v17
	s_nop 0
	v_med3_f32 v22, v20, s54, v170
	v_med3_f32 v21, v21, s54, v170
	v_mov_b32_e32 v20, 0
	v_cvt_pk_fp8_f32 v20, v22, v21
	v_fma_f32 v22, v138, s10, v14
	v_fma_f32 v23, v139, s10, v15
	s_nop 0
	v_med3_f32 v21, v22, s54, v170
	v_med3_f32 v22, v23, s54, v170
	v_cvt_pk_fp8_f32 v20, v21, v22 op_sel:[0,0,1]
	v_fma_f32 v22, v128, s10, v12
	v_fma_f32 v23, v129, s10, v13
	v_mov_b32_e32 v21, 0
	v_med3_f32 v22, v22, s54, v170
	v_med3_f32 v23, v23, s54, v170
	v_cvt_pk_fp8_f32 v21, v22, v23
	v_fma_f32 v22, v130, s10, v10
	v_fma_f32 v23, v131, s10, v11
	s_nop 0
	v_med3_f32 v22, v22, s54, v170
	v_med3_f32 v23, v23, s54, v170
	v_cvt_pk_fp8_f32 v21, v22, v23 op_sel:[0,0,1]
	v_fma_f32 v22, v140, s10, v8
	v_fma_f32 v23, v141, s10, v9
	s_nop 0
	v_med3_f32 v24, v22, s54, v170
	v_med3_f32 v23, v23, s54, v170
	v_mov_b32_e32 v22, 0
	v_cvt_pk_fp8_f32 v22, v24, v23
	v_fma_f32 v24, v142, s10, v6
	v_fma_f32 v25, v143, s10, v7
	s_nop 0
	v_med3_f32 v23, v24, s54, v170
	v_med3_f32 v24, v25, s54, v170
	v_cvt_pk_fp8_f32 v22, v23, v24 op_sel:[0,0,1]
	v_fma_f32 v24, v132, s10, v4
	v_fma_f32 v25, v133, s10, v5
	v_mov_b32_e32 v23, 0
	v_med3_f32 v24, v24, s54, v170
	v_med3_f32 v25, v25, s54, v170
	v_cvt_pk_fp8_f32 v23, v24, v25
	v_fma_f32 v24, v134, s10, v2
	v_fma_f32 v25, v135, s10, v3
	s_nop 0
	v_med3_f32 v24, v24, s54, v170
	v_med3_f32 v25, v25, s54, v170
	v_cvt_pk_fp8_f32 v23, v24, v25 op_sel:[0,0,1]
	v_add_u32_e32 v24, s55, v19
	v_ashrrev_i32_e32 v25, 31, v24
	v_lshlrev_b64 v[24:25], 10, v[24:25]
	v_lshl_add_u64 v[24:25], s[4:5], 0, v[24:25]
	v_lshl_add_u64 v[24:25], v[24:25], 0, v[0:1]
	global_store_dwordx4 v[24:25], v[20:23], off
.LBB0_2126:
	s_or_b64 exec, exec, s[20:21]
	v_or_b32_e32 v19, 32, v18
	v_cmp_gt_i32_e32 vcc, s56, v19
	s_and_saveexec_b64 s[20:21], vcc
	s_cbranch_execz .LBB0_2128
	v_fma_f32 v20, v120, s10, v16
	v_fma_f32 v21, v121, s10, v17
	s_nop 0
	v_med3_f32 v22, v20, s54, v170
	v_med3_f32 v21, v21, s54, v170
	v_mov_b32_e32 v20, 0
	v_cvt_pk_fp8_f32 v20, v22, v21
	v_fma_f32 v22, v122, s10, v14
	v_fma_f32 v23, v123, s10, v15
	s_nop 0
	v_med3_f32 v21, v22, s54, v170
	v_med3_f32 v22, v23, s54, v170
	v_cvt_pk_fp8_f32 v20, v21, v22 op_sel:[0,0,1]
	v_fma_f32 v22, v112, s10, v12
	v_fma_f32 v23, v113, s10, v13
	v_mov_b32_e32 v21, 0
	v_med3_f32 v22, v22, s54, v170
	v_med3_f32 v23, v23, s54, v170
	v_cvt_pk_fp8_f32 v21, v22, v23
	v_fma_f32 v22, v114, s10, v10
	v_fma_f32 v23, v115, s10, v11
	s_nop 0
	v_med3_f32 v22, v22, s54, v170
	v_med3_f32 v23, v23, s54, v170
	v_cvt_pk_fp8_f32 v21, v22, v23 op_sel:[0,0,1]
	v_fma_f32 v22, v124, s10, v8
	v_fma_f32 v23, v125, s10, v9
	s_nop 0
	v_med3_f32 v24, v22, s54, v170
	v_med3_f32 v23, v23, s54, v170
	v_mov_b32_e32 v22, 0
	v_cvt_pk_fp8_f32 v22, v24, v23
	v_fma_f32 v24, v126, s10, v6
	v_fma_f32 v25, v127, s10, v7
	s_nop 0
	v_med3_f32 v23, v24, s54, v170
	v_med3_f32 v24, v25, s54, v170
	v_cvt_pk_fp8_f32 v22, v23, v24 op_sel:[0,0,1]
	v_fma_f32 v24, v116, s10, v4
	v_fma_f32 v25, v117, s10, v5
	v_mov_b32_e32 v23, 0
	v_med3_f32 v24, v24, s54, v170
	v_med3_f32 v25, v25, s54, v170
	v_cvt_pk_fp8_f32 v23, v24, v25
	v_fma_f32 v24, v118, s10, v2
	v_fma_f32 v25, v119, s10, v3
	s_nop 0
	v_med3_f32 v24, v24, s54, v170
	v_med3_f32 v25, v25, s54, v170
	v_cvt_pk_fp8_f32 v23, v24, v25 op_sel:[0,0,1]
	v_add_u32_e32 v24, s55, v19
	v_ashrrev_i32_e32 v25, 31, v24
	v_lshlrev_b64 v[24:25], 10, v[24:25]
	v_lshl_add_u64 v[24:25], s[4:5], 0, v[24:25]
	v_lshl_add_u64 v[24:25], v[24:25], 0, v[0:1]
	global_store_dwordx4 v[24:25], v[20:23], off
.LBB0_2128:
	s_or_b64 exec, exec, s[20:21]
	v_or_b32_e32 v19, 48, v18
	v_cmp_gt_i32_e32 vcc, s56, v19
	s_and_saveexec_b64 s[20:21], vcc
	s_cbranch_execz .LBB0_2130
	v_fma_f32 v20, v108, s10, v16
	v_fma_f32 v21, v109, s10, v17
	s_nop 0
	v_med3_f32 v22, v20, s54, v170
	v_med3_f32 v21, v21, s54, v170
	v_mov_b32_e32 v20, 0
	v_cvt_pk_fp8_f32 v20, v22, v21
	v_fma_f32 v22, v110, s10, v14
	v_fma_f32 v23, v111, s10, v15
	s_nop 0
	v_med3_f32 v21, v22, s54, v170
	v_med3_f32 v22, v23, s54, v170
	v_cvt_pk_fp8_f32 v20, v21, v22 op_sel:[0,0,1]
	v_fma_f32 v22, v92, s10, v12
	v_fma_f32 v23, v93, s10, v13
	v_mov_b32_e32 v21, 0
	v_med3_f32 v22, v22, s54, v170
	v_med3_f32 v23, v23, s54, v170
	v_cvt_pk_fp8_f32 v21, v22, v23
	v_fma_f32 v22, v94, s10, v10
	v_fma_f32 v23, v95, s10, v11
	s_nop 0
	v_med3_f32 v22, v22, s54, v170
	v_med3_f32 v23, v23, s54, v170
	v_cvt_pk_fp8_f32 v21, v22, v23 op_sel:[0,0,1]
	v_fma_f32 v22, v96, s10, v8
	v_fma_f32 v23, v97, s10, v9
	s_nop 0
	v_med3_f32 v24, v22, s54, v170
	v_med3_f32 v23, v23, s54, v170
	v_mov_b32_e32 v22, 0
	v_cvt_pk_fp8_f32 v22, v24, v23
	v_fma_f32 v24, v98, s10, v6
	v_fma_f32 v25, v99, s10, v7
	s_nop 0
	v_med3_f32 v23, v24, s54, v170
	v_med3_f32 v24, v25, s54, v170
	v_cvt_pk_fp8_f32 v22, v23, v24 op_sel:[0,0,1]
	v_fma_f32 v24, v80, s10, v4
	v_fma_f32 v25, v81, s10, v5
	v_mov_b32_e32 v23, 0
	v_med3_f32 v24, v24, s54, v170
	v_med3_f32 v25, v25, s54, v170
	v_cvt_pk_fp8_f32 v23, v24, v25
	v_fma_f32 v24, v82, s10, v2
	v_fma_f32 v25, v83, s10, v3
	s_nop 0
	v_med3_f32 v24, v24, s54, v170
	v_med3_f32 v25, v25, s54, v170
	v_cvt_pk_fp8_f32 v23, v24, v25 op_sel:[0,0,1]
	v_add_u32_e32 v24, s55, v19
	v_ashrrev_i32_e32 v25, 31, v24
	v_lshlrev_b64 v[24:25], 10, v[24:25]
	v_lshl_add_u64 v[24:25], s[4:5], 0, v[24:25]
	v_lshl_add_u64 v[24:25], v[24:25], 0, v[0:1]
	global_store_dwordx4 v[24:25], v[20:23], off
.LBB0_2130:
	s_or_b64 exec, exec, s[20:21]
	v_add_u32_e32 v19, 0x80, v18
	v_cmp_gt_i32_e32 vcc, s56, v19
	s_and_saveexec_b64 s[20:21], vcc
	s_cbranch_execz .LBB0_2132
	v_fma_f32 v20, v100, s10, v16
	v_fma_f32 v21, v101, s10, v17
	s_nop 0
	v_med3_f32 v22, v20, s54, v170
	v_med3_f32 v21, v21, s54, v170
	v_mov_b32_e32 v20, 0
	v_cvt_pk_fp8_f32 v20, v22, v21
	v_fma_f32 v22, v102, s10, v14
	v_fma_f32 v23, v103, s10, v15
	s_nop 0
	v_med3_f32 v21, v22, s54, v170
	v_med3_f32 v22, v23, s54, v170
	v_cvt_pk_fp8_f32 v20, v21, v22 op_sel:[0,0,1]
	v_fma_f32 v22, v84, s10, v12
	v_fma_f32 v23, v85, s10, v13
	v_mov_b32_e32 v21, 0
	v_med3_f32 v22, v22, s54, v170
	v_med3_f32 v23, v23, s54, v170
	v_cvt_pk_fp8_f32 v21, v22, v23
	v_fma_f32 v22, v86, s10, v10
	v_fma_f32 v23, v87, s10, v11
	s_nop 0
	v_med3_f32 v22, v22, s54, v170
	v_med3_f32 v23, v23, s54, v170
	v_cvt_pk_fp8_f32 v21, v22, v23 op_sel:[0,0,1]
	v_fma_f32 v22, v104, s10, v8
	v_fma_f32 v23, v105, s10, v9
	s_nop 0
	v_med3_f32 v24, v22, s54, v170
	v_med3_f32 v23, v23, s54, v170
	v_mov_b32_e32 v22, 0
	v_cvt_pk_fp8_f32 v22, v24, v23
	v_fma_f32 v24, v106, s10, v6
	v_fma_f32 v25, v107, s10, v7
	s_nop 0
	v_med3_f32 v23, v24, s54, v170
	v_med3_f32 v24, v25, s54, v170
	v_cvt_pk_fp8_f32 v22, v23, v24 op_sel:[0,0,1]
	v_fma_f32 v24, v88, s10, v4
	v_fma_f32 v25, v89, s10, v5
	v_mov_b32_e32 v23, 0
	v_med3_f32 v24, v24, s54, v170
	v_med3_f32 v25, v25, s54, v170
	v_cvt_pk_fp8_f32 v23, v24, v25
	v_fma_f32 v24, v90, s10, v2
	v_fma_f32 v25, v91, s10, v3
	s_nop 0
	v_med3_f32 v24, v24, s54, v170
	v_med3_f32 v25, v25, s54, v170
	v_cvt_pk_fp8_f32 v23, v24, v25 op_sel:[0,0,1]
	v_add_u32_e32 v24, s55, v19
	v_ashrrev_i32_e32 v25, 31, v24
	v_lshlrev_b64 v[24:25], 10, v[24:25]
	v_lshl_add_u64 v[24:25], s[4:5], 0, v[24:25]
	v_lshl_add_u64 v[24:25], v[24:25], 0, v[0:1]
	global_store_dwordx4 v[24:25], v[20:23], off
.LBB0_2132:
	s_or_b64 exec, exec, s[20:21]
	v_add_u32_e32 v19, 0x90, v18
	v_cmp_gt_i32_e32 vcc, s56, v19
	s_and_saveexec_b64 s[20:21], vcc
	s_cbranch_execz .LBB0_2134
	v_fma_f32 v20, v76, s10, v16
	v_fma_f32 v21, v77, s10, v17
	s_nop 0
	v_med3_f32 v22, v20, s54, v170
	v_med3_f32 v21, v21, s54, v170
	v_mov_b32_e32 v20, 0
	v_cvt_pk_fp8_f32 v20, v22, v21
	v_fma_f32 v22, v78, s10, v14
	v_fma_f32 v23, v79, s10, v15
	s_nop 0
	v_med3_f32 v21, v22, s54, v170
	v_med3_f32 v22, v23, s54, v170
	v_cvt_pk_fp8_f32 v20, v21, v22 op_sel:[0,0,1]
	v_fma_f32 v22, v68, s10, v12
	v_fma_f32 v23, v69, s10, v13
	v_mov_b32_e32 v21, 0
	v_med3_f32 v22, v22, s54, v170
	v_med3_f32 v23, v23, s54, v170
	v_cvt_pk_fp8_f32 v21, v22, v23
	v_fma_f32 v22, v70, s10, v10
	v_fma_f32 v23, v71, s10, v11
	s_nop 0
	v_med3_f32 v22, v22, s54, v170
	v_med3_f32 v23, v23, s54, v170
	v_cvt_pk_fp8_f32 v21, v22, v23 op_sel:[0,0,1]
	v_fma_f32 v22, v72, s10, v8
	v_fma_f32 v23, v73, s10, v9
	s_nop 0
	v_med3_f32 v24, v22, s54, v170
	v_med3_f32 v23, v23, s54, v170
	v_mov_b32_e32 v22, 0
	v_cvt_pk_fp8_f32 v22, v24, v23
	v_fma_f32 v24, v74, s10, v6
	v_fma_f32 v25, v75, s10, v7
	s_nop 0
	v_med3_f32 v23, v24, s54, v170
	v_med3_f32 v24, v25, s54, v170
	v_cvt_pk_fp8_f32 v22, v23, v24 op_sel:[0,0,1]
	v_fma_f32 v24, v64, s10, v4
	v_fma_f32 v25, v65, s10, v5
	v_mov_b32_e32 v23, 0
	v_med3_f32 v24, v24, s54, v170
	v_med3_f32 v25, v25, s54, v170
	v_cvt_pk_fp8_f32 v23, v24, v25
	v_fma_f32 v24, v66, s10, v2
	v_fma_f32 v25, v67, s10, v3
	s_nop 0
	v_med3_f32 v24, v24, s54, v170
	v_med3_f32 v25, v25, s54, v170
	v_cvt_pk_fp8_f32 v23, v24, v25 op_sel:[0,0,1]
	v_add_u32_e32 v24, s55, v19
	v_ashrrev_i32_e32 v25, 31, v24
	v_lshlrev_b64 v[24:25], 10, v[24:25]
	v_lshl_add_u64 v[24:25], s[4:5], 0, v[24:25]
	v_lshl_add_u64 v[24:25], v[24:25], 0, v[0:1]
	global_store_dwordx4 v[24:25], v[20:23], off
.LBB0_2134:
	s_or_b64 exec, exec, s[20:21]
	v_add_u32_e32 v19, 0xa0, v18
	v_cmp_gt_i32_e32 vcc, s56, v19
	s_and_saveexec_b64 s[20:21], vcc
	s_cbranch_execz .LBB0_2136
	v_fma_f32 v20, v60, s10, v16
	v_fma_f32 v21, v61, s10, v17
	s_nop 0
	v_med3_f32 v22, v20, s54, v170
	v_med3_f32 v21, v21, s54, v170
	v_mov_b32_e32 v20, 0
	v_cvt_pk_fp8_f32 v20, v22, v21
	v_fma_f32 v22, v62, s10, v14
	v_fma_f32 v23, v63, s10, v15
	s_nop 0
	v_med3_f32 v21, v22, s54, v170
	v_med3_f32 v22, v23, s54, v170
	v_cvt_pk_fp8_f32 v20, v21, v22 op_sel:[0,0,1]
	v_fma_f32 v22, v52, s10, v12
	v_fma_f32 v23, v53, s10, v13
	v_mov_b32_e32 v21, 0
	v_med3_f32 v22, v22, s54, v170
	v_med3_f32 v23, v23, s54, v170
	v_cvt_pk_fp8_f32 v21, v22, v23
	v_fma_f32 v22, v54, s10, v10
	v_fma_f32 v23, v55, s10, v11
	s_nop 0
	v_med3_f32 v22, v22, s54, v170
	v_med3_f32 v23, v23, s54, v170
	v_cvt_pk_fp8_f32 v21, v22, v23 op_sel:[0,0,1]
	v_fma_f32 v22, v56, s10, v8
	v_fma_f32 v23, v57, s10, v9
	s_nop 0
	v_med3_f32 v24, v22, s54, v170
	v_med3_f32 v23, v23, s54, v170
	v_mov_b32_e32 v22, 0
	v_cvt_pk_fp8_f32 v22, v24, v23
	v_fma_f32 v24, v58, s10, v6
	v_fma_f32 v25, v59, s10, v7
	s_nop 0
	v_med3_f32 v23, v24, s54, v170
	v_med3_f32 v24, v25, s54, v170
	v_cvt_pk_fp8_f32 v22, v23, v24 op_sel:[0,0,1]
	v_fma_f32 v24, v48, s10, v4
	v_fma_f32 v25, v49, s10, v5
	v_mov_b32_e32 v23, 0
	v_med3_f32 v24, v24, s54, v170
	v_med3_f32 v25, v25, s54, v170
	v_cvt_pk_fp8_f32 v23, v24, v25
	v_fma_f32 v24, v50, s10, v2
	v_fma_f32 v25, v51, s10, v3
	s_nop 0
	v_med3_f32 v24, v24, s54, v170
	v_med3_f32 v25, v25, s54, v170
	v_cvt_pk_fp8_f32 v23, v24, v25 op_sel:[0,0,1]
	v_add_u32_e32 v24, s55, v19
	v_ashrrev_i32_e32 v25, 31, v24
	v_lshlrev_b64 v[24:25], 10, v[24:25]
	v_lshl_add_u64 v[24:25], s[4:5], 0, v[24:25]
	v_lshl_add_u64 v[24:25], v[24:25], 0, v[0:1]
	global_store_dwordx4 v[24:25], v[20:23], off
.LBB0_2136:
	s_or_b64 exec, exec, s[20:21]
	v_add_u32_e32 v18, 0xb0, v18
	v_cmp_gt_i32_e32 vcc, s56, v18
	s_and_saveexec_b64 s[20:21], vcc
	s_cbranch_execz .LBB0_2138
	v_fma_f32 v4, v32, s10, v4
	v_fma_f32 v5, v33, s10, v5
	v_fma_f32 v16, v44, s10, v16
	v_fma_f32 v17, v45, s10, v17
	v_fma_f32 v12, v40, s10, v12
	v_fma_f32 v13, v41, s10, v13
	v_fma_f32 v8, v36, s10, v8
	v_fma_f32 v9, v37, s10, v9
	v_med3_f32 v4, v4, s54, v170
	v_med3_f32 v5, v5, s54, v170
	v_mov_b32_e32 v23, 0
	v_med3_f32 v16, v16, s54, v170
	v_med3_f32 v17, v17, s54, v170
	v_mov_b32_e32 v20, 0
	v_med3_f32 v12, v12, s54, v170
	v_med3_f32 v13, v13, s54, v170
	v_mov_b32_e32 v21, 0
	v_med3_f32 v8, v8, s54, v170
	v_med3_f32 v9, v9, s54, v170
	v_mov_b32_e32 v22, 0
	v_cvt_pk_fp8_f32 v23, v4, v5
	v_cvt_pk_fp8_f32 v20, v16, v17
	v_cvt_pk_fp8_f32 v21, v12, v13
	v_cvt_pk_fp8_f32 v22, v8, v9
	v_fma_f32 v2, v34, s10, v2
	v_fma_f32 v3, v35, s10, v3
	v_fma_f32 v14, v46, s10, v14
	v_fma_f32 v15, v47, s10, v15
	v_fma_f32 v10, v42, s10, v10
	v_fma_f32 v11, v43, s10, v11
	v_fma_f32 v6, v38, s10, v6
	v_fma_f32 v7, v39, s10, v7
	v_med3_f32 v2, v2, s54, v170
	v_med3_f32 v3, v3, s54, v170
	v_med3_f32 v14, v14, s54, v170
	v_med3_f32 v15, v15, s54, v170
	v_med3_f32 v10, v10, s54, v170
	v_med3_f32 v11, v11, s54, v170
	v_med3_f32 v6, v6, s54, v170
	v_med3_f32 v7, v7, s54, v170
	v_cvt_pk_fp8_f32 v23, v2, v3 op_sel:[0,0,1]
	v_add_u32_e32 v2, s55, v18
	v_cvt_pk_fp8_f32 v20, v14, v15 op_sel:[0,0,1]
	v_cvt_pk_fp8_f32 v21, v10, v11 op_sel:[0,0,1]
	v_cvt_pk_fp8_f32 v22, v6, v7 op_sel:[0,0,1]
	v_ashrrev_i32_e32 v3, 31, v2
	v_lshlrev_b64 v[2:3], 10, v[2:3]
	v_lshl_add_u64 v[2:3], s[4:5], 0, v[2:3]
	v_lshl_add_u64 v[0:1], v[2:3], 0, v[0:1]
	global_store_dwordx4 v[0:1], v[20:23], off
